# GU epilogue arithmetic rewritten (6 VALU per element, bitwise same), DOWN epilogue sel_g loads batched, 64-bit accumulator zero-init, deferred wconv claims, saddr DMA, code warm loads
# speedup vs baseline: 1.0253x; 1.0253x over previous
.LBB0_24:
	s_mul_hi_i32 s0, s53, 0x2aaaaaab
	s_lshr_b32 s1, s0, 31
	s_ashr_i32 s0, s0, 3
	s_add_i32 s54, s0, s1
	v_lshl_or_b32 v0, s53, 7, v42
	s_mul_i32 s0, s54, 0x1800
	v_subrev_u32_e32 v0, s0, v0
	v_ashrrev_i32_e32 v1, 31, v0
	v_lshlrev_b64 v[0:1], 2, v[0:1]
	v_mad_i64_i32 v[0:1], s[0:1], s54, v46, v[0:1]
	v_lshl_add_u64 v[40:41], v[38:39], 0, v[0:1]
	v_mov_b32_e32 v0, 0
	s_mov_b64 s[8:9], 0
	v_mov_b32_e32 v48, v45
	v_mov_b32_e32 v49, v44
	v_mov_b32_e32 v1, 0
	v_mov_b64_e32 v[2:3], 0
	v_mov_b64_e32 v[4:5], 0
	v_mov_b64_e32 v[6:7], 0
	v_mov_b64_e32 v[8:9], 0
	v_mov_b64_e32 v[10:11], 0
	v_mov_b64_e32 v[12:13], 0
	v_mov_b64_e32 v[14:15], 0
	v_mov_b64_e32 v[16:17], 0
	v_mov_b64_e32 v[18:19], 0
	v_mov_b64_e32 v[20:21], 0
	v_mov_b64_e32 v[22:23], 0
	v_mov_b64_e32 v[24:25], 0
	v_mov_b64_e32 v[26:27], 0
	v_mov_b64_e32 v[28:29], 0
	v_mov_b64_e32 v[30:31], 0
	v_mov_b64_e32 v[32:33], 0
	v_mov_b64_e32 v[34:35], 0
	s_branch .LBB0_32

.LBB0_232:
	s_ashr_i32 s23, s22, 31
	s_lshl_b64 s[24:25], s[22:23], 19
	s_add_u32 s24, s40, s24
	s_addc_u32 s25, s41, s25
	s_ashr_i32 s21, s20, 31
	s_lshl_b64 s[26:27], s[20:21], 19
	s_add_u32 s26, s38, s26
	s_addc_u32 s27, s39, s27
	s_and_b64 s[28:29], s[6:7], exec
	v_mov_b32_e32 v0, 0
	s_cselect_b32 s21, s27, s17
	s_cselect_b32 s23, s26, s16
	s_mov_b32 s61, -2
	s_mov_b64 s[28:29], 0
	v_mov_b32_e32 v1, 0
	v_mov_b64_e32 v[2:3], 0
	v_mov_b64_e32 v[4:5], 0
	v_mov_b64_e32 v[6:7], 0
	v_mov_b64_e32 v[8:9], 0
	v_mov_b64_e32 v[10:11], 0
	v_mov_b64_e32 v[12:13], 0
	v_mov_b64_e32 v[14:15], 0
	v_mov_b64_e32 v[16:17], 0
	v_mov_b64_e32 v[18:19], 0
	v_mov_b64_e32 v[20:21], 0
	v_mov_b64_e32 v[22:23], 0
	v_mov_b64_e32 v[24:25], 0
	v_mov_b64_e32 v[26:27], 0
	v_mov_b64_e32 v[28:29], 0
	v_mov_b64_e32 v[30:31], 0
	v_mov_b64_e32 v[32:33], 0
	v_mov_b64_e32 v[34:35], 0
	v_mov_b64_e32 v[36:37], 0
	v_mov_b64_e32 v[38:39], 0
	v_mov_b64_e32 v[40:41], 0
	v_mov_b64_e32 v[42:43], 0
	v_mov_b64_e32 v[44:45], 0
	v_mov_b64_e32 v[46:47], 0
	v_mov_b64_e32 v[48:49], 0
	v_mov_b64_e32 v[50:51], 0
	v_mov_b64_e32 v[52:53], 0
	v_mov_b64_e32 v[54:55], 0
	v_mov_b64_e32 v[56:57], 0
	v_mov_b64_e32 v[58:59], 0
	v_mov_b64_e32 v[60:61], 0
	v_mov_b64_e32 v[62:63], 0
	v_mov_b64_e32 v[64:65], 0
	v_mov_b64_e32 v[66:67], 0
	v_mov_b64_e32 v[68:69], 0
	v_mov_b64_e32 v[70:71], 0
	v_mov_b64_e32 v[72:73], 0
	v_mov_b64_e32 v[74:75], 0
	v_mov_b64_e32 v[76:77], 0
	v_mov_b64_e32 v[78:79], 0
	v_mov_b64_e32 v[80:81], 0
	v_mov_b64_e32 v[82:83], 0
	v_mov_b64_e32 v[84:85], 0
	v_mov_b64_e32 v[86:87], 0
	v_mov_b64_e32 v[88:89], 0
	v_mov_b64_e32 v[90:91], 0
	v_mov_b64_e32 v[92:93], 0
	v_mov_b64_e32 v[94:95], 0
	v_mov_b64_e32 v[96:97], 0
	v_mov_b64_e32 v[98:99], 0
	v_mov_b64_e32 v[100:101], 0
	v_mov_b64_e32 v[102:103], 0
	v_mov_b64_e32 v[104:105], 0
	v_mov_b64_e32 v[106:107], 0
	v_mov_b64_e32 v[108:109], 0
	v_mov_b64_e32 v[110:111], 0
	v_mov_b64_e32 v[112:113], 0
	v_mov_b64_e32 v[114:115], 0
	v_mov_b64_e32 v[116:117], 0
	v_mov_b64_e32 v[118:119], 0
	v_mov_b64_e32 v[120:121], 0
	v_mov_b64_e32 v[122:123], 0
	v_mov_b64_e32 v[124:125], 0
	v_mov_b64_e32 v[126:127], 0

.LBB0_557:
	s_ashr_i32 s27, s26, 31
	s_lshl_b64 s[28:29], s[26:27], 19
	s_add_u32 s28, s49, s28
	s_addc_u32 s29, s50, s29
	s_ashr_i32 s25, s24, 31
	s_lshl_b64 s[30:31], s[24:25], 19
	s_add_u32 s30, s47, s30
	s_addc_u32 s31, s48, s31
	s_and_b64 s[38:39], s[8:9], exec
	v_mov_b32_e32 v0, 0
	s_cselect_b32 s1, s31, s35
	s_cselect_b32 s3, s30, s34
	s_mov_b32 s20, -2
	s_mov_b64 s[38:39], 0
	s_waitcnt lgkmcnt(0)
	v_mov_b32_e32 v1, v0
	v_mov_b32_e32 v2, v0
	v_mov_b32_e32 v3, v0
	v_mov_b32_e32 v4, v0
	v_mov_b32_e32 v5, v0
	v_mov_b32_e32 v6, v0
	v_mov_b32_e32 v7, v0
	v_mov_b32_e32 v16, v0
	v_mov_b32_e32 v17, v0
	v_mov_b32_e32 v18, v0
	v_mov_b32_e32 v19, v0
	v_mov_b32_e32 v20, v0
	v_mov_b32_e32 v21, v0
	v_mov_b32_e32 v22, v0
	v_mov_b32_e32 v23, v0
	v_mov_b32_e32 v32, v0
	v_mov_b32_e32 v33, v0
	v_mov_b32_e32 v34, v0
	v_mov_b32_e32 v35, v0
	v_mov_b32_e32 v36, v0
	v_mov_b32_e32 v37, v0
	v_mov_b32_e32 v38, v0
	v_mov_b32_e32 v39, v0
	v_mov_b32_e32 v48, v0
	v_mov_b32_e32 v49, v0
	v_mov_b32_e32 v50, v0
	v_mov_b32_e32 v51, v0
	s_waitcnt vmcnt(0)
	v_mov_b64_e32 v[8:9], 0
	v_mov_b64_e32 v[10:11], 0
	v_mov_b64_e32 v[12:13], 0
	v_mov_b64_e32 v[14:15], 0
	v_mov_b64_e32 v[24:25], 0
	v_mov_b64_e32 v[26:27], 0
	v_mov_b64_e32 v[28:29], 0
	v_mov_b64_e32 v[30:31], 0
	v_mov_b64_e32 v[40:41], 0
	v_mov_b64_e32 v[42:43], 0
	v_mov_b64_e32 v[44:45], 0
	v_mov_b64_e32 v[46:47], 0
	v_mov_b64_e32 v[52:53], 0
	v_mov_b64_e32 v[54:55], 0
	v_mov_b64_e32 v[56:57], 0
	v_mov_b64_e32 v[58:59], 0
	v_mov_b64_e32 v[60:61], 0
	v_mov_b64_e32 v[62:63], 0
	v_mov_b64_e32 v[64:65], 0
	v_mov_b64_e32 v[66:67], 0
	v_mov_b64_e32 v[68:69], 0
	v_mov_b64_e32 v[70:71], 0
	v_mov_b64_e32 v[72:73], 0
	v_mov_b64_e32 v[74:75], 0
	v_mov_b64_e32 v[76:77], 0
	v_mov_b64_e32 v[78:79], 0
	v_mov_b64_e32 v[80:81], 0
	v_mov_b64_e32 v[82:83], 0
	v_mov_b64_e32 v[84:85], 0
	v_mov_b64_e32 v[86:87], 0
	v_mov_b64_e32 v[96:97], 0
	v_mov_b64_e32 v[98:99], 0
	v_mov_b64_e32 v[100:101], 0
	v_mov_b64_e32 v[102:103], 0
	v_mov_b64_e32 v[112:113], 0
	v_mov_b64_e32 v[114:115], 0
	v_mov_b64_e32 v[116:117], 0
	v_mov_b64_e32 v[118:119], 0
	v_mov_b64_e32 v[120:121], 0
	v_mov_b64_e32 v[122:123], 0
	v_mov_b64_e32 v[124:125], 0
	v_mov_b64_e32 v[126:127], 0
	v_mov_b64_e32 v[128:129], 0
	v_mov_b64_e32 v[130:131], 0
	v_mov_b64_e32 v[132:133], 0
	v_mov_b64_e32 v[134:135], 0
	v_mov_b64_e32 v[136:137], 0
	v_mov_b64_e32 v[138:139], 0
	v_mov_b64_e32 v[140:141], 0
	v_mov_b64_e32 v[142:143], 0

.LBB0_994:
	v_mov_b32_e32 v0, v209
	s_nop 15
	s_nop 15
	s_mov_b32 s101, 0x44800000
	s_ashr_i32 s2, s0, 31
	v_ashrrev_i32_e32 v1, 2, v0
	v_and_b32_e32 v1, 0xffffffc0, v1
	v_lshl_add_u32 v1, s33, 8, v1
	v_and_or_b32 v4, v0, 15, v1
	v_lshrrev_b32_e32 v2, 1, v0
	s_lshr_b32 s2, s2, 29
	s_add_i32 s2, s0, s2
	s_and_b32 s2, s2, 0x1fffff8
	s_sub_i32 s0, s0, s2
	v_and_b32_e32 v2, 0x78, v2
	v_ashrrev_i32_e32 v5, 31, v4
	v_lshl_or_b32 v2, s0, 7, v2
	v_lshlrev_b64 v[0:1], 10, v[4:5]
	v_ashrrev_i32_e32 v3, 31, v2
	v_lshl_add_u64 v[0:1], s[14:15], 0, v[0:1]
	v_lshl_add_u64 v[0:1], v[0:1], 0, v[2:3]
	v_mul_f32_e32 v10, 0xbd38aa3b, v188
	v_mul_f32_e32 v11, 0xbd38aa3b, v189
	v_mul_f32_e32 v12, 0xbd38aa3b, v190
	v_mul_f32_e32 v13, 0xbd38aa3b, v191
	v_mul_f32_e32 v14, 0xbd38aa3b, v180
	v_mul_f32_e32 v15, 0xbd38aa3b, v181
	v_mul_f32_e32 v16, 0xbd38aa3b, v182
	v_mul_f32_e32 v17, 0xbd38aa3b, v183
	v_exp_f32_e32 v10, v10
	v_exp_f32_e32 v11, v11
	v_exp_f32_e32 v12, v12
	v_exp_f32_e32 v13, v13
	v_exp_f32_e32 v14, v14
	v_exp_f32_e32 v15, v15
	v_exp_f32_e32 v16, v16
	v_exp_f32_e32 v17, v17
	v_fma_f32 v10, v10, s101, s101
	v_fma_f32 v11, v11, s101, s101
	v_fma_f32 v12, v12, s101, s101
	v_fma_f32 v13, v13, s101, s101
	v_fma_f32 v14, v14, s101, s101
	v_fma_f32 v15, v15, s101, s101
	v_fma_f32 v16, v16, s101, s101
	v_fma_f32 v17, v17, s101, s101
	v_rcp_f32_e32 v10, v10
	v_rcp_f32_e32 v11, v11
	v_rcp_f32_e32 v12, v12
	v_rcp_f32_e32 v13, v13
	v_rcp_f32_e32 v14, v14
	v_rcp_f32_e32 v15, v15
	v_rcp_f32_e32 v16, v16
	v_rcp_f32_e32 v17, v17
	v_mul_f32_e32 v10, v188, v10
	v_mul_f32_e32 v11, v189, v11
	v_mul_f32_e32 v12, v190, v12
	v_mul_f32_e32 v13, v191, v13
	v_mul_f32_e32 v14, v180, v14
	v_mul_f32_e32 v15, v181, v15
	v_mul_f32_e32 v16, v182, v16
	v_mul_f32_e32 v17, v183, v17
	v_mul_f32_e32 v10, v10, v184
	v_mul_f32_e32 v11, v11, v185
	v_mul_f32_e32 v12, v12, v186
	v_mul_f32_e32 v13, v13, v187
	v_mul_f32_e32 v14, v14, v176
	v_mul_f32_e32 v15, v15, v177
	v_mul_f32_e32 v16, v16, v178
	v_mul_f32_e32 v17, v17, v179
	v_cvt_pk_fp8_f32 v18, v10, v11
	v_cvt_pk_fp8_f32 v19, v14, v15
	v_cvt_pk_fp8_f32 v18, v12, v13 op_sel:[0,0,1]
	v_cvt_pk_fp8_f32 v19, v16, v17 op_sel:[0,0,1]
	s_nop 0
	global_store_dwordx2 v[0:1], v[18:19], off
	v_or_b32_e32 v8, 16, v4
	v_ashrrev_i32_e32 v9, 31, v8
	v_lshlrev_b64 v[8:9], 10, v[8:9]
	v_lshl_add_u64 v[8:9], s[14:15], 0, v[8:9]
	v_lshl_add_u64 v[8:9], v[8:9], 0, v[2:3]
	v_mul_f32_e32 v10, 0xbd38aa3b, v172
	v_mul_f32_e32 v11, 0xbd38aa3b, v173
	v_mul_f32_e32 v12, 0xbd38aa3b, v174
	v_mul_f32_e32 v13, 0xbd38aa3b, v175
	v_mul_f32_e32 v14, 0xbd38aa3b, v164
	v_mul_f32_e32 v15, 0xbd38aa3b, v165
	v_mul_f32_e32 v16, 0xbd38aa3b, v166
	v_mul_f32_e32 v17, 0xbd38aa3b, v167
	v_exp_f32_e32 v10, v10
	v_exp_f32_e32 v11, v11
	v_exp_f32_e32 v12, v12
	v_exp_f32_e32 v13, v13
	v_exp_f32_e32 v14, v14
	v_exp_f32_e32 v15, v15
	v_exp_f32_e32 v16, v16
	v_exp_f32_e32 v17, v17
	v_fma_f32 v10, v10, s101, s101
	v_fma_f32 v11, v11, s101, s101
	v_fma_f32 v12, v12, s101, s101
	v_fma_f32 v13, v13, s101, s101
	v_fma_f32 v14, v14, s101, s101
	v_fma_f32 v15, v15, s101, s101
	v_fma_f32 v16, v16, s101, s101
	v_fma_f32 v17, v17, s101, s101
	v_rcp_f32_e32 v10, v10
	v_rcp_f32_e32 v11, v11
	v_rcp_f32_e32 v12, v12
	v_rcp_f32_e32 v13, v13
	v_rcp_f32_e32 v14, v14
	v_rcp_f32_e32 v15, v15
	v_rcp_f32_e32 v16, v16
	v_rcp_f32_e32 v17, v17
	v_mul_f32_e32 v10, v172, v10
	v_mul_f32_e32 v11, v173, v11
	v_mul_f32_e32 v12, v174, v12
	v_mul_f32_e32 v13, v175, v13
	v_mul_f32_e32 v14, v164, v14
	v_mul_f32_e32 v15, v165, v15
	v_mul_f32_e32 v16, v166, v16
	v_mul_f32_e32 v17, v167, v17
	v_mul_f32_e32 v10, v10, v168
	v_mul_f32_e32 v11, v11, v169
	v_mul_f32_e32 v12, v12, v170
	v_mul_f32_e32 v13, v13, v171
	v_mul_f32_e32 v14, v14, v160
	v_mul_f32_e32 v15, v15, v161
	v_mul_f32_e32 v16, v16, v162
	v_mul_f32_e32 v17, v17, v163
	v_cvt_pk_fp8_f32 v18, v10, v11
	v_cvt_pk_fp8_f32 v19, v14, v15
	v_cvt_pk_fp8_f32 v18, v12, v13 op_sel:[0,0,1]
	v_cvt_pk_fp8_f32 v19, v16, v17 op_sel:[0,0,1]
	s_nop 0
	global_store_dwordx2 v[8:9], v[18:19], off
	v_or_b32_e32 v8, 32, v4
	v_ashrrev_i32_e32 v9, 31, v8
	v_or_b32_e32 v4, 48, v4
	v_lshlrev_b64 v[6:7], 10, v[8:9]
	v_lshl_add_u64 v[6:7], s[14:15], 0, v[6:7]
	v_lshl_add_u64 v[6:7], v[6:7], 0, v[2:3]
	v_mul_f32_e32 v10, 0xbd38aa3b, v156
	v_mul_f32_e32 v11, 0xbd38aa3b, v157
	v_mul_f32_e32 v12, 0xbd38aa3b, v158
	v_mul_f32_e32 v13, 0xbd38aa3b, v159
	v_mul_f32_e32 v14, 0xbd38aa3b, v148
	v_mul_f32_e32 v15, 0xbd38aa3b, v149
	v_mul_f32_e32 v16, 0xbd38aa3b, v150
	v_mul_f32_e32 v17, 0xbd38aa3b, v151
	v_exp_f32_e32 v10, v10
	v_exp_f32_e32 v11, v11
	v_exp_f32_e32 v12, v12
	v_exp_f32_e32 v13, v13
	v_exp_f32_e32 v14, v14
	v_exp_f32_e32 v15, v15
	v_exp_f32_e32 v16, v16
	v_exp_f32_e32 v17, v17
	v_fma_f32 v10, v10, s101, s101
	v_fma_f32 v11, v11, s101, s101
	v_fma_f32 v12, v12, s101, s101
	v_fma_f32 v13, v13, s101, s101
	v_fma_f32 v14, v14, s101, s101
	v_fma_f32 v15, v15, s101, s101
	v_fma_f32 v16, v16, s101, s101
	v_fma_f32 v17, v17, s101, s101
	v_rcp_f32_e32 v10, v10
	v_rcp_f32_e32 v11, v11
	v_rcp_f32_e32 v12, v12
	v_rcp_f32_e32 v13, v13
	v_rcp_f32_e32 v14, v14
	v_rcp_f32_e32 v15, v15
	v_rcp_f32_e32 v16, v16
	v_rcp_f32_e32 v17, v17
	v_mul_f32_e32 v10, v156, v10
	v_mul_f32_e32 v11, v157, v11
	v_mul_f32_e32 v12, v158, v12
	v_mul_f32_e32 v13, v159, v13
	v_mul_f32_e32 v14, v148, v14
	v_mul_f32_e32 v15, v149, v15
	v_mul_f32_e32 v16, v150, v16
	v_mul_f32_e32 v17, v151, v17
	v_mul_f32_e32 v10, v10, v152
	v_mul_f32_e32 v11, v11, v153
	v_mul_f32_e32 v12, v12, v154
	v_mul_f32_e32 v13, v13, v155
	v_mul_f32_e32 v14, v14, v144
	v_mul_f32_e32 v15, v15, v145
	v_mul_f32_e32 v16, v16, v146
	v_mul_f32_e32 v17, v17, v147
	v_cvt_pk_fp8_f32 v18, v10, v11
	v_cvt_pk_fp8_f32 v19, v14, v15
	v_cvt_pk_fp8_f32 v18, v12, v13 op_sel:[0,0,1]
	v_cvt_pk_fp8_f32 v19, v16, v17 op_sel:[0,0,1]
	s_nop 0
	global_store_dwordx2 v[6:7], v[18:19], off
	v_ashrrev_i32_e32 v5, 31, v4
	v_lshlrev_b64 v[4:5], 10, v[4:5]
	v_lshl_add_u64 v[4:5], s[14:15], 0, v[4:5]
	v_lshl_add_u64 v[2:3], v[4:5], 0, v[2:3]
	s_mov_b32 s33, s52
	v_mul_f32_e32 v10, 0xbd38aa3b, v140
	v_mul_f32_e32 v11, 0xbd38aa3b, v141
	v_mul_f32_e32 v12, 0xbd38aa3b, v142
	v_mul_f32_e32 v13, 0xbd38aa3b, v143
	v_mul_f32_e32 v14, 0xbd38aa3b, v132
	v_mul_f32_e32 v15, 0xbd38aa3b, v133
	v_mul_f32_e32 v16, 0xbd38aa3b, v134
	v_mul_f32_e32 v17, 0xbd38aa3b, v135
	v_exp_f32_e32 v10, v10
	v_exp_f32_e32 v11, v11
	v_exp_f32_e32 v12, v12
	v_exp_f32_e32 v13, v13
	v_exp_f32_e32 v14, v14
	v_exp_f32_e32 v15, v15
	v_exp_f32_e32 v16, v16
	v_exp_f32_e32 v17, v17
	v_fma_f32 v10, v10, s101, s101
	v_fma_f32 v11, v11, s101, s101
	v_fma_f32 v12, v12, s101, s101
	v_fma_f32 v13, v13, s101, s101
	v_fma_f32 v14, v14, s101, s101
	v_fma_f32 v15, v15, s101, s101
	v_fma_f32 v16, v16, s101, s101
	v_fma_f32 v17, v17, s101, s101
	v_rcp_f32_e32 v10, v10
	v_rcp_f32_e32 v11, v11
	v_rcp_f32_e32 v12, v12
	v_rcp_f32_e32 v13, v13
	v_rcp_f32_e32 v14, v14
	v_rcp_f32_e32 v15, v15
	v_rcp_f32_e32 v16, v16
	v_rcp_f32_e32 v17, v17
	v_mul_f32_e32 v10, v140, v10
	v_mul_f32_e32 v11, v141, v11
	v_mul_f32_e32 v12, v142, v12
	v_mul_f32_e32 v13, v143, v13
	v_mul_f32_e32 v14, v132, v14
	v_mul_f32_e32 v15, v133, v15
	v_mul_f32_e32 v16, v134, v16
	v_mul_f32_e32 v17, v135, v17
	v_mul_f32_e32 v10, v10, v136
	v_mul_f32_e32 v11, v11, v137
	v_mul_f32_e32 v12, v12, v138
	v_mul_f32_e32 v13, v13, v139
	v_mul_f32_e32 v14, v14, v128
	v_mul_f32_e32 v15, v15, v129
	v_mul_f32_e32 v16, v16, v130
	v_mul_f32_e32 v17, v17, v131
	v_cvt_pk_fp8_f32 v18, v10, v11
	v_cvt_pk_fp8_f32 v19, v14, v15
	v_cvt_pk_fp8_f32 v18, v12, v13 op_sel:[0,0,1]
	v_cvt_pk_fp8_f32 v19, v16, v17 op_sel:[0,0,1]
	s_nop 0
	global_store_dwordx2 v[2:3], v[18:19], off
	s_mov_b32 s0, s18
	v_add_co_u32_e32 v6, vcc, s49, v0
	v_addc_co_u32_e32 v7, vcc, 0, v1, vcc
	v_mul_f32_e32 v10, 0xbd38aa3b, v124
	v_mul_f32_e32 v11, 0xbd38aa3b, v125
	v_mul_f32_e32 v12, 0xbd38aa3b, v126
	v_mul_f32_e32 v13, 0xbd38aa3b, v127
	v_mul_f32_e32 v14, 0xbd38aa3b, v116
	v_mul_f32_e32 v15, 0xbd38aa3b, v117
	v_mul_f32_e32 v16, 0xbd38aa3b, v118
	v_mul_f32_e32 v17, 0xbd38aa3b, v119
	v_exp_f32_e32 v10, v10
	v_exp_f32_e32 v11, v11
	v_exp_f32_e32 v12, v12
	v_exp_f32_e32 v13, v13
	v_exp_f32_e32 v14, v14
	v_exp_f32_e32 v15, v15
	v_exp_f32_e32 v16, v16
	v_exp_f32_e32 v17, v17
	v_fma_f32 v10, v10, s101, s101
	v_fma_f32 v11, v11, s101, s101
	v_fma_f32 v12, v12, s101, s101
	v_fma_f32 v13, v13, s101, s101
	v_fma_f32 v14, v14, s101, s101
	v_fma_f32 v15, v15, s101, s101
	v_fma_f32 v16, v16, s101, s101
	v_fma_f32 v17, v17, s101, s101
	v_rcp_f32_e32 v10, v10
	v_rcp_f32_e32 v11, v11
	v_rcp_f32_e32 v12, v12
	v_rcp_f32_e32 v13, v13
	v_rcp_f32_e32 v14, v14
	v_rcp_f32_e32 v15, v15
	v_rcp_f32_e32 v16, v16
	v_rcp_f32_e32 v17, v17
	v_mul_f32_e32 v10, v124, v10
	v_mul_f32_e32 v11, v125, v11
	v_mul_f32_e32 v12, v126, v12
	v_mul_f32_e32 v13, v127, v13
	v_mul_f32_e32 v14, v116, v14
	v_mul_f32_e32 v15, v117, v15
	v_mul_f32_e32 v16, v118, v16
	v_mul_f32_e32 v17, v119, v17
	v_mul_f32_e32 v10, v10, v120
	v_mul_f32_e32 v11, v11, v121
	v_mul_f32_e32 v12, v12, v122
	v_mul_f32_e32 v13, v13, v123
	v_mul_f32_e32 v14, v14, v112
	v_mul_f32_e32 v15, v15, v113
	v_mul_f32_e32 v16, v16, v114
	v_mul_f32_e32 v17, v17, v115
	v_cvt_pk_fp8_f32 v18, v10, v11
	v_cvt_pk_fp8_f32 v19, v14, v15
	v_cvt_pk_fp8_f32 v18, v12, v13 op_sel:[0,0,1]
	v_cvt_pk_fp8_f32 v19, v16, v17 op_sel:[0,0,1]
	s_nop 0
	global_store_dwordx2 v[6:7], v[18:19], off
	v_add_co_u32_e32 v6, vcc, s50, v0
	v_addc_co_u32_e32 v7, vcc, 0, v1, vcc
	v_mul_f32_e32 v10, 0xbd38aa3b, v108
	v_mul_f32_e32 v11, 0xbd38aa3b, v109
	v_mul_f32_e32 v12, 0xbd38aa3b, v110
	v_mul_f32_e32 v13, 0xbd38aa3b, v111
	v_mul_f32_e32 v14, 0xbd38aa3b, v100
	v_mul_f32_e32 v15, 0xbd38aa3b, v101
	v_mul_f32_e32 v16, 0xbd38aa3b, v102
	v_mul_f32_e32 v17, 0xbd38aa3b, v103
	v_exp_f32_e32 v10, v10
	v_exp_f32_e32 v11, v11
	v_exp_f32_e32 v12, v12
	v_exp_f32_e32 v13, v13
	v_exp_f32_e32 v14, v14
	v_exp_f32_e32 v15, v15
	v_exp_f32_e32 v16, v16
	v_exp_f32_e32 v17, v17
	v_fma_f32 v10, v10, s101, s101
	v_fma_f32 v11, v11, s101, s101
	v_fma_f32 v12, v12, s101, s101
	v_fma_f32 v13, v13, s101, s101
	v_fma_f32 v14, v14, s101, s101
	v_fma_f32 v15, v15, s101, s101
	v_fma_f32 v16, v16, s101, s101
	v_fma_f32 v17, v17, s101, s101
	v_rcp_f32_e32 v10, v10
	v_rcp_f32_e32 v11, v11
	v_rcp_f32_e32 v12, v12
	v_rcp_f32_e32 v13, v13
	v_rcp_f32_e32 v14, v14
	v_rcp_f32_e32 v15, v15
	v_rcp_f32_e32 v16, v16
	v_rcp_f32_e32 v17, v17
	v_mul_f32_e32 v10, v108, v10
	v_mul_f32_e32 v11, v109, v11
	v_mul_f32_e32 v12, v110, v12
	v_mul_f32_e32 v13, v111, v13
	v_mul_f32_e32 v14, v100, v14
	v_mul_f32_e32 v15, v101, v15
	v_mul_f32_e32 v16, v102, v16
	v_mul_f32_e32 v17, v103, v17
	v_mul_f32_e32 v10, v10, v104
	v_mul_f32_e32 v11, v11, v105
	v_mul_f32_e32 v12, v12, v106
	v_mul_f32_e32 v13, v13, v107
	v_mul_f32_e32 v14, v14, v96
	v_mul_f32_e32 v15, v15, v97
	v_mul_f32_e32 v16, v16, v98
	v_mul_f32_e32 v17, v17, v99
	v_cvt_pk_fp8_f32 v18, v10, v11
	v_cvt_pk_fp8_f32 v19, v14, v15
	v_cvt_pk_fp8_f32 v18, v12, v13 op_sel:[0,0,1]
	v_cvt_pk_fp8_f32 v19, v16, v17 op_sel:[0,0,1]
	s_nop 0
	global_store_dwordx2 v[6:7], v[18:19], off
	v_add_co_u32_e32 v6, vcc, s51, v0
	v_addc_co_u32_e32 v7, vcc, 0, v1, vcc
	v_mul_f32_e32 v10, 0xbd38aa3b, v92
	v_mul_f32_e32 v11, 0xbd38aa3b, v93
	v_mul_f32_e32 v12, 0xbd38aa3b, v94
	v_mul_f32_e32 v13, 0xbd38aa3b, v95
	v_mul_f32_e32 v14, 0xbd38aa3b, v84
	v_mul_f32_e32 v15, 0xbd38aa3b, v85
	v_mul_f32_e32 v16, 0xbd38aa3b, v86
	v_mul_f32_e32 v17, 0xbd38aa3b, v87
	v_exp_f32_e32 v10, v10
	v_exp_f32_e32 v11, v11
	v_exp_f32_e32 v12, v12
	v_exp_f32_e32 v13, v13
	v_exp_f32_e32 v14, v14
	v_exp_f32_e32 v15, v15
	v_exp_f32_e32 v16, v16
	v_exp_f32_e32 v17, v17
	v_fma_f32 v10, v10, s101, s101
	v_fma_f32 v11, v11, s101, s101
	v_fma_f32 v12, v12, s101, s101
	v_fma_f32 v13, v13, s101, s101
	v_fma_f32 v14, v14, s101, s101
	v_fma_f32 v15, v15, s101, s101
	v_fma_f32 v16, v16, s101, s101
	v_fma_f32 v17, v17, s101, s101
	v_rcp_f32_e32 v10, v10
	v_rcp_f32_e32 v11, v11
	v_rcp_f32_e32 v12, v12
	v_rcp_f32_e32 v13, v13
	v_rcp_f32_e32 v14, v14
	v_rcp_f32_e32 v15, v15
	v_rcp_f32_e32 v16, v16
	v_rcp_f32_e32 v17, v17
	v_mul_f32_e32 v10, v92, v10
	v_mul_f32_e32 v11, v93, v11
	v_mul_f32_e32 v12, v94, v12
	v_mul_f32_e32 v13, v95, v13
	v_mul_f32_e32 v14, v84, v14
	v_mul_f32_e32 v15, v85, v15
	v_mul_f32_e32 v16, v86, v16
	v_mul_f32_e32 v17, v87, v17
	v_mul_f32_e32 v10, v10, v88
	v_mul_f32_e32 v11, v11, v89
	v_mul_f32_e32 v12, v12, v90
	v_mul_f32_e32 v13, v13, v91
	v_mul_f32_e32 v14, v14, v80
	v_mul_f32_e32 v15, v15, v81
	v_mul_f32_e32 v16, v16, v82
	v_mul_f32_e32 v17, v17, v83
	v_cvt_pk_fp8_f32 v18, v10, v11
	v_cvt_pk_fp8_f32 v19, v14, v15
	v_cvt_pk_fp8_f32 v18, v12, v13 op_sel:[0,0,1]
	v_cvt_pk_fp8_f32 v19, v16, v17 op_sel:[0,0,1]
	s_nop 0
	global_store_dwordx2 v[6:7], v[18:19], off
	v_add_co_u32_e32 v0, vcc, 0x2c000, v0
	s_mov_b64 s[2:3], s[20:21]
	s_nop 0
	v_addc_co_u32_e32 v1, vcc, 0, v1, vcc
	s_and_b64 vcc, exec, s[6:7]
	v_mul_f32_e32 v10, 0xbd38aa3b, v76
	v_mul_f32_e32 v11, 0xbd38aa3b, v77
	v_mul_f32_e32 v12, 0xbd38aa3b, v78
	v_mul_f32_e32 v13, 0xbd38aa3b, v79
	v_mul_f32_e32 v14, 0xbd38aa3b, v68
	v_mul_f32_e32 v15, 0xbd38aa3b, v69
	v_mul_f32_e32 v16, 0xbd38aa3b, v70
	v_mul_f32_e32 v17, 0xbd38aa3b, v71
	v_exp_f32_e32 v10, v10
	v_exp_f32_e32 v11, v11
	v_exp_f32_e32 v12, v12
	v_exp_f32_e32 v13, v13
	v_exp_f32_e32 v14, v14
	v_exp_f32_e32 v15, v15
	v_exp_f32_e32 v16, v16
	v_exp_f32_e32 v17, v17
	v_fma_f32 v10, v10, s101, s101
	v_fma_f32 v11, v11, s101, s101
	v_fma_f32 v12, v12, s101, s101
	v_fma_f32 v13, v13, s101, s101
	v_fma_f32 v14, v14, s101, s101
	v_fma_f32 v15, v15, s101, s101
	v_fma_f32 v16, v16, s101, s101
	v_fma_f32 v17, v17, s101, s101
	v_rcp_f32_e32 v10, v10
	v_rcp_f32_e32 v11, v11
	v_rcp_f32_e32 v12, v12
	v_rcp_f32_e32 v13, v13
	v_rcp_f32_e32 v14, v14
	v_rcp_f32_e32 v15, v15
	v_rcp_f32_e32 v16, v16
	v_rcp_f32_e32 v17, v17
	v_mul_f32_e32 v10, v76, v10
	v_mul_f32_e32 v11, v77, v11
	v_mul_f32_e32 v12, v78, v12
	v_mul_f32_e32 v13, v79, v13
	v_mul_f32_e32 v14, v68, v14
	v_mul_f32_e32 v15, v69, v15
	v_mul_f32_e32 v16, v70, v16
	v_mul_f32_e32 v17, v71, v17
	v_mul_f32_e32 v10, v10, v72
	v_mul_f32_e32 v11, v11, v73
	v_mul_f32_e32 v12, v12, v74
	v_mul_f32_e32 v13, v13, v75
	v_mul_f32_e32 v14, v14, v64
	v_mul_f32_e32 v15, v15, v65
	v_mul_f32_e32 v16, v16, v66
	v_mul_f32_e32 v17, v17, v67
	v_cvt_pk_fp8_f32 v18, v10, v11
	v_cvt_pk_fp8_f32 v19, v14, v15
	v_cvt_pk_fp8_f32 v18, v12, v13 op_sel:[0,0,1]
	v_cvt_pk_fp8_f32 v19, v16, v17 op_sel:[0,0,1]
	s_nop 0
	global_store_dwordx2 v[0:1], v[18:19], off
	s_cbranch_vccnz .LBB0_1001

.LBB0_997:
	s_ashr_i32 s19, s18, 31
	s_lshl_b64 s[4:5], s[18:19], 18
	s_add_u32 s20, s28, s4
	s_addc_u32 s21, s29, s5
	s_and_b64 s[4:5], s[8:9], exec
	s_cselect_b32 s19, s21, s3
	s_cselect_b32 s53, s20, s2
	s_lshl_b32 s4, s41, 10
	s_add_i32 s4, s4, 0
	s_add_i32 s4, s4, 0x20010
	v_mov_b32_e32 v64, 0
	v_add3_u32 v233, s4, v213, v214
	v_add3_u32 v234, s4, v215, v216
	s_mov_b32 s54, -2
	s_mov_b64 s[4:5], 0xdbff000
	v_mov_b32_e32 v65, 0
	v_mov_b64_e32 v[66:67], 0
	v_mov_b64_e32 v[68:69], 0
	v_mov_b64_e32 v[70:71], 0
	v_mov_b64_e32 v[72:73], 0
	v_mov_b64_e32 v[74:75], 0
	v_mov_b64_e32 v[76:77], 0
	v_mov_b64_e32 v[78:79], 0
	v_mov_b64_e32 v[80:81], 0
	v_mov_b64_e32 v[82:83], 0
	v_mov_b64_e32 v[84:85], 0
	v_mov_b64_e32 v[86:87], 0
	v_mov_b64_e32 v[88:89], 0
	v_mov_b64_e32 v[90:91], 0
	v_mov_b64_e32 v[92:93], 0
	v_mov_b64_e32 v[94:95], 0
	v_mov_b64_e32 v[96:97], 0
	v_mov_b64_e32 v[98:99], 0
	v_mov_b64_e32 v[100:101], 0
	v_mov_b64_e32 v[102:103], 0
	v_mov_b64_e32 v[104:105], 0
	v_mov_b64_e32 v[106:107], 0
	v_mov_b64_e32 v[108:109], 0
	v_mov_b64_e32 v[110:111], 0
	v_mov_b64_e32 v[112:113], 0
	v_mov_b64_e32 v[114:115], 0
	v_mov_b64_e32 v[116:117], 0
	v_mov_b64_e32 v[118:119], 0
	v_mov_b64_e32 v[120:121], 0
	v_mov_b64_e32 v[122:123], 0
	v_mov_b64_e32 v[124:125], 0
	v_mov_b64_e32 v[126:127], 0
	v_mov_b64_e32 v[128:129], 0
	v_mov_b64_e32 v[130:131], 0
	v_mov_b64_e32 v[132:133], 0
	v_mov_b64_e32 v[134:135], 0
	v_mov_b64_e32 v[136:137], 0
	v_mov_b64_e32 v[138:139], 0
	v_mov_b64_e32 v[140:141], 0
	v_mov_b64_e32 v[142:143], 0
	v_mov_b64_e32 v[144:145], 0
	v_mov_b64_e32 v[146:147], 0
	v_mov_b64_e32 v[148:149], 0
	v_mov_b64_e32 v[150:151], 0
	v_mov_b64_e32 v[152:153], 0
	v_mov_b64_e32 v[154:155], 0
	v_mov_b64_e32 v[156:157], 0
	v_mov_b64_e32 v[158:159], 0
	v_mov_b64_e32 v[160:161], 0
	v_mov_b64_e32 v[162:163], 0
	v_mov_b64_e32 v[164:165], 0
	v_mov_b64_e32 v[166:167], 0
	v_mov_b64_e32 v[168:169], 0
	v_mov_b64_e32 v[170:171], 0
	v_mov_b64_e32 v[172:173], 0
	v_mov_b64_e32 v[174:175], 0
	v_mov_b64_e32 v[176:177], 0
	v_mov_b64_e32 v[178:179], 0
	v_mov_b64_e32 v[180:181], 0
	v_mov_b64_e32 v[182:183], 0
	v_mov_b64_e32 v[184:185], 0
	v_mov_b64_e32 v[186:187], 0
	v_mov_b64_e32 v[188:189], 0
	v_mov_b64_e32 v[190:191], 0
	s_branch .LBB0_999

.LBB0_1062:
	s_ashr_i32 s17, s16, 31
	s_lshl_b64 s[20:21], s[16:17], 18
	s_add_u32 s20, s39, s20
	s_addc_u32 s21, s40, s21
	s_ashr_i32 s19, s18, 31
	s_lshl_b64 s[22:23], s[18:19], 18
	s_add_u32 s22, s37, s22
	s_addc_u32 s23, s38, s23
	s_and_b64 s[26:27], s[8:9], exec
	v_mov_b32_e32 v32, 0
	s_cselect_b32 s17, s23, s5
	s_cselect_b32 s19, s22, s4
	s_mov_b32 s33, -2
	s_mov_b64 s[30:31], 0
	v_mov_b32_e32 v33, 0
	v_mov_b64_e32 v[34:35], 0
	v_mov_b64_e32 v[36:37], 0
	v_mov_b64_e32 v[38:39], 0
	v_mov_b64_e32 v[40:41], 0
	v_mov_b64_e32 v[42:43], 0
	v_mov_b64_e32 v[44:45], 0
	v_mov_b64_e32 v[46:47], 0
	v_mov_b64_e32 v[48:49], 0
	v_mov_b64_e32 v[50:51], 0
	v_mov_b64_e32 v[52:53], 0
	v_mov_b64_e32 v[54:55], 0
	v_mov_b64_e32 v[56:57], 0
	v_mov_b64_e32 v[58:59], 0
	v_mov_b64_e32 v[60:61], 0
	v_mov_b64_e32 v[62:63], 0
	v_mov_b64_e32 v[64:65], 0
	v_mov_b64_e32 v[66:67], 0
	v_mov_b64_e32 v[68:69], 0
	v_mov_b64_e32 v[70:71], 0
	v_mov_b64_e32 v[72:73], 0
	v_mov_b64_e32 v[74:75], 0
	v_mov_b64_e32 v[76:77], 0
	v_mov_b64_e32 v[78:79], 0
	v_mov_b64_e32 v[80:81], 0
	v_mov_b64_e32 v[82:83], 0
	v_mov_b64_e32 v[84:85], 0
	v_mov_b64_e32 v[86:87], 0
	v_mov_b64_e32 v[88:89], 0
	v_mov_b64_e32 v[90:91], 0
	v_mov_b64_e32 v[92:93], 0
	v_mov_b64_e32 v[94:95], 0
	v_mov_b64_e32 v[96:97], 0
	v_mov_b64_e32 v[98:99], 0
	v_mov_b64_e32 v[100:101], 0
	v_mov_b64_e32 v[102:103], 0
	v_mov_b64_e32 v[104:105], 0
	v_mov_b64_e32 v[106:107], 0
	v_mov_b64_e32 v[108:109], 0
	v_mov_b64_e32 v[110:111], 0
	v_mov_b64_e32 v[112:113], 0
	v_mov_b64_e32 v[114:115], 0
	v_mov_b64_e32 v[116:117], 0
	v_mov_b64_e32 v[118:119], 0
	v_mov_b64_e32 v[120:121], 0
	v_mov_b64_e32 v[122:123], 0
	v_mov_b64_e32 v[124:125], 0
	v_mov_b64_e32 v[126:127], 0
	v_mov_b64_e32 v[128:129], 0
	v_mov_b64_e32 v[130:131], 0
	v_mov_b64_e32 v[132:133], 0
	v_mov_b64_e32 v[134:135], 0
	v_mov_b64_e32 v[136:137], 0
	v_mov_b64_e32 v[138:139], 0
	v_mov_b64_e32 v[140:141], 0
	v_mov_b64_e32 v[142:143], 0
	v_mov_b64_e32 v[144:145], 0
	v_mov_b64_e32 v[146:147], 0
	v_mov_b64_e32 v[148:149], 0
	v_mov_b64_e32 v[150:151], 0
	v_mov_b64_e32 v[152:153], 0
	v_mov_b64_e32 v[154:155], 0
	v_mov_b64_e32 v[156:157], 0
	v_mov_b64_e32 v[158:159], 0
.LBB0_1063:
	s_add_u32 s26, s30, 0x100
	ds_read_b128 v[0:3], v174
	ds_read_b128 v[4:7], v175
	ds_read_b128 v[8:11], v182
	ds_read_b128 v[12:15], v183
	s_addc_u32 s27, s31, 0
	s_and_b32 s60, s26, 0x300
	s_add_u32 s59, s4, s60
	s_addc_u32 s61, s5, 0
	s_cmp_eq_u32 s33, 4
	s_cselect_b64 s[34:35], -1, 0
	s_and_b64 s[28:29], s[34:35], exec
	s_cselect_b32 s29, s17, s61
	s_cselect_b32 s28, s19, s59
	s_cselect_b32 s59, 0, 0
	s_cselect_b32 s60, 0, s60
	s_add_u32 s30, s24, s30
	s_addc_u32 s31, s25, s31
	s_add_u32 s30, s30, 0x20080
	s_addc_u32 s31, s31, 0
	ds_read_b128 v[194:197], v190
	ds_read_b128 v[210:213], v190 offset:2048
	ds_read_b128 v[198:201], v191
	ds_read_b128 v[214:217], v191 offset:2048
	ds_read_b128 v[218:221], v190 offset:4096
	ds_read_b128 v[226:229], v190 offset:6144
	ds_read_b128 v[222:225], v191 offset:4096
	ds_read_b128 v[230:233], v191 offset:6144
	s_add_i32 m0, s1, 0xc000
	s_nop 0
	global_load_lds_dwordx4 v166, s[30:31]
	s_add_i32 m0, s1, 0xe000
	s_nop 0
	global_load_lds_dwordx4 v162, s[30:31]
	s_waitcnt lgkmcnt(8)
	s_barrier
	s_waitcnt lgkmcnt(0)
	s_setprio 1
	s_waitcnt lgkmcnt(0)
	v_mfma_scale_f32_16x16x128_f8f6f4 v[156:159], v[0:7], v[194:201], v[156:159], v173, v173 op_sel_hi:[0,0,0]
	v_mfma_scale_f32_16x16x128_f8f6f4 v[152:155], v[8:15], v[194:201], v[152:155], v173, v173 op_sel_hi:[0,0,0]
	v_mfma_scale_f32_16x16x128_f8f6f4 v[140:143], v[0:7], v[210:217], v[140:143], v173, v173 op_sel_hi:[0,0,0]
	v_mfma_scale_f32_16x16x128_f8f6f4 v[136:139], v[8:15], v[210:217], v[136:139], v173, v173 op_sel_hi:[0,0,0]
	v_mfma_scale_f32_16x16x128_f8f6f4 v[124:127], v[0:7], v[218:225], v[124:127], v173, v173 op_sel_hi:[0,0,0]
	v_mfma_scale_f32_16x16x128_f8f6f4 v[120:123], v[8:15], v[218:225], v[120:123], v173, v173 op_sel_hi:[0,0,0]
	v_mfma_scale_f32_16x16x128_f8f6f4 v[108:111], v[0:7], v[226:233], v[108:111], v173, v173 op_sel_hi:[0,0,0]
	v_mfma_scale_f32_16x16x128_f8f6f4 v[104:107], v[8:15], v[226:233], v[104:107], v173, v173 op_sel_hi:[0,0,0]
	s_setprio 0
	s_barrier
	s_mov_b64 s[30:31], s[28:29]
	s_mov_b32 m0, s3
	ds_read_b128 v[16:19], v176
	ds_read_b128 v[20:23], v177
	ds_read_b128 v[24:27], v184
	ds_read_b128 v[28:31], v185
	s_nop 0
	global_load_lds_dwordx4 v164, s[30:31]
	s_mov_b32 m0, s43
	s_nop 0
	global_load_lds_dwordx4 v160, s[30:31]
	s_barrier
	s_waitcnt lgkmcnt(0)
	s_setprio 1
	s_waitcnt lgkmcnt(0)
	v_mfma_scale_f32_16x16x128_f8f6f4 v[148:151], v[16:23], v[194:201], v[148:151], v173, v173 op_sel_hi:[0,0,0]
	v_mfma_scale_f32_16x16x128_f8f6f4 v[144:147], v[24:31], v[194:201], v[144:147], v173, v173 op_sel_hi:[0,0,0]
	v_mfma_scale_f32_16x16x128_f8f6f4 v[132:135], v[16:23], v[210:217], v[132:135], v173, v173 op_sel_hi:[0,0,0]
	v_mfma_scale_f32_16x16x128_f8f6f4 v[128:131], v[24:31], v[210:217], v[128:131], v173, v173 op_sel_hi:[0,0,0]
	v_mfma_scale_f32_16x16x128_f8f6f4 v[116:119], v[16:23], v[218:225], v[116:119], v173, v173 op_sel_hi:[0,0,0]
	v_mfma_scale_f32_16x16x128_f8f6f4 v[112:115], v[24:31], v[218:225], v[112:115], v173, v173 op_sel_hi:[0,0,0]
	v_mfma_scale_f32_16x16x128_f8f6f4 v[100:103], v[16:23], v[226:233], v[100:103], v173, v173 op_sel_hi:[0,0,0]
	v_mfma_scale_f32_16x16x128_f8f6f4 v[96:99], v[24:31], v[226:233], v[96:99], v173, v173 op_sel_hi:[0,0,0]
	s_setprio 0
	s_and_b64 s[30:31], s[8:9], s[34:35]
	s_and_b64 s[30:31], s[30:31], exec
	s_cselect_b32 s30, s20, s24
	s_cselect_b32 s31, s21, s25
	s_add_u32 s30, s30, s60
	s_addc_u32 s31, s31, s59
	s_mov_b64 s[34:35], s[30:31]
	s_mov_b32 m0, s1
	s_barrier
	ds_read_b128 v[194:197], v190 offset:16384
	ds_read_b128 v[210:213], v190 offset:18432
	ds_read_b128 v[198:201], v191 offset:16384
	ds_read_b128 v[214:217], v191 offset:18432
	ds_read_b128 v[218:221], v190 offset:20480
	ds_read_b128 v[226:229], v190 offset:22528
	ds_read_b128 v[222:225], v191 offset:20480
	ds_read_b128 v[230:233], v191 offset:22528
	s_nop 0
	global_load_lds_dwordx4 v166, s[34:35]
	s_mov_b32 m0, s44
	s_nop 0
	global_load_lds_dwordx4 v162, s[34:35]
	s_barrier
	s_waitcnt lgkmcnt(0)
	s_setprio 1
	s_waitcnt lgkmcnt(0)
	v_mfma_scale_f32_16x16x128_f8f6f4 v[92:95], v[0:7], v[194:201], v[92:95], v173, v173 op_sel_hi:[0,0,0]
	v_mfma_scale_f32_16x16x128_f8f6f4 v[88:91], v[8:15], v[194:201], v[88:91], v173, v173 op_sel_hi:[0,0,0]
	v_mfma_scale_f32_16x16x128_f8f6f4 v[76:79], v[0:7], v[210:217], v[76:79], v173, v173 op_sel_hi:[0,0,0]
	v_mfma_scale_f32_16x16x128_f8f6f4 v[72:75], v[8:15], v[210:217], v[72:75], v173, v173 op_sel_hi:[0,0,0]
	v_mfma_scale_f32_16x16x128_f8f6f4 v[60:63], v[0:7], v[218:225], v[60:63], v173, v173 op_sel_hi:[0,0,0]
	v_mfma_scale_f32_16x16x128_f8f6f4 v[56:59], v[8:15], v[218:225], v[56:59], v173, v173 op_sel_hi:[0,0,0]
	v_mfma_scale_f32_16x16x128_f8f6f4 v[44:47], v[0:7], v[226:233], v[44:47], v173, v173 op_sel_hi:[0,0,0]
	v_mfma_scale_f32_16x16x128_f8f6f4 v[40:43], v[8:15], v[226:233], v[40:43], v173, v173 op_sel_hi:[0,0,0]
	s_setprio 0
	s_barrier
	s_add_u32 s34, s28, 0x20000
	s_addc_u32 s35, s29, 0
	s_mov_b32 m0, s45
	s_nop 0
	global_load_lds_dwordx4 v164, s[34:35]
	s_mov_b32 m0, s46
	s_nop 0
	global_load_lds_dwordx4 v160, s[34:35]
	s_waitcnt vmcnt(6)
	s_barrier
	s_setprio 1
	v_mfma_scale_f32_16x16x128_f8f6f4 v[84:87], v[16:23], v[194:201], v[84:87], v173, v173 op_sel_hi:[0,0,0]
	v_mfma_scale_f32_16x16x128_f8f6f4 v[80:83], v[24:31], v[194:201], v[80:83], v173, v173 op_sel_hi:[0,0,0]
	v_mfma_scale_f32_16x16x128_f8f6f4 v[68:71], v[16:23], v[210:217], v[68:71], v173, v173 op_sel_hi:[0,0,0]
	v_mfma_scale_f32_16x16x128_f8f6f4 v[64:67], v[24:31], v[210:217], v[64:67], v173, v173 op_sel_hi:[0,0,0]
	v_mfma_scale_f32_16x16x128_f8f6f4 v[52:55], v[16:23], v[218:225], v[52:55], v173, v173 op_sel_hi:[0,0,0]
	v_mfma_scale_f32_16x16x128_f8f6f4 v[48:51], v[24:31], v[218:225], v[48:51], v173, v173 op_sel_hi:[0,0,0]
	v_mfma_scale_f32_16x16x128_f8f6f4 v[36:39], v[16:23], v[226:233], v[36:39], v173, v173 op_sel_hi:[0,0,0]
	v_mfma_scale_f32_16x16x128_f8f6f4 v[32:35], v[24:31], v[226:233], v[32:35], v173, v173 op_sel_hi:[0,0,0]
	s_setprio 0
	s_barrier
	ds_read_b128 v[0:3], v178
	ds_read_b128 v[4:7], v179
	ds_read_b128 v[8:11], v186
	ds_read_b128 v[12:15], v187
	s_add_u32 s34, s30, 0x20000
	s_addc_u32 s35, s31, 0
	s_mov_b32 m0, s47
	ds_read_b128 v[16:19], v190 offset:32768
	ds_read_b128 v[24:27], v190 offset:34816
	ds_read_b128 v[20:23], v191 offset:32768
	ds_read_b128 v[28:31], v191 offset:34816
	ds_read_b128 v[194:197], v190 offset:36864
	ds_read_b128 v[210:213], v190 offset:38912
	ds_read_b128 v[198:201], v191 offset:36864
	ds_read_b128 v[214:217], v191 offset:38912
	s_nop 0
	global_load_lds_dwordx4 v166, s[34:35]
	s_mov_b32 m0, s48
	s_nop 0
	global_load_lds_dwordx4 v162, s[34:35]
	s_waitcnt lgkmcnt(8)
	s_barrier
	s_waitcnt lgkmcnt(0)
	s_setprio 1
	s_waitcnt lgkmcnt(0)
	v_mfma_scale_f32_16x16x128_f8f6f4 v[156:159], v[0:7], v[16:23], v[156:159], v173, v173 op_sel_hi:[0,0,0]
	v_mfma_scale_f32_16x16x128_f8f6f4 v[152:155], v[8:15], v[16:23], v[152:155], v173, v173 op_sel_hi:[0,0,0]
	v_mfma_scale_f32_16x16x128_f8f6f4 v[140:143], v[0:7], v[24:31], v[140:143], v173, v173 op_sel_hi:[0,0,0]
	v_mfma_scale_f32_16x16x128_f8f6f4 v[136:139], v[8:15], v[24:31], v[136:139], v173, v173 op_sel_hi:[0,0,0]
	v_mfma_scale_f32_16x16x128_f8f6f4 v[124:127], v[0:7], v[194:201], v[124:127], v173, v173 op_sel_hi:[0,0,0]
	v_mfma_scale_f32_16x16x128_f8f6f4 v[120:123], v[8:15], v[194:201], v[120:123], v173, v173 op_sel_hi:[0,0,0]
	v_mfma_scale_f32_16x16x128_f8f6f4 v[108:111], v[0:7], v[210:217], v[108:111], v173, v173 op_sel_hi:[0,0,0]
	v_mfma_scale_f32_16x16x128_f8f6f4 v[104:107], v[8:15], v[210:217], v[104:107], v173, v173 op_sel_hi:[0,0,0]
	s_setprio 0
	s_barrier
	s_add_u32 s34, s28, 0x80
	s_addc_u32 s35, s29, 0
	s_mov_b32 m0, s50
	ds_read_b128 v[218:221], v180
	ds_read_b128 v[222:225], v181
	ds_read_b128 v[226:229], v188
	ds_read_b128 v[230:233], v189
	s_nop 0
	global_load_lds_dwordx4 v164, s[34:35]
	s_mov_b32 m0, s51
	s_nop 0
	global_load_lds_dwordx4 v160, s[34:35]
	s_barrier
	s_waitcnt lgkmcnt(0)
	s_setprio 1
	s_waitcnt lgkmcnt(0)
	v_mfma_scale_f32_16x16x128_f8f6f4 v[148:151], v[218:225], v[16:23], v[148:151], v173, v173 op_sel_hi:[0,0,0]
	v_mfma_scale_f32_16x16x128_f8f6f4 v[144:147], v[226:233], v[16:23], v[144:147], v173, v173 op_sel_hi:[0,0,0]
	v_mfma_scale_f32_16x16x128_f8f6f4 v[132:135], v[218:225], v[24:31], v[132:135], v173, v173 op_sel_hi:[0,0,0]
	v_mfma_scale_f32_16x16x128_f8f6f4 v[128:131], v[226:233], v[24:31], v[128:131], v173, v173 op_sel_hi:[0,0,0]
	v_mfma_scale_f32_16x16x128_f8f6f4 v[116:119], v[218:225], v[194:201], v[116:119], v173, v173 op_sel_hi:[0,0,0]
	v_mfma_scale_f32_16x16x128_f8f6f4 v[112:115], v[226:233], v[194:201], v[112:115], v173, v173 op_sel_hi:[0,0,0]
	v_mfma_scale_f32_16x16x128_f8f6f4 v[100:103], v[218:225], v[210:217], v[100:103], v173, v173 op_sel_hi:[0,0,0]
	v_mfma_scale_f32_16x16x128_f8f6f4 v[96:99], v[226:233], v[210:217], v[96:99], v173, v173 op_sel_hi:[0,0,0]
	s_setprio 0
	s_add_u32 s30, s30, 0x80
	s_addc_u32 s31, s31, 0
	s_mov_b32 m0, s52
	s_barrier
	ds_read_b128 v[16:19], v190 offset:49152
	ds_read_b128 v[24:27], v190 offset:51200
	ds_read_b128 v[20:23], v191 offset:49152
	ds_read_b128 v[28:31], v191 offset:51200
	ds_read_b128 v[194:197], v190 offset:53248
	ds_read_b128 v[210:213], v190 offset:55296
	ds_read_b128 v[198:201], v191 offset:53248
	ds_read_b128 v[214:217], v191 offset:55296
	s_nop 0
	global_load_lds_dwordx4 v166, s[30:31]
	s_mov_b32 m0, s53
	s_nop 0
	global_load_lds_dwordx4 v162, s[30:31]
	s_barrier
	s_waitcnt lgkmcnt(0)
	s_setprio 1
	s_waitcnt lgkmcnt(0)
	v_mfma_scale_f32_16x16x128_f8f6f4 v[92:95], v[0:7], v[16:23], v[92:95], v173, v173 op_sel_hi:[0,0,0]
	v_mfma_scale_f32_16x16x128_f8f6f4 v[88:91], v[8:15], v[16:23], v[88:91], v173, v173 op_sel_hi:[0,0,0]
	v_mfma_scale_f32_16x16x128_f8f6f4 v[76:79], v[0:7], v[24:31], v[76:79], v173, v173 op_sel_hi:[0,0,0]
	v_mfma_scale_f32_16x16x128_f8f6f4 v[72:75], v[8:15], v[24:31], v[72:75], v173, v173 op_sel_hi:[0,0,0]
	v_mfma_scale_f32_16x16x128_f8f6f4 v[60:63], v[0:7], v[194:201], v[60:63], v173, v173 op_sel_hi:[0,0,0]
	v_mfma_scale_f32_16x16x128_f8f6f4 v[56:59], v[8:15], v[194:201], v[56:59], v173, v173 op_sel_hi:[0,0,0]
	v_mfma_scale_f32_16x16x128_f8f6f4 v[44:47], v[0:7], v[210:217], v[44:47], v173, v173 op_sel_hi:[0,0,0]
	v_mfma_scale_f32_16x16x128_f8f6f4 v[40:43], v[8:15], v[210:217], v[40:43], v173, v173 op_sel_hi:[0,0,0]
	s_setprio 0
	s_barrier
	s_add_u32 s28, s28, 0x20080
	s_addc_u32 s29, s29, 0
	s_mov_b32 m0, s54
	s_nop 0
	global_load_lds_dwordx4 v164, s[28:29]
	s_mov_b32 m0, s55
	s_nop 0
	global_load_lds_dwordx4 v160, s[28:29]
	s_waitcnt vmcnt(6)
	s_barrier
	s_setprio 1
	v_mfma_scale_f32_16x16x128_f8f6f4 v[84:87], v[218:225], v[16:23], v[84:87], v173, v173 op_sel_hi:[0,0,0]
	v_mfma_scale_f32_16x16x128_f8f6f4 v[80:83], v[226:233], v[16:23], v[80:83], v173, v173 op_sel_hi:[0,0,0]
	v_mfma_scale_f32_16x16x128_f8f6f4 v[68:71], v[218:225], v[24:31], v[68:71], v173, v173 op_sel_hi:[0,0,0]
	v_mfma_scale_f32_16x16x128_f8f6f4 v[64:67], v[226:233], v[24:31], v[64:67], v173, v173 op_sel_hi:[0,0,0]
	v_mfma_scale_f32_16x16x128_f8f6f4 v[52:55], v[218:225], v[194:201], v[52:55], v173, v173 op_sel_hi:[0,0,0]
	v_mfma_scale_f32_16x16x128_f8f6f4 v[48:51], v[226:233], v[194:201], v[48:51], v173, v173 op_sel_hi:[0,0,0]
	v_mfma_scale_f32_16x16x128_f8f6f4 v[36:39], v[218:225], v[210:217], v[36:39], v173, v173 op_sel_hi:[0,0,0]
	v_mfma_scale_f32_16x16x128_f8f6f4 v[32:35], v[226:233], v[210:217], v[32:35], v173, v173 op_sel_hi:[0,0,0]
	s_setprio 0
	s_add_i32 s33, s33, 2
	s_cmp_gt_u32 s33, 5
	s_mov_b64 s[30:31], s[26:27]
	s_barrier
	s_cbranch_scc0 .LBB0_1063
	v_mov_b32_e32 v2, v172
	s_nop 15
	s_nop 15
	v_mov_b32_e32 v8, 0
	v_ashrrev_i32_e32 v0, 2, v2
	v_and_b32_e32 v0, 0xffffffc0, v0
	v_lshl_add_u32 v0, s2, 8, v0
	v_and_or_b32 v6, v2, 15, v0
	v_ashrrev_i32_e32 v7, 31, v6
	v_lshl_add_u64 v[0:1], v[6:7], 2, s[10:11]
	global_load_dword v14, v[0:1], off
	global_load_dword v194, v[0:1], off offset:64
	global_load_dword v195, v[0:1], off offset:128
	global_load_dword v196, v[0:1], off offset:192
	global_load_dword v197, v[0:1], off offset:512
	global_load_dword v198, v[0:1], off offset:576
	global_load_dword v199, v[0:1], off offset:640
	global_load_dword v200, v[0:1], off offset:704
	s_ashr_i32 s2, s0, 31
	s_lshr_b32 s2, s2, 30
	s_add_i32 s2, s0, s2
	v_lshrrev_b32_e32 v2, 1, v2
	s_and_b32 s2, s2, 0xfffffc
	v_and_b32_e32 v2, 0x78, v2
	s_sub_i32 s0, s0, s2
	v_lshl_or_b32 v4, s0, 8, v2
	v_lshlrev_b64 v[2:3], 10, v[6:7]
	v_mov_b32_e32 v9, 0
	v_mov_b32_e32 v10, 0
	v_mov_b32_e32 v11, 0
	v_ashrrev_i32_e32 v5, 31, v4
	v_or_b32_e32 v12, 16, v6
	v_lshl_add_u64 v[2:3], s[14:15], 0, v[2:3]
	v_ashrrev_i32_e32 v13, 31, v12
	v_lshl_add_u64 v[2:3], v[2:3], 0, v[4:5]
	s_mov_b32 s0, 0x20000
	s_mov_b64 s[4:5], 0x20000
	s_mov_b64 s[24:25], s[20:21]
	s_mov_b32 s2, s16
	s_waitcnt vmcnt(0)
	v_mul_f32_e32 v7, 0x3d000000, v14
	v_mul_f32_e32 v14, 0x42000000, v7
	v_pk_mul_f32 v[18:19], v[156:157], v[14:15] op_sel_hi:[1,0]
	v_pk_mul_f32 v[22:23], v[152:153], v[14:15] op_sel_hi:[1,0]
	v_pk_mul_f32 v[16:17], v[158:159], v[14:15] op_sel_hi:[1,0]
	v_pk_mul_f32 v[20:21], v[154:155], v[14:15] op_sel_hi:[1,0]
	v_pk_mul_f32 v[24:25], v[150:151], v[14:15] op_sel_hi:[1,0]
	v_pk_mul_f32 v[26:27], v[148:149], v[14:15] op_sel_hi:[1,0]
	v_pk_mul_f32 v[28:29], v[146:147], v[14:15] op_sel_hi:[1,0]
	v_pk_mul_f32 v[14:15], v[144:145], v[14:15] op_sel_hi:[1,0]
	v_med3_f32 v7, v18, s57, v192
	v_med3_f32 v18, v22, s57, v192
	v_med3_f32 v19, v19, s57, v192
	v_med3_f32 v22, v23, s57, v192
	v_med3_f32 v23, v26, s57, v192
	v_med3_f32 v14, v14, s57, v192
	v_med3_f32 v26, v27, s57, v192
	v_med3_f32 v15, v15, s57, v192
	v_cvt_pk_fp8_f32 v8, v7, v19
	v_cvt_pk_fp8_f32 v9, v18, v22
	v_cvt_pk_fp8_f32 v10, v23, v26
	v_cvt_pk_fp8_f32 v11, v14, v15
	v_med3_f32 v16, v16, s57, v192
	v_med3_f32 v20, v20, s57, v192
	v_med3_f32 v17, v17, s57, v192
	v_med3_f32 v21, v21, s57, v192
	v_med3_f32 v24, v24, s57, v192
	v_med3_f32 v27, v28, s57, v192
	v_med3_f32 v25, v25, s57, v192
	v_med3_f32 v28, v29, s57, v192
	v_cvt_pk_fp8_f32 v8, v16, v17 op_sel:[0,0,1]
	v_cvt_pk_fp8_f32 v9, v20, v21 op_sel:[0,0,1]
	v_cvt_pk_fp8_f32 v10, v24, v25 op_sel:[0,0,1]
	v_cvt_pk_fp8_f32 v11, v27, v28 op_sel:[0,0,1]
	v_lshl_add_u64 v[14:15], v[12:13], 2, s[10:11]
	global_store_dwordx2 v[2:3], v[8:9], off
	global_store_dwordx2 v[2:3], v[10:11], off offset:128
	v_mov_b32_e32 v8, 0
	v_mov_b32_e32 v9, 0
	v_mov_b32_e32 v10, 0
	v_mov_b32_e32 v11, 0
	v_lshlrev_b64 v[12:13], 10, v[12:13]
	v_or_b32_e32 v14, 32, v6
	v_lshl_add_u64 v[12:13], s[14:15], 0, v[12:13]
	v_ashrrev_i32_e32 v15, 31, v14
	v_lshl_add_u64 v[12:13], v[12:13], 0, v[4:5]
	v_lshl_add_u64 v[16:17], v[14:15], 2, s[10:11]
	v_or_b32_e32 v6, 48, v6
	v_mul_f32_e32 v7, 0x3d000000, v194
	v_mul_f32_e32 v18, 0x42000000, v7
	v_pk_mul_f32 v[22:23], v[140:141], v[18:19] op_sel_hi:[1,0]
	v_pk_mul_f32 v[26:27], v[136:137], v[18:19] op_sel_hi:[1,0]
	v_pk_mul_f32 v[20:21], v[142:143], v[18:19] op_sel_hi:[1,0]
	v_pk_mul_f32 v[24:25], v[138:139], v[18:19] op_sel_hi:[1,0]
	v_pk_mul_f32 v[28:29], v[134:135], v[18:19] op_sel_hi:[1,0]
	v_pk_mul_f32 v[30:31], v[132:133], v[18:19] op_sel_hi:[1,0]
	v_pk_mul_f32 v[130:131], v[130:131], v[18:19] op_sel_hi:[1,0]
	v_pk_mul_f32 v[18:19], v[128:129], v[18:19] op_sel_hi:[1,0]
	v_med3_f32 v7, v22, s57, v192
	v_med3_f32 v22, v26, s57, v192
	v_med3_f32 v23, v23, s57, v192
	v_med3_f32 v26, v27, s57, v192
	v_med3_f32 v27, v30, s57, v192
	v_med3_f32 v18, v18, s57, v192
	v_med3_f32 v30, v31, s57, v192
	v_med3_f32 v19, v19, s57, v192
	v_cvt_pk_fp8_f32 v8, v7, v23
	v_cvt_pk_fp8_f32 v9, v22, v26
	v_cvt_pk_fp8_f32 v10, v27, v30
	v_cvt_pk_fp8_f32 v11, v18, v19
	v_med3_f32 v20, v20, s57, v192
	v_med3_f32 v24, v24, s57, v192
	v_med3_f32 v21, v21, s57, v192
	v_med3_f32 v25, v25, s57, v192
	v_med3_f32 v28, v28, s57, v192
	v_med3_f32 v31, v130, s57, v192
	v_med3_f32 v29, v29, s57, v192
	v_med3_f32 v128, v131, s57, v192
	v_cvt_pk_fp8_f32 v8, v20, v21 op_sel:[0,0,1]
	v_cvt_pk_fp8_f32 v9, v24, v25 op_sel:[0,0,1]
	v_cvt_pk_fp8_f32 v10, v28, v29 op_sel:[0,0,1]
	v_cvt_pk_fp8_f32 v11, v31, v128 op_sel:[0,0,1]
	global_store_dwordx2 v[12:13], v[8:9], off
	global_store_dwordx2 v[12:13], v[10:11], off offset:128
	v_mov_b32_e32 v8, 0
	v_mov_b32_e32 v9, 0
	v_mov_b32_e32 v10, 0
	v_mov_b32_e32 v11, 0
	v_lshlrev_b64 v[12:13], 10, v[14:15]
	v_lshl_add_u64 v[12:13], s[14:15], 0, v[12:13]
	v_ashrrev_i32_e32 v7, 31, v6
	v_lshl_add_u64 v[12:13], v[12:13], 0, v[4:5]
	v_lshl_add_u64 v[14:15], v[6:7], 2, s[10:11]
	v_lshlrev_b64 v[6:7], 10, v[6:7]
	v_lshl_add_u64 v[6:7], s[14:15], 0, v[6:7]
	v_lshl_add_u64 v[4:5], v[6:7], 0, v[4:5]
	v_mov_b32_e32 v6, 0
	v_mov_b32_e32 v7, 0
	v_mul_f32_e32 v16, 0x3d000000, v195
	v_mul_f32_e32 v16, 0x42000000, v16
	v_pk_mul_f32 v[20:21], v[124:125], v[16:17] op_sel_hi:[1,0]
	v_pk_mul_f32 v[24:25], v[120:121], v[16:17] op_sel_hi:[1,0]
	v_pk_mul_f32 v[18:19], v[126:127], v[16:17] op_sel_hi:[1,0]
	v_pk_mul_f32 v[22:23], v[122:123], v[16:17] op_sel_hi:[1,0]
	v_pk_mul_f32 v[26:27], v[118:119], v[16:17] op_sel_hi:[1,0]
	v_pk_mul_f32 v[28:29], v[116:117], v[16:17] op_sel_hi:[1,0]
	v_pk_mul_f32 v[30:31], v[114:115], v[16:17] op_sel_hi:[1,0]
	v_pk_mul_f32 v[16:17], v[112:113], v[16:17] op_sel_hi:[1,0]
	v_med3_f32 v20, v20, s57, v192
	v_med3_f32 v24, v24, s57, v192
	v_med3_f32 v21, v21, s57, v192
	v_med3_f32 v25, v25, s57, v192
	v_med3_f32 v28, v28, s57, v192
	v_med3_f32 v16, v16, s57, v192
	v_med3_f32 v29, v29, s57, v192
	v_med3_f32 v17, v17, s57, v192
	v_cvt_pk_fp8_f32 v8, v20, v21
	v_cvt_pk_fp8_f32 v9, v24, v25
	v_cvt_pk_fp8_f32 v10, v28, v29
	v_cvt_pk_fp8_f32 v11, v16, v17
	v_med3_f32 v18, v18, s57, v192
	v_med3_f32 v22, v22, s57, v192
	v_med3_f32 v19, v19, s57, v192
	v_med3_f32 v23, v23, s57, v192
	v_med3_f32 v26, v26, s57, v192
	v_med3_f32 v30, v30, s57, v192
	v_med3_f32 v27, v27, s57, v192
	v_med3_f32 v31, v31, s57, v192
	v_cvt_pk_fp8_f32 v8, v18, v19 op_sel:[0,0,1]
	v_cvt_pk_fp8_f32 v9, v22, v23 op_sel:[0,0,1]
	v_cvt_pk_fp8_f32 v10, v26, v27 op_sel:[0,0,1]
	v_cvt_pk_fp8_f32 v11, v30, v31 op_sel:[0,0,1]
	global_store_dwordx2 v[12:13], v[8:9], off
	global_store_dwordx2 v[12:13], v[10:11], off offset:128
	v_mov_b32_e32 v8, 0
	v_mov_b32_e32 v9, 0
	v_mov_b32_e32 v10, 0
	v_mov_b32_e32 v11, 0
	v_mul_f32_e32 v12, 0x3d000000, v196
	v_mul_f32_e32 v12, 0x42000000, v12
	v_pk_mul_f32 v[16:17], v[108:109], v[12:13] op_sel_hi:[1,0]
	v_pk_mul_f32 v[20:21], v[104:105], v[12:13] op_sel_hi:[1,0]
	v_pk_mul_f32 v[14:15], v[110:111], v[12:13] op_sel_hi:[1,0]
	v_pk_mul_f32 v[18:19], v[106:107], v[12:13] op_sel_hi:[1,0]
	v_pk_mul_f32 v[22:23], v[102:103], v[12:13] op_sel_hi:[1,0]
	v_pk_mul_f32 v[24:25], v[100:101], v[12:13] op_sel_hi:[1,0]
	v_pk_mul_f32 v[26:27], v[98:99], v[12:13] op_sel_hi:[1,0]
	v_pk_mul_f32 v[12:13], v[96:97], v[12:13] op_sel_hi:[1,0]
	v_med3_f32 v16, v16, s57, v192
	v_med3_f32 v20, v20, s57, v192
	v_med3_f32 v17, v17, s57, v192
	v_med3_f32 v21, v21, s57, v192
	v_med3_f32 v24, v24, s57, v192
	v_med3_f32 v12, v12, s57, v192
	v_med3_f32 v25, v25, s57, v192
	v_med3_f32 v13, v13, s57, v192
	v_cvt_pk_fp8_f32 v8, v16, v17
	v_cvt_pk_fp8_f32 v9, v20, v21
	v_cvt_pk_fp8_f32 v10, v24, v25
	v_cvt_pk_fp8_f32 v11, v12, v13
	v_med3_f32 v14, v14, s57, v192
	v_med3_f32 v18, v18, s57, v192
	v_med3_f32 v15, v15, s57, v192
	v_med3_f32 v19, v19, s57, v192
	v_med3_f32 v22, v22, s57, v192
	v_med3_f32 v26, v26, s57, v192
	v_med3_f32 v23, v23, s57, v192
	v_med3_f32 v27, v27, s57, v192
	v_cvt_pk_fp8_f32 v8, v14, v15 op_sel:[0,0,1]
	v_cvt_pk_fp8_f32 v9, v18, v19 op_sel:[0,0,1]
	v_cvt_pk_fp8_f32 v10, v22, v23 op_sel:[0,0,1]
	v_cvt_pk_fp8_f32 v11, v26, v27 op_sel:[0,0,1]
	global_store_dwordx2 v[4:5], v[8:9], off
	global_store_dwordx2 v[4:5], v[10:11], off offset:128
	v_mov_b32_e32 v4, 0
	v_mov_b32_e32 v5, 0
	v_lshl_add_u64 v[8:9], v[2:3], 0, s[4:5]
	s_mov_b64 s[4:5], 0x24000
	v_mul_f32_e32 v10, 0x3d000000, v197
	v_mul_f32_e32 v10, 0x42000000, v10
	v_pk_mul_f32 v[14:15], v[92:93], v[10:11] op_sel_hi:[1,0]
	v_pk_mul_f32 v[18:19], v[88:89], v[10:11] op_sel_hi:[1,0]
	v_pk_mul_f32 v[12:13], v[94:95], v[10:11] op_sel_hi:[1,0]
	v_pk_mul_f32 v[16:17], v[90:91], v[10:11] op_sel_hi:[1,0]
	v_pk_mul_f32 v[20:21], v[86:87], v[10:11] op_sel_hi:[1,0]
	v_pk_mul_f32 v[22:23], v[84:85], v[10:11] op_sel_hi:[1,0]
	v_pk_mul_f32 v[24:25], v[82:83], v[10:11] op_sel_hi:[1,0]
	v_pk_mul_f32 v[10:11], v[80:81], v[10:11] op_sel_hi:[1,0]
	v_med3_f32 v14, v14, s57, v192
	v_med3_f32 v18, v18, s57, v192
	v_med3_f32 v15, v15, s57, v192
	v_med3_f32 v19, v19, s57, v192
	v_med3_f32 v22, v22, s57, v192
	v_med3_f32 v10, v10, s57, v192
	v_med3_f32 v23, v23, s57, v192
	v_med3_f32 v11, v11, s57, v192
	v_cvt_pk_fp8_f32 v4, v14, v15
	v_cvt_pk_fp8_f32 v5, v18, v19
	v_cvt_pk_fp8_f32 v6, v22, v23
	v_cvt_pk_fp8_f32 v7, v10, v11
	v_med3_f32 v12, v12, s57, v192
	v_med3_f32 v16, v16, s57, v192
	v_med3_f32 v13, v13, s57, v192
	v_med3_f32 v17, v17, s57, v192
	v_med3_f32 v20, v20, s57, v192
	v_med3_f32 v24, v24, s57, v192
	v_med3_f32 v21, v21, s57, v192
	v_med3_f32 v25, v25, s57, v192
	v_cvt_pk_fp8_f32 v4, v12, v13 op_sel:[0,0,1]
	v_cvt_pk_fp8_f32 v5, v16, v17 op_sel:[0,0,1]
	v_cvt_pk_fp8_f32 v6, v20, v21 op_sel:[0,0,1]
	v_cvt_pk_fp8_f32 v7, v24, v25 op_sel:[0,0,1]
	v_add_co_u32_e32 v10, vcc, s0, v2
	s_mov_b32 s0, 0x24000
	s_nop 0
	v_addc_co_u32_e32 v11, vcc, 0, v3, vcc
	global_store_dwordx2 v[10:11], v[4:5], off
	global_store_dwordx2 v[8:9], v[6:7], off offset:128
	v_mov_b32_e32 v4, 0
	v_mov_b32_e32 v5, 0
	v_mov_b32_e32 v6, 0
	v_mov_b32_e32 v7, 0
	v_lshl_add_u64 v[8:9], v[2:3], 0, s[4:5]
	s_mov_b64 s[4:5], 0x28000
	v_mul_f32_e32 v10, 0x3d000000, v198
	v_mul_f32_e32 v10, 0x42000000, v10
	v_pk_mul_f32 v[14:15], v[76:77], v[10:11] op_sel_hi:[1,0]
	v_pk_mul_f32 v[18:19], v[72:73], v[10:11] op_sel_hi:[1,0]
	v_pk_mul_f32 v[12:13], v[78:79], v[10:11] op_sel_hi:[1,0]
	v_pk_mul_f32 v[16:17], v[74:75], v[10:11] op_sel_hi:[1,0]
	v_pk_mul_f32 v[20:21], v[70:71], v[10:11] op_sel_hi:[1,0]
	v_pk_mul_f32 v[22:23], v[68:69], v[10:11] op_sel_hi:[1,0]
	v_pk_mul_f32 v[24:25], v[66:67], v[10:11] op_sel_hi:[1,0]
	v_pk_mul_f32 v[10:11], v[64:65], v[10:11] op_sel_hi:[1,0]
	v_med3_f32 v14, v14, s57, v192
	v_med3_f32 v18, v18, s57, v192
	v_med3_f32 v15, v15, s57, v192
	v_med3_f32 v19, v19, s57, v192
	v_med3_f32 v22, v22, s57, v192
	v_med3_f32 v10, v10, s57, v192
	v_med3_f32 v23, v23, s57, v192
	v_med3_f32 v11, v11, s57, v192
	v_cvt_pk_fp8_f32 v4, v14, v15
	v_cvt_pk_fp8_f32 v5, v18, v19
	v_cvt_pk_fp8_f32 v6, v22, v23
	v_cvt_pk_fp8_f32 v7, v10, v11
	v_med3_f32 v12, v12, s57, v192
	v_med3_f32 v16, v16, s57, v192
	v_med3_f32 v13, v13, s57, v192
	v_med3_f32 v17, v17, s57, v192
	v_med3_f32 v20, v20, s57, v192
	v_med3_f32 v24, v24, s57, v192
	v_med3_f32 v21, v21, s57, v192
	v_med3_f32 v25, v25, s57, v192
	v_cvt_pk_fp8_f32 v4, v12, v13 op_sel:[0,0,1]
	v_cvt_pk_fp8_f32 v5, v16, v17 op_sel:[0,0,1]
	v_cvt_pk_fp8_f32 v6, v20, v21 op_sel:[0,0,1]
	v_cvt_pk_fp8_f32 v7, v24, v25 op_sel:[0,0,1]
	v_add_co_u32_e32 v10, vcc, s0, v2
	s_mov_b32 s0, 0x28000
	s_nop 0
	v_addc_co_u32_e32 v11, vcc, 0, v3, vcc
	global_store_dwordx2 v[10:11], v[4:5], off
	global_store_dwordx2 v[8:9], v[6:7], off offset:128
	v_mov_b32_e32 v4, 0
	v_mov_b32_e32 v5, 0
	v_mov_b32_e32 v6, 0
	v_mov_b32_e32 v7, 0
	v_lshl_add_u64 v[8:9], v[2:3], 0, s[4:5]
	s_mov_b64 s[4:5], s[22:23]
	v_mul_f32_e32 v10, 0x3d000000, v199
	v_mul_f32_e32 v10, 0x42000000, v10
	v_pk_mul_f32 v[14:15], v[60:61], v[10:11] op_sel_hi:[1,0]
	v_pk_mul_f32 v[18:19], v[56:57], v[10:11] op_sel_hi:[1,0]
	v_pk_mul_f32 v[12:13], v[62:63], v[10:11] op_sel_hi:[1,0]
	v_pk_mul_f32 v[16:17], v[58:59], v[10:11] op_sel_hi:[1,0]
	v_pk_mul_f32 v[20:21], v[54:55], v[10:11] op_sel_hi:[1,0]
	v_pk_mul_f32 v[22:23], v[52:53], v[10:11] op_sel_hi:[1,0]
	v_pk_mul_f32 v[24:25], v[50:51], v[10:11] op_sel_hi:[1,0]
	v_pk_mul_f32 v[10:11], v[48:49], v[10:11] op_sel_hi:[1,0]
	v_med3_f32 v14, v14, s57, v192
	v_med3_f32 v18, v18, s57, v192
	v_med3_f32 v15, v15, s57, v192
	v_med3_f32 v19, v19, s57, v192
	v_med3_f32 v22, v22, s57, v192
	v_med3_f32 v10, v10, s57, v192
	v_med3_f32 v23, v23, s57, v192
	v_med3_f32 v11, v11, s57, v192
	v_cvt_pk_fp8_f32 v4, v14, v15
	v_cvt_pk_fp8_f32 v5, v18, v19
	v_cvt_pk_fp8_f32 v6, v22, v23
	v_cvt_pk_fp8_f32 v7, v10, v11
	v_med3_f32 v12, v12, s57, v192
	v_med3_f32 v16, v16, s57, v192
	v_med3_f32 v13, v13, s57, v192
	v_med3_f32 v17, v17, s57, v192
	v_med3_f32 v20, v20, s57, v192
	v_med3_f32 v24, v24, s57, v192
	v_med3_f32 v21, v21, s57, v192
	v_med3_f32 v25, v25, s57, v192
	v_cvt_pk_fp8_f32 v4, v12, v13 op_sel:[0,0,1]
	v_cvt_pk_fp8_f32 v5, v16, v17 op_sel:[0,0,1]
	v_cvt_pk_fp8_f32 v6, v20, v21 op_sel:[0,0,1]
	v_cvt_pk_fp8_f32 v7, v24, v25 op_sel:[0,0,1]
	v_add_co_u32_e32 v10, vcc, s0, v2
	s_mov_b32 s0, s18
	s_nop 0
	v_addc_co_u32_e32 v11, vcc, 0, v3, vcc
	global_store_dwordx2 v[10:11], v[4:5], off
	global_store_dwordx2 v[8:9], v[6:7], off offset:128
	v_mov_b32_e32 v0, 0
	v_mov_b32_e32 v1, 0
	v_mov_b32_e32 v4, 0
	v_mov_b32_e32 v5, 0
	s_and_b64 vcc, exec, s[6:7]
	s_mov_b64 s[6:7], 0x2c000
	v_lshl_add_u64 v[6:7], v[2:3], 0, s[6:7]
	v_add_co_u32_e64 v2, s[6:7], s58, v2
	v_mul_f32_e32 v8, 0x3d000000, v200
	v_mul_f32_e32 v8, 0x42000000, v8
	v_pk_mul_f32 v[12:13], v[44:45], v[8:9] op_sel_hi:[1,0]
	v_pk_mul_f32 v[16:17], v[40:41], v[8:9] op_sel_hi:[1,0]
	v_pk_mul_f32 v[10:11], v[46:47], v[8:9] op_sel_hi:[1,0]
	v_pk_mul_f32 v[14:15], v[42:43], v[8:9] op_sel_hi:[1,0]
	v_pk_mul_f32 v[18:19], v[38:39], v[8:9] op_sel_hi:[1,0]
	v_pk_mul_f32 v[20:21], v[36:37], v[8:9] op_sel_hi:[1,0]
	v_pk_mul_f32 v[22:23], v[34:35], v[8:9] op_sel_hi:[1,0]
	v_pk_mul_f32 v[8:9], v[32:33], v[8:9] op_sel_hi:[1,0]
	v_med3_f32 v12, v12, s57, v192
	v_med3_f32 v16, v16, s57, v192
	v_med3_f32 v13, v13, s57, v192
	v_med3_f32 v17, v17, s57, v192
	v_med3_f32 v20, v20, s57, v192
	v_med3_f32 v8, v8, s57, v192
	v_med3_f32 v21, v21, s57, v192
	v_med3_f32 v9, v9, s57, v192
	v_cvt_pk_fp8_f32 v0, v12, v13
	v_cvt_pk_fp8_f32 v1, v16, v17
	v_cvt_pk_fp8_f32 v4, v20, v21
	v_cvt_pk_fp8_f32 v5, v8, v9
	v_med3_f32 v10, v10, s57, v192
	v_med3_f32 v14, v14, s57, v192
	v_med3_f32 v11, v11, s57, v192
	v_med3_f32 v15, v15, s57, v192
	v_med3_f32 v18, v18, s57, v192
	v_med3_f32 v22, v22, s57, v192
	v_med3_f32 v19, v19, s57, v192
	v_med3_f32 v23, v23, s57, v192
	v_cvt_pk_fp8_f32 v0, v10, v11 op_sel:[0,0,1]
	v_cvt_pk_fp8_f32 v1, v14, v15 op_sel:[0,0,1]
	v_cvt_pk_fp8_f32 v4, v18, v19 op_sel:[0,0,1]
	v_cvt_pk_fp8_f32 v5, v22, v23 op_sel:[0,0,1]
	v_addc_co_u32_e64 v3, s[6:7], 0, v3, s[6:7]
	global_store_dwordx2 v[2:3], v[0:1], off
	global_store_dwordx2 v[6:7], v[4:5], off offset:128
	s_cbranch_vccz .LBB0_1060
	s_waitcnt vmcnt(0)
	v_readlane_b32 s54, v242, 34
	s_cmpk_gt_u32 s36, 0xff
	v_readlane_b32 s55, v242, 35
	s_cbranch_scc1 .LBB0_1067
	s_barrier

.LBB0_1203:
	s_ashr_i32 s21, s20, 31
	s_lshl_b64 s[24:25], s[20:21], 19
	s_add_u32 s24, s40, s24
	s_addc_u32 s25, s41, s25
	s_ashr_i32 s19, s18, 31
	s_lshl_b64 s[26:27], s[18:19], 19
	s_add_u32 s26, s38, s26
	s_addc_u32 s27, s39, s27
	s_and_b64 s[28:29], s[12:13], exec
	v_mov_b32_e32 v0, 0
	s_cselect_b32 s19, s27, s17
	s_cselect_b32 s21, s26, s16
	s_mov_b32 s60, -2
	s_mov_b64 s[28:29], 0
	v_mov_b32_e32 v1, 0
	v_mov_b64_e32 v[2:3], 0
	v_mov_b64_e32 v[4:5], 0
	v_mov_b64_e32 v[6:7], 0
	v_mov_b64_e32 v[8:9], 0
	v_mov_b64_e32 v[10:11], 0
	v_mov_b64_e32 v[12:13], 0
	v_mov_b64_e32 v[14:15], 0
	v_mov_b64_e32 v[16:17], 0
	v_mov_b64_e32 v[18:19], 0
	v_mov_b64_e32 v[20:21], 0
	v_mov_b64_e32 v[22:23], 0
	v_mov_b64_e32 v[24:25], 0
	v_mov_b64_e32 v[26:27], 0
	v_mov_b64_e32 v[28:29], 0
	v_mov_b64_e32 v[30:31], 0
	v_mov_b64_e32 v[32:33], 0
	v_mov_b64_e32 v[34:35], 0
	v_mov_b64_e32 v[36:37], 0
	v_mov_b64_e32 v[38:39], 0
	v_mov_b64_e32 v[40:41], 0
	v_mov_b64_e32 v[42:43], 0
	v_mov_b64_e32 v[44:45], 0
	v_mov_b64_e32 v[46:47], 0
	v_mov_b64_e32 v[48:49], 0
	v_mov_b64_e32 v[50:51], 0
	v_mov_b64_e32 v[52:53], 0
	v_mov_b64_e32 v[54:55], 0
	v_mov_b64_e32 v[56:57], 0
	v_mov_b64_e32 v[58:59], 0
	v_mov_b64_e32 v[60:61], 0
	v_mov_b64_e32 v[62:63], 0
	v_mov_b64_e32 v[64:65], 0
	v_mov_b64_e32 v[66:67], 0
	v_mov_b64_e32 v[68:69], 0
	v_mov_b64_e32 v[70:71], 0
	v_mov_b64_e32 v[72:73], 0
	v_mov_b64_e32 v[74:75], 0
	v_mov_b64_e32 v[76:77], 0
	v_mov_b64_e32 v[78:79], 0
	v_mov_b64_e32 v[80:81], 0
	v_mov_b64_e32 v[82:83], 0
	v_mov_b64_e32 v[84:85], 0
	v_mov_b64_e32 v[86:87], 0
	v_mov_b64_e32 v[88:89], 0
	v_mov_b64_e32 v[90:91], 0
	v_mov_b64_e32 v[92:93], 0
	v_mov_b64_e32 v[94:95], 0
	v_mov_b64_e32 v[96:97], 0
	v_mov_b64_e32 v[98:99], 0
	v_mov_b64_e32 v[100:101], 0
	v_mov_b64_e32 v[102:103], 0
	v_mov_b64_e32 v[104:105], 0
	v_mov_b64_e32 v[106:107], 0
	v_mov_b64_e32 v[108:109], 0
	v_mov_b64_e32 v[110:111], 0
	v_mov_b64_e32 v[112:113], 0
	v_mov_b64_e32 v[114:115], 0
	v_mov_b64_e32 v[116:117], 0
	v_mov_b64_e32 v[118:119], 0
	v_mov_b64_e32 v[120:121], 0
	v_mov_b64_e32 v[122:123], 0
	v_mov_b64_e32 v[124:125], 0
	v_mov_b64_e32 v[126:127], 0

.LBB0_1557:
	s_ashr_i32 s25, s24, 31
	s_lshl_b64 s[26:27], s[24:25], 19
	s_add_u32 s26, s45, s26
	s_addc_u32 s27, s46, s27
	s_ashr_i32 s23, s22, 31
	s_lshl_b64 s[28:29], s[22:23], 19
	s_add_u32 s28, s43, s28
	s_addc_u32 s29, s44, s29
	s_and_b64 s[34:35], s[14:15], exec
	v_mov_b32_e32 v0, 0
	s_cselect_b32 s1, s29, s5
	s_cselect_b32 s10, s28, s4
	s_mov_b32 s23, -2
	s_mov_b64 s[34:35], 0
	s_waitcnt lgkmcnt(0)
	v_mov_b32_e32 v1, 0
	v_mov_b64_e32 v[2:3], 0
	v_mov_b64_e32 v[4:5], 0
	v_mov_b64_e32 v[6:7], 0
	v_mov_b64_e32 v[8:9], 0
	v_mov_b64_e32 v[10:11], 0
	v_mov_b64_e32 v[12:13], 0
	v_mov_b64_e32 v[14:15], 0
	v_mov_b64_e32 v[16:17], 0
	v_mov_b64_e32 v[18:19], 0
	v_mov_b64_e32 v[20:21], 0
	v_mov_b64_e32 v[22:23], 0
	v_mov_b64_e32 v[24:25], 0
	v_mov_b64_e32 v[26:27], 0
	v_mov_b64_e32 v[28:29], 0
	v_mov_b64_e32 v[30:31], 0
	v_mov_b64_e32 v[40:41], 0
	v_mov_b64_e32 v[42:43], 0
	v_mov_b64_e32 v[44:45], 0
	v_mov_b64_e32 v[46:47], 0
	v_mov_b64_e32 v[56:57], 0
	v_mov_b64_e32 v[58:59], 0
	v_mov_b64_e32 v[60:61], 0
	v_mov_b64_e32 v[62:63], 0
	v_mov_b64_e32 v[64:65], 0
	v_mov_b64_e32 v[66:67], 0
	v_mov_b64_e32 v[68:69], 0
	v_mov_b64_e32 v[70:71], 0
	v_mov_b64_e32 v[72:73], 0
	v_mov_b64_e32 v[74:75], 0
	v_mov_b64_e32 v[76:77], 0
	v_mov_b64_e32 v[78:79], 0
	v_mov_b64_e32 v[80:81], 0
	v_mov_b64_e32 v[82:83], 0
	v_mov_b64_e32 v[84:85], 0
	v_mov_b64_e32 v[86:87], 0
	v_mov_b64_e32 v[96:97], 0
	v_mov_b64_e32 v[98:99], 0
	v_mov_b64_e32 v[100:101], 0
	v_mov_b64_e32 v[102:103], 0
	v_mov_b64_e32 v[112:113], 0
	v_mov_b64_e32 v[114:115], 0
	v_mov_b32_e32 v116, 0
	s_waitcnt vmcnt(0)
	v_mov_b64_e32 v[88:89], 0
	v_mov_b64_e32 v[90:91], 0
	v_mov_b64_e32 v[92:93], 0
	v_mov_b64_e32 v[94:95], 0
	v_mov_b64_e32 v[104:105], 0
	v_mov_b64_e32 v[106:107], 0
	v_mov_b64_e32 v[108:109], 0
	v_mov_b64_e32 v[110:111], 0
	v_mov_b32_e32 v117, 0
	v_mov_b64_e32 v[118:119], 0
	v_mov_b64_e32 v[120:121], 0
	v_mov_b64_e32 v[122:123], 0
	v_mov_b64_e32 v[124:125], 0
	v_mov_b64_e32 v[126:127], 0
	v_mov_b64_e32 v[128:129], 0
	v_mov_b64_e32 v[130:131], 0
	v_mov_b64_e32 v[132:133], 0
	v_mov_b64_e32 v[134:135], 0
	v_mov_b64_e32 v[136:137], 0
	v_mov_b64_e32 v[138:139], 0
	v_mov_b64_e32 v[140:141], 0
	v_mov_b64_e32 v[142:143], 0

.LBB0_1990:
	v_mov_b32_e32 v0, v209
	s_nop 15
	s_nop 15
	s_mov_b32 s101, 0x44800000
	s_ashr_i32 s2, s0, 31
	v_ashrrev_i32_e32 v1, 2, v0
	v_and_b32_e32 v1, 0xffffffc0, v1
	v_lshl_add_u32 v1, s33, 8, v1
	v_and_or_b32 v4, v0, 15, v1
	v_lshrrev_b32_e32 v2, 1, v0
	s_lshr_b32 s2, s2, 29
	s_add_i32 s2, s0, s2
	s_and_b32 s2, s2, 0x1fffff8
	s_sub_i32 s0, s0, s2
	v_and_b32_e32 v2, 0x78, v2
	v_ashrrev_i32_e32 v5, 31, v4
	v_lshl_or_b32 v2, s0, 7, v2
	v_lshlrev_b64 v[0:1], 10, v[4:5]
	v_ashrrev_i32_e32 v3, 31, v2
	v_lshl_add_u64 v[0:1], s[10:11], 0, v[0:1]
	v_lshl_add_u64 v[0:1], v[0:1], 0, v[2:3]
	v_mul_f32_e32 v10, 0xbd38aa3b, v188
	v_mul_f32_e32 v11, 0xbd38aa3b, v189
	v_mul_f32_e32 v12, 0xbd38aa3b, v190
	v_mul_f32_e32 v13, 0xbd38aa3b, v191
	v_mul_f32_e32 v14, 0xbd38aa3b, v180
	v_mul_f32_e32 v15, 0xbd38aa3b, v181
	v_mul_f32_e32 v16, 0xbd38aa3b, v182
	v_mul_f32_e32 v17, 0xbd38aa3b, v183
	v_exp_f32_e32 v10, v10
	v_exp_f32_e32 v11, v11
	v_exp_f32_e32 v12, v12
	v_exp_f32_e32 v13, v13
	v_exp_f32_e32 v14, v14
	v_exp_f32_e32 v15, v15
	v_exp_f32_e32 v16, v16
	v_exp_f32_e32 v17, v17
	v_fma_f32 v10, v10, s101, s101
	v_fma_f32 v11, v11, s101, s101
	v_fma_f32 v12, v12, s101, s101
	v_fma_f32 v13, v13, s101, s101
	v_fma_f32 v14, v14, s101, s101
	v_fma_f32 v15, v15, s101, s101
	v_fma_f32 v16, v16, s101, s101
	v_fma_f32 v17, v17, s101, s101
	v_rcp_f32_e32 v10, v10
	v_rcp_f32_e32 v11, v11
	v_rcp_f32_e32 v12, v12
	v_rcp_f32_e32 v13, v13
	v_rcp_f32_e32 v14, v14
	v_rcp_f32_e32 v15, v15
	v_rcp_f32_e32 v16, v16
	v_rcp_f32_e32 v17, v17
	v_mul_f32_e32 v10, v188, v10
	v_mul_f32_e32 v11, v189, v11
	v_mul_f32_e32 v12, v190, v12
	v_mul_f32_e32 v13, v191, v13
	v_mul_f32_e32 v14, v180, v14
	v_mul_f32_e32 v15, v181, v15
	v_mul_f32_e32 v16, v182, v16
	v_mul_f32_e32 v17, v183, v17
	v_mul_f32_e32 v10, v10, v184
	v_mul_f32_e32 v11, v11, v185
	v_mul_f32_e32 v12, v12, v186
	v_mul_f32_e32 v13, v13, v187
	v_mul_f32_e32 v14, v14, v176
	v_mul_f32_e32 v15, v15, v177
	v_mul_f32_e32 v16, v16, v178
	v_mul_f32_e32 v17, v17, v179
	v_cvt_pk_fp8_f32 v18, v10, v11
	v_cvt_pk_fp8_f32 v19, v14, v15
	v_cvt_pk_fp8_f32 v18, v12, v13 op_sel:[0,0,1]
	v_cvt_pk_fp8_f32 v19, v16, v17 op_sel:[0,0,1]
	s_nop 0
	global_store_dwordx2 v[0:1], v[18:19], off
	v_or_b32_e32 v8, 16, v4
	v_ashrrev_i32_e32 v9, 31, v8
	v_lshlrev_b64 v[8:9], 10, v[8:9]
	v_lshl_add_u64 v[8:9], s[10:11], 0, v[8:9]
	v_lshl_add_u64 v[8:9], v[8:9], 0, v[2:3]
	v_mul_f32_e32 v10, 0xbd38aa3b, v172
	v_mul_f32_e32 v11, 0xbd38aa3b, v173
	v_mul_f32_e32 v12, 0xbd38aa3b, v174
	v_mul_f32_e32 v13, 0xbd38aa3b, v175
	v_mul_f32_e32 v14, 0xbd38aa3b, v164
	v_mul_f32_e32 v15, 0xbd38aa3b, v165
	v_mul_f32_e32 v16, 0xbd38aa3b, v166
	v_mul_f32_e32 v17, 0xbd38aa3b, v167
	v_exp_f32_e32 v10, v10
	v_exp_f32_e32 v11, v11
	v_exp_f32_e32 v12, v12
	v_exp_f32_e32 v13, v13
	v_exp_f32_e32 v14, v14
	v_exp_f32_e32 v15, v15
	v_exp_f32_e32 v16, v16
	v_exp_f32_e32 v17, v17
	v_fma_f32 v10, v10, s101, s101
	v_fma_f32 v11, v11, s101, s101
	v_fma_f32 v12, v12, s101, s101
	v_fma_f32 v13, v13, s101, s101
	v_fma_f32 v14, v14, s101, s101
	v_fma_f32 v15, v15, s101, s101
	v_fma_f32 v16, v16, s101, s101
	v_fma_f32 v17, v17, s101, s101
	v_rcp_f32_e32 v10, v10
	v_rcp_f32_e32 v11, v11
	v_rcp_f32_e32 v12, v12
	v_rcp_f32_e32 v13, v13
	v_rcp_f32_e32 v14, v14
	v_rcp_f32_e32 v15, v15
	v_rcp_f32_e32 v16, v16
	v_rcp_f32_e32 v17, v17
	v_mul_f32_e32 v10, v172, v10
	v_mul_f32_e32 v11, v173, v11
	v_mul_f32_e32 v12, v174, v12
	v_mul_f32_e32 v13, v175, v13
	v_mul_f32_e32 v14, v164, v14
	v_mul_f32_e32 v15, v165, v15
	v_mul_f32_e32 v16, v166, v16
	v_mul_f32_e32 v17, v167, v17
	v_mul_f32_e32 v10, v10, v168
	v_mul_f32_e32 v11, v11, v169
	v_mul_f32_e32 v12, v12, v170
	v_mul_f32_e32 v13, v13, v171
	v_mul_f32_e32 v14, v14, v160
	v_mul_f32_e32 v15, v15, v161
	v_mul_f32_e32 v16, v16, v162
	v_mul_f32_e32 v17, v17, v163
	v_cvt_pk_fp8_f32 v18, v10, v11
	v_cvt_pk_fp8_f32 v19, v14, v15
	v_cvt_pk_fp8_f32 v18, v12, v13 op_sel:[0,0,1]
	v_cvt_pk_fp8_f32 v19, v16, v17 op_sel:[0,0,1]
	s_nop 0
	global_store_dwordx2 v[8:9], v[18:19], off
	v_or_b32_e32 v8, 32, v4
	v_ashrrev_i32_e32 v9, 31, v8
	v_or_b32_e32 v4, 48, v4
	v_lshlrev_b64 v[6:7], 10, v[8:9]
	v_lshl_add_u64 v[6:7], s[10:11], 0, v[6:7]
	v_lshl_add_u64 v[6:7], v[6:7], 0, v[2:3]
	v_mul_f32_e32 v10, 0xbd38aa3b, v156
	v_mul_f32_e32 v11, 0xbd38aa3b, v157
	v_mul_f32_e32 v12, 0xbd38aa3b, v158
	v_mul_f32_e32 v13, 0xbd38aa3b, v159
	v_mul_f32_e32 v14, 0xbd38aa3b, v148
	v_mul_f32_e32 v15, 0xbd38aa3b, v149
	v_mul_f32_e32 v16, 0xbd38aa3b, v150
	v_mul_f32_e32 v17, 0xbd38aa3b, v151
	v_exp_f32_e32 v10, v10
	v_exp_f32_e32 v11, v11
	v_exp_f32_e32 v12, v12
	v_exp_f32_e32 v13, v13
	v_exp_f32_e32 v14, v14
	v_exp_f32_e32 v15, v15
	v_exp_f32_e32 v16, v16
	v_exp_f32_e32 v17, v17
	v_fma_f32 v10, v10, s101, s101
	v_fma_f32 v11, v11, s101, s101
	v_fma_f32 v12, v12, s101, s101
	v_fma_f32 v13, v13, s101, s101
	v_fma_f32 v14, v14, s101, s101
	v_fma_f32 v15, v15, s101, s101
	v_fma_f32 v16, v16, s101, s101
	v_fma_f32 v17, v17, s101, s101
	v_rcp_f32_e32 v10, v10
	v_rcp_f32_e32 v11, v11
	v_rcp_f32_e32 v12, v12
	v_rcp_f32_e32 v13, v13
	v_rcp_f32_e32 v14, v14
	v_rcp_f32_e32 v15, v15
	v_rcp_f32_e32 v16, v16
	v_rcp_f32_e32 v17, v17
	v_mul_f32_e32 v10, v156, v10
	v_mul_f32_e32 v11, v157, v11
	v_mul_f32_e32 v12, v158, v12
	v_mul_f32_e32 v13, v159, v13
	v_mul_f32_e32 v14, v148, v14
	v_mul_f32_e32 v15, v149, v15
	v_mul_f32_e32 v16, v150, v16
	v_mul_f32_e32 v17, v151, v17
	v_mul_f32_e32 v10, v10, v152
	v_mul_f32_e32 v11, v11, v153
	v_mul_f32_e32 v12, v12, v154
	v_mul_f32_e32 v13, v13, v155
	v_mul_f32_e32 v14, v14, v144
	v_mul_f32_e32 v15, v15, v145
	v_mul_f32_e32 v16, v16, v146
	v_mul_f32_e32 v17, v17, v147
	v_cvt_pk_fp8_f32 v18, v10, v11
	v_cvt_pk_fp8_f32 v19, v14, v15
	v_cvt_pk_fp8_f32 v18, v12, v13 op_sel:[0,0,1]
	v_cvt_pk_fp8_f32 v19, v16, v17 op_sel:[0,0,1]
	s_nop 0
	global_store_dwordx2 v[6:7], v[18:19], off
	v_ashrrev_i32_e32 v5, 31, v4
	v_lshlrev_b64 v[4:5], 10, v[4:5]
	v_lshl_add_u64 v[4:5], s[10:11], 0, v[4:5]
	v_lshl_add_u64 v[2:3], v[4:5], 0, v[2:3]
	s_mov_b32 s0, 0x20000
	v_mul_f32_e32 v10, 0xbd38aa3b, v140
	v_mul_f32_e32 v11, 0xbd38aa3b, v141
	v_mul_f32_e32 v12, 0xbd38aa3b, v142
	v_mul_f32_e32 v13, 0xbd38aa3b, v143
	v_mul_f32_e32 v14, 0xbd38aa3b, v132
	v_mul_f32_e32 v15, 0xbd38aa3b, v133
	v_mul_f32_e32 v16, 0xbd38aa3b, v134
	v_mul_f32_e32 v17, 0xbd38aa3b, v135
	v_exp_f32_e32 v10, v10
	v_exp_f32_e32 v11, v11
	v_exp_f32_e32 v12, v12
	v_exp_f32_e32 v13, v13
	v_exp_f32_e32 v14, v14
	v_exp_f32_e32 v15, v15
	v_exp_f32_e32 v16, v16
	v_exp_f32_e32 v17, v17
	v_fma_f32 v10, v10, s101, s101
	v_fma_f32 v11, v11, s101, s101
	v_fma_f32 v12, v12, s101, s101
	v_fma_f32 v13, v13, s101, s101
	v_fma_f32 v14, v14, s101, s101
	v_fma_f32 v15, v15, s101, s101
	v_fma_f32 v16, v16, s101, s101
	v_fma_f32 v17, v17, s101, s101
	v_rcp_f32_e32 v10, v10
	v_rcp_f32_e32 v11, v11
	v_rcp_f32_e32 v12, v12
	v_rcp_f32_e32 v13, v13
	v_rcp_f32_e32 v14, v14
	v_rcp_f32_e32 v15, v15
	v_rcp_f32_e32 v16, v16
	v_rcp_f32_e32 v17, v17
	v_mul_f32_e32 v10, v140, v10
	v_mul_f32_e32 v11, v141, v11
	v_mul_f32_e32 v12, v142, v12
	v_mul_f32_e32 v13, v143, v13
	v_mul_f32_e32 v14, v132, v14
	v_mul_f32_e32 v15, v133, v15
	v_mul_f32_e32 v16, v134, v16
	v_mul_f32_e32 v17, v135, v17
	v_mul_f32_e32 v10, v10, v136
	v_mul_f32_e32 v11, v11, v137
	v_mul_f32_e32 v12, v12, v138
	v_mul_f32_e32 v13, v13, v139
	v_mul_f32_e32 v14, v14, v128
	v_mul_f32_e32 v15, v15, v129
	v_mul_f32_e32 v16, v16, v130
	v_mul_f32_e32 v17, v17, v131
	v_cvt_pk_fp8_f32 v18, v10, v11
	v_cvt_pk_fp8_f32 v19, v14, v15
	v_cvt_pk_fp8_f32 v18, v12, v13 op_sel:[0,0,1]
	v_cvt_pk_fp8_f32 v19, v16, v17 op_sel:[0,0,1]
	s_nop 0
	global_store_dwordx2 v[2:3], v[18:19], off
	s_mov_b32 s33, s49
	v_add_co_u32_e32 v6, vcc, s0, v0
	v_addc_co_u32_e32 v7, vcc, 0, v1, vcc
	v_mul_f32_e32 v10, 0xbd38aa3b, v124
	v_mul_f32_e32 v11, 0xbd38aa3b, v125
	v_mul_f32_e32 v12, 0xbd38aa3b, v126
	v_mul_f32_e32 v13, 0xbd38aa3b, v127
	v_mul_f32_e32 v14, 0xbd38aa3b, v116
	v_mul_f32_e32 v15, 0xbd38aa3b, v117
	v_mul_f32_e32 v16, 0xbd38aa3b, v118
	v_mul_f32_e32 v17, 0xbd38aa3b, v119
	v_exp_f32_e32 v10, v10
	v_exp_f32_e32 v11, v11
	v_exp_f32_e32 v12, v12
	v_exp_f32_e32 v13, v13
	v_exp_f32_e32 v14, v14
	v_exp_f32_e32 v15, v15
	v_exp_f32_e32 v16, v16
	v_exp_f32_e32 v17, v17
	v_fma_f32 v10, v10, s101, s101
	v_fma_f32 v11, v11, s101, s101
	v_fma_f32 v12, v12, s101, s101
	v_fma_f32 v13, v13, s101, s101
	v_fma_f32 v14, v14, s101, s101
	v_fma_f32 v15, v15, s101, s101
	v_fma_f32 v16, v16, s101, s101
	v_fma_f32 v17, v17, s101, s101
	v_rcp_f32_e32 v10, v10
	v_rcp_f32_e32 v11, v11
	v_rcp_f32_e32 v12, v12
	v_rcp_f32_e32 v13, v13
	v_rcp_f32_e32 v14, v14
	v_rcp_f32_e32 v15, v15
	v_rcp_f32_e32 v16, v16
	v_rcp_f32_e32 v17, v17
	v_mul_f32_e32 v10, v124, v10
	v_mul_f32_e32 v11, v125, v11
	v_mul_f32_e32 v12, v126, v12
	v_mul_f32_e32 v13, v127, v13
	v_mul_f32_e32 v14, v116, v14
	v_mul_f32_e32 v15, v117, v15
	v_mul_f32_e32 v16, v118, v16
	v_mul_f32_e32 v17, v119, v17
	v_mul_f32_e32 v10, v10, v120
	v_mul_f32_e32 v11, v11, v121
	v_mul_f32_e32 v12, v12, v122
	v_mul_f32_e32 v13, v13, v123
	v_mul_f32_e32 v14, v14, v112
	v_mul_f32_e32 v15, v15, v113
	v_mul_f32_e32 v16, v16, v114
	v_mul_f32_e32 v17, v17, v115
	v_cvt_pk_fp8_f32 v18, v10, v11
	v_cvt_pk_fp8_f32 v19, v14, v15
	v_cvt_pk_fp8_f32 v18, v12, v13 op_sel:[0,0,1]
	v_cvt_pk_fp8_f32 v19, v16, v17 op_sel:[0,0,1]
	s_nop 0
	global_store_dwordx2 v[6:7], v[18:19], off
	s_mov_b32 s0, 0x24000
	v_add_co_u32_e32 v6, vcc, s0, v0
	v_addc_co_u32_e32 v7, vcc, 0, v1, vcc
	v_mul_f32_e32 v10, 0xbd38aa3b, v108
	v_mul_f32_e32 v11, 0xbd38aa3b, v109
	v_mul_f32_e32 v12, 0xbd38aa3b, v110
	v_mul_f32_e32 v13, 0xbd38aa3b, v111
	v_mul_f32_e32 v14, 0xbd38aa3b, v100
	v_mul_f32_e32 v15, 0xbd38aa3b, v101
	v_mul_f32_e32 v16, 0xbd38aa3b, v102
	v_mul_f32_e32 v17, 0xbd38aa3b, v103
	v_exp_f32_e32 v10, v10
	v_exp_f32_e32 v11, v11
	v_exp_f32_e32 v12, v12
	v_exp_f32_e32 v13, v13
	v_exp_f32_e32 v14, v14
	v_exp_f32_e32 v15, v15
	v_exp_f32_e32 v16, v16
	v_exp_f32_e32 v17, v17
	v_fma_f32 v10, v10, s101, s101
	v_fma_f32 v11, v11, s101, s101
	v_fma_f32 v12, v12, s101, s101
	v_fma_f32 v13, v13, s101, s101
	v_fma_f32 v14, v14, s101, s101
	v_fma_f32 v15, v15, s101, s101
	v_fma_f32 v16, v16, s101, s101
	v_fma_f32 v17, v17, s101, s101
	v_rcp_f32_e32 v10, v10
	v_rcp_f32_e32 v11, v11
	v_rcp_f32_e32 v12, v12
	v_rcp_f32_e32 v13, v13
	v_rcp_f32_e32 v14, v14
	v_rcp_f32_e32 v15, v15
	v_rcp_f32_e32 v16, v16
	v_rcp_f32_e32 v17, v17
	v_mul_f32_e32 v10, v108, v10
	v_mul_f32_e32 v11, v109, v11
	v_mul_f32_e32 v12, v110, v12
	v_mul_f32_e32 v13, v111, v13
	v_mul_f32_e32 v14, v100, v14
	v_mul_f32_e32 v15, v101, v15
	v_mul_f32_e32 v16, v102, v16
	v_mul_f32_e32 v17, v103, v17
	v_mul_f32_e32 v10, v10, v104
	v_mul_f32_e32 v11, v11, v105
	v_mul_f32_e32 v12, v12, v106
	v_mul_f32_e32 v13, v13, v107
	v_mul_f32_e32 v14, v14, v96
	v_mul_f32_e32 v15, v15, v97
	v_mul_f32_e32 v16, v16, v98
	v_mul_f32_e32 v17, v17, v99
	v_cvt_pk_fp8_f32 v18, v10, v11
	v_cvt_pk_fp8_f32 v19, v14, v15
	v_cvt_pk_fp8_f32 v18, v12, v13 op_sel:[0,0,1]
	v_cvt_pk_fp8_f32 v19, v16, v17 op_sel:[0,0,1]
	s_nop 0
	global_store_dwordx2 v[6:7], v[18:19], off
	s_mov_b32 s0, 0x28000
	v_add_co_u32_e32 v6, vcc, s0, v0
	v_addc_co_u32_e32 v7, vcc, 0, v1, vcc
	v_mul_f32_e32 v10, 0xbd38aa3b, v92
	v_mul_f32_e32 v11, 0xbd38aa3b, v93
	v_mul_f32_e32 v12, 0xbd38aa3b, v94
	v_mul_f32_e32 v13, 0xbd38aa3b, v95
	v_mul_f32_e32 v14, 0xbd38aa3b, v84
	v_mul_f32_e32 v15, 0xbd38aa3b, v85
	v_mul_f32_e32 v16, 0xbd38aa3b, v86
	v_mul_f32_e32 v17, 0xbd38aa3b, v87
	v_exp_f32_e32 v10, v10
	v_exp_f32_e32 v11, v11
	v_exp_f32_e32 v12, v12
	v_exp_f32_e32 v13, v13
	v_exp_f32_e32 v14, v14
	v_exp_f32_e32 v15, v15
	v_exp_f32_e32 v16, v16
	v_exp_f32_e32 v17, v17
	v_fma_f32 v10, v10, s101, s101
	v_fma_f32 v11, v11, s101, s101
	v_fma_f32 v12, v12, s101, s101
	v_fma_f32 v13, v13, s101, s101
	v_fma_f32 v14, v14, s101, s101
	v_fma_f32 v15, v15, s101, s101
	v_fma_f32 v16, v16, s101, s101
	v_fma_f32 v17, v17, s101, s101
	v_rcp_f32_e32 v10, v10
	v_rcp_f32_e32 v11, v11
	v_rcp_f32_e32 v12, v12
	v_rcp_f32_e32 v13, v13
	v_rcp_f32_e32 v14, v14
	v_rcp_f32_e32 v15, v15
	v_rcp_f32_e32 v16, v16
	v_rcp_f32_e32 v17, v17
	v_mul_f32_e32 v10, v92, v10
	v_mul_f32_e32 v11, v93, v11
	v_mul_f32_e32 v12, v94, v12
	v_mul_f32_e32 v13, v95, v13
	v_mul_f32_e32 v14, v84, v14
	v_mul_f32_e32 v15, v85, v15
	v_mul_f32_e32 v16, v86, v16
	v_mul_f32_e32 v17, v87, v17
	v_mul_f32_e32 v10, v10, v88
	v_mul_f32_e32 v11, v11, v89
	v_mul_f32_e32 v12, v12, v90
	v_mul_f32_e32 v13, v13, v91
	v_mul_f32_e32 v14, v14, v80
	v_mul_f32_e32 v15, v15, v81
	v_mul_f32_e32 v16, v16, v82
	v_mul_f32_e32 v17, v17, v83
	v_cvt_pk_fp8_f32 v18, v10, v11
	v_cvt_pk_fp8_f32 v19, v14, v15
	v_cvt_pk_fp8_f32 v18, v12, v13 op_sel:[0,0,1]
	v_cvt_pk_fp8_f32 v19, v16, v17 op_sel:[0,0,1]
	s_nop 0
	global_store_dwordx2 v[6:7], v[18:19], off
	v_add_co_u32_e32 v0, vcc, 0x2c000, v0
	s_mov_b32 s0, s20
	s_nop 0
	v_addc_co_u32_e32 v1, vcc, 0, v1, vcc
	s_and_b64 vcc, exec, s[14:15]
	s_mov_b64 s[2:3], s[12:13]
	v_mul_f32_e32 v10, 0xbd38aa3b, v76
	v_mul_f32_e32 v11, 0xbd38aa3b, v77
	v_mul_f32_e32 v12, 0xbd38aa3b, v78
	v_mul_f32_e32 v13, 0xbd38aa3b, v79
	v_mul_f32_e32 v14, 0xbd38aa3b, v68
	v_mul_f32_e32 v15, 0xbd38aa3b, v69
	v_mul_f32_e32 v16, 0xbd38aa3b, v70
	v_mul_f32_e32 v17, 0xbd38aa3b, v71
	v_exp_f32_e32 v10, v10
	v_exp_f32_e32 v11, v11
	v_exp_f32_e32 v12, v12
	v_exp_f32_e32 v13, v13
	v_exp_f32_e32 v14, v14
	v_exp_f32_e32 v15, v15
	v_exp_f32_e32 v16, v16
	v_exp_f32_e32 v17, v17
	v_fma_f32 v10, v10, s101, s101
	v_fma_f32 v11, v11, s101, s101
	v_fma_f32 v12, v12, s101, s101
	v_fma_f32 v13, v13, s101, s101
	v_fma_f32 v14, v14, s101, s101
	v_fma_f32 v15, v15, s101, s101
	v_fma_f32 v16, v16, s101, s101
	v_fma_f32 v17, v17, s101, s101
	v_rcp_f32_e32 v10, v10
	v_rcp_f32_e32 v11, v11
	v_rcp_f32_e32 v12, v12
	v_rcp_f32_e32 v13, v13
	v_rcp_f32_e32 v14, v14
	v_rcp_f32_e32 v15, v15
	v_rcp_f32_e32 v16, v16
	v_rcp_f32_e32 v17, v17
	v_mul_f32_e32 v10, v76, v10
	v_mul_f32_e32 v11, v77, v11
	v_mul_f32_e32 v12, v78, v12
	v_mul_f32_e32 v13, v79, v13
	v_mul_f32_e32 v14, v68, v14
	v_mul_f32_e32 v15, v69, v15
	v_mul_f32_e32 v16, v70, v16
	v_mul_f32_e32 v17, v71, v17
	v_mul_f32_e32 v10, v10, v72
	v_mul_f32_e32 v11, v11, v73
	v_mul_f32_e32 v12, v12, v74
	v_mul_f32_e32 v13, v13, v75
	v_mul_f32_e32 v14, v14, v64
	v_mul_f32_e32 v15, v15, v65
	v_mul_f32_e32 v16, v16, v66
	v_mul_f32_e32 v17, v17, v67
	v_cvt_pk_fp8_f32 v18, v10, v11
	v_cvt_pk_fp8_f32 v19, v14, v15
	v_cvt_pk_fp8_f32 v18, v12, v13 op_sel:[0,0,1]
	v_cvt_pk_fp8_f32 v19, v16, v17 op_sel:[0,0,1]
	s_nop 0
	global_store_dwordx2 v[0:1], v[18:19], off
	s_cbranch_vccnz .LBB0_1997

.LBB0_1993:
	s_ashr_i32 s21, s20, 31
	s_lshl_b64 s[4:5], s[20:21], 18
	s_add_u32 s12, s28, s4
	s_addc_u32 s13, s29, s5
	s_and_b64 s[4:5], s[16:17], exec
	s_cselect_b32 s21, s13, s3
	s_cselect_b32 s50, s12, s2
	s_lshl_b32 s4, s41, 10
	s_add_i32 s4, s4, 0
	s_add_i32 s4, s4, 0x20010
	v_mov_b32_e32 v64, 0
	v_add3_u32 v233, s4, v213, v214
	v_add3_u32 v234, s4, v215, v216
	s_mov_b32 s51, -2
	s_mov_b64 s[4:5], 0xdbff000
	v_mov_b32_e32 v65, 0
	v_mov_b64_e32 v[66:67], 0
	v_mov_b64_e32 v[68:69], 0
	v_mov_b64_e32 v[70:71], 0
	v_mov_b64_e32 v[72:73], 0
	v_mov_b64_e32 v[74:75], 0
	v_mov_b64_e32 v[76:77], 0
	v_mov_b64_e32 v[78:79], 0
	v_mov_b64_e32 v[80:81], 0
	v_mov_b64_e32 v[82:83], 0
	v_mov_b64_e32 v[84:85], 0
	v_mov_b64_e32 v[86:87], 0
	v_mov_b64_e32 v[88:89], 0
	v_mov_b64_e32 v[90:91], 0
	v_mov_b64_e32 v[92:93], 0
	v_mov_b64_e32 v[94:95], 0
	v_mov_b64_e32 v[96:97], 0
	v_mov_b64_e32 v[98:99], 0
	v_mov_b64_e32 v[100:101], 0
	v_mov_b64_e32 v[102:103], 0
	v_mov_b64_e32 v[104:105], 0
	v_mov_b64_e32 v[106:107], 0
	v_mov_b64_e32 v[108:109], 0
	v_mov_b64_e32 v[110:111], 0
	v_mov_b64_e32 v[112:113], 0
	v_mov_b64_e32 v[114:115], 0
	v_mov_b64_e32 v[116:117], 0
	v_mov_b64_e32 v[118:119], 0
	v_mov_b64_e32 v[120:121], 0
	v_mov_b64_e32 v[122:123], 0
	v_mov_b64_e32 v[124:125], 0
	v_mov_b64_e32 v[126:127], 0
	v_mov_b64_e32 v[128:129], 0
	v_mov_b64_e32 v[130:131], 0
	v_mov_b64_e32 v[132:133], 0
	v_mov_b64_e32 v[134:135], 0
	v_mov_b64_e32 v[136:137], 0
	v_mov_b64_e32 v[138:139], 0
	v_mov_b64_e32 v[140:141], 0
	v_mov_b64_e32 v[142:143], 0
	v_mov_b64_e32 v[144:145], 0
	v_mov_b64_e32 v[146:147], 0
	v_mov_b64_e32 v[148:149], 0
	v_mov_b64_e32 v[150:151], 0
	v_mov_b64_e32 v[152:153], 0
	v_mov_b64_e32 v[154:155], 0
	v_mov_b64_e32 v[156:157], 0
	v_mov_b64_e32 v[158:159], 0
	v_mov_b64_e32 v[160:161], 0
	v_mov_b64_e32 v[162:163], 0
	v_mov_b64_e32 v[164:165], 0
	v_mov_b64_e32 v[166:167], 0
	v_mov_b64_e32 v[168:169], 0
	v_mov_b64_e32 v[170:171], 0
	v_mov_b64_e32 v[172:173], 0
	v_mov_b64_e32 v[174:175], 0
	v_mov_b64_e32 v[176:177], 0
	v_mov_b64_e32 v[178:179], 0
	v_mov_b64_e32 v[180:181], 0
	v_mov_b64_e32 v[182:183], 0
	v_mov_b64_e32 v[184:185], 0
	v_mov_b64_e32 v[186:187], 0
	v_mov_b64_e32 v[188:189], 0
	v_mov_b64_e32 v[190:191], 0
	s_branch .LBB0_1995

.LBB0_2058:
	s_ashr_i32 s13, s12, 31
	s_lshl_b64 s[6:7], s[12:13], 18
	s_add_u32 s6, s37, s6
	s_addc_u32 s7, s38, s7
	s_ashr_i32 s19, s18, 31
	s_lshl_b64 s[20:21], s[18:19], 18
	s_add_u32 s20, s35, s20
	s_addc_u32 s21, s36, s21
	s_and_b64 s[24:25], s[16:17], exec
	v_mov_b32_e32 v32, 0
	s_cselect_b32 s13, s21, s3
	s_cselect_b32 s19, s20, s2
	s_mov_b32 s33, -2
	s_mov_b64 s[28:29], 0
	v_mov_b32_e32 v33, 0
	v_mov_b64_e32 v[34:35], 0
	v_mov_b64_e32 v[36:37], 0
	v_mov_b64_e32 v[38:39], 0
	v_mov_b64_e32 v[40:41], 0
	v_mov_b64_e32 v[42:43], 0
	v_mov_b64_e32 v[44:45], 0
	v_mov_b64_e32 v[46:47], 0
	v_mov_b64_e32 v[48:49], 0
	v_mov_b64_e32 v[50:51], 0
	v_mov_b64_e32 v[52:53], 0
	v_mov_b64_e32 v[54:55], 0
	v_mov_b64_e32 v[56:57], 0
	v_mov_b64_e32 v[58:59], 0
	v_mov_b64_e32 v[60:61], 0
	v_mov_b64_e32 v[62:63], 0
	v_mov_b64_e32 v[64:65], 0
	v_mov_b64_e32 v[66:67], 0
	v_mov_b64_e32 v[68:69], 0
	v_mov_b64_e32 v[70:71], 0
	v_mov_b64_e32 v[72:73], 0
	v_mov_b64_e32 v[74:75], 0
	v_mov_b64_e32 v[76:77], 0
	v_mov_b64_e32 v[78:79], 0
	v_mov_b64_e32 v[80:81], 0
	v_mov_b64_e32 v[82:83], 0
	v_mov_b64_e32 v[84:85], 0
	v_mov_b64_e32 v[86:87], 0
	v_mov_b64_e32 v[88:89], 0
	v_mov_b64_e32 v[90:91], 0
	v_mov_b64_e32 v[92:93], 0
	v_mov_b64_e32 v[94:95], 0
	v_mov_b64_e32 v[96:97], 0
	v_mov_b64_e32 v[98:99], 0
	v_mov_b64_e32 v[100:101], 0
	v_mov_b64_e32 v[102:103], 0
	v_mov_b64_e32 v[104:105], 0
	v_mov_b64_e32 v[106:107], 0
	v_mov_b64_e32 v[108:109], 0
	v_mov_b64_e32 v[110:111], 0
	v_mov_b64_e32 v[112:113], 0
	v_mov_b64_e32 v[114:115], 0
	v_mov_b64_e32 v[116:117], 0
	v_mov_b64_e32 v[118:119], 0
	v_mov_b64_e32 v[120:121], 0
	v_mov_b64_e32 v[122:123], 0
	v_mov_b64_e32 v[124:125], 0
	v_mov_b64_e32 v[126:127], 0
	v_mov_b64_e32 v[128:129], 0
	v_mov_b64_e32 v[130:131], 0
	v_mov_b64_e32 v[132:133], 0
	v_mov_b64_e32 v[134:135], 0
	v_mov_b64_e32 v[136:137], 0
	v_mov_b64_e32 v[138:139], 0
	v_mov_b64_e32 v[140:141], 0
	v_mov_b64_e32 v[142:143], 0
	v_mov_b64_e32 v[144:145], 0
	v_mov_b64_e32 v[146:147], 0
	v_mov_b64_e32 v[148:149], 0
	v_mov_b64_e32 v[150:151], 0
	v_mov_b64_e32 v[152:153], 0
	v_mov_b64_e32 v[154:155], 0
	v_mov_b64_e32 v[156:157], 0
	v_mov_b64_e32 v[158:159], 0
.LBB0_2059:
	s_add_u32 s24, s28, 0x100
	ds_read_b128 v[0:3], v174
	ds_read_b128 v[4:7], v175
	ds_read_b128 v[8:11], v182
	ds_read_b128 v[12:15], v183
	s_addc_u32 s25, s29, 0
	s_and_b32 s57, s24, 0x300
	s_add_u32 s56, s2, s57
	s_addc_u32 s58, s3, 0
	s_cmp_eq_u32 s33, 4
	s_cselect_b64 s[30:31], -1, 0
	s_and_b64 s[26:27], s[30:31], exec
	s_cselect_b32 s27, s13, s58
	s_cselect_b32 s26, s19, s56
	s_cselect_b32 s56, 0, 0
	s_cselect_b32 s57, 0, s57
	s_add_u32 s28, s4, s28
	s_addc_u32 s29, s5, s29
	s_add_u32 s28, s28, 0x20080
	s_addc_u32 s29, s29, 0
	ds_read_b128 v[194:197], v190
	ds_read_b128 v[210:213], v190 offset:2048
	ds_read_b128 v[198:201], v191
	ds_read_b128 v[214:217], v191 offset:2048
	ds_read_b128 v[218:221], v190 offset:4096
	ds_read_b128 v[226:229], v190 offset:6144
	ds_read_b128 v[222:225], v191 offset:4096
	ds_read_b128 v[230:233], v191 offset:6144
	s_add_i32 m0, s1, 0xc000
	s_nop 0
	global_load_lds_dwordx4 v166, s[28:29]
	s_add_i32 m0, s1, 0xe000
	s_nop 0
	global_load_lds_dwordx4 v162, s[28:29]
	s_waitcnt lgkmcnt(8)
	s_barrier
	s_waitcnt lgkmcnt(0)
	s_setprio 1
	s_waitcnt lgkmcnt(0)
	v_mfma_scale_f32_16x16x128_f8f6f4 v[156:159], v[0:7], v[194:201], v[156:159], v173, v173 op_sel_hi:[0,0,0]
	v_mfma_scale_f32_16x16x128_f8f6f4 v[152:155], v[8:15], v[194:201], v[152:155], v173, v173 op_sel_hi:[0,0,0]
	v_mfma_scale_f32_16x16x128_f8f6f4 v[140:143], v[0:7], v[210:217], v[140:143], v173, v173 op_sel_hi:[0,0,0]
	v_mfma_scale_f32_16x16x128_f8f6f4 v[136:139], v[8:15], v[210:217], v[136:139], v173, v173 op_sel_hi:[0,0,0]
	v_mfma_scale_f32_16x16x128_f8f6f4 v[124:127], v[0:7], v[218:225], v[124:127], v173, v173 op_sel_hi:[0,0,0]
	v_mfma_scale_f32_16x16x128_f8f6f4 v[120:123], v[8:15], v[218:225], v[120:123], v173, v173 op_sel_hi:[0,0,0]
	v_mfma_scale_f32_16x16x128_f8f6f4 v[108:111], v[0:7], v[226:233], v[108:111], v173, v173 op_sel_hi:[0,0,0]
	v_mfma_scale_f32_16x16x128_f8f6f4 v[104:107], v[8:15], v[226:233], v[104:107], v173, v173 op_sel_hi:[0,0,0]
	s_setprio 0
	s_barrier
	s_mov_b64 s[28:29], s[26:27]
	s_mov_b32 m0, s23
	ds_read_b128 v[16:19], v176
	ds_read_b128 v[20:23], v177
	ds_read_b128 v[24:27], v184
	ds_read_b128 v[28:31], v185
	s_nop 0
	global_load_lds_dwordx4 v164, s[28:29]
	s_mov_b32 m0, s41
	s_nop 0
	global_load_lds_dwordx4 v160, s[28:29]
	s_barrier
	s_waitcnt lgkmcnt(0)
	s_setprio 1
	s_waitcnt lgkmcnt(0)
	v_mfma_scale_f32_16x16x128_f8f6f4 v[148:151], v[16:23], v[194:201], v[148:151], v173, v173 op_sel_hi:[0,0,0]
	v_mfma_scale_f32_16x16x128_f8f6f4 v[144:147], v[24:31], v[194:201], v[144:147], v173, v173 op_sel_hi:[0,0,0]
	v_mfma_scale_f32_16x16x128_f8f6f4 v[132:135], v[16:23], v[210:217], v[132:135], v173, v173 op_sel_hi:[0,0,0]
	v_mfma_scale_f32_16x16x128_f8f6f4 v[128:131], v[24:31], v[210:217], v[128:131], v173, v173 op_sel_hi:[0,0,0]
	v_mfma_scale_f32_16x16x128_f8f6f4 v[116:119], v[16:23], v[218:225], v[116:119], v173, v173 op_sel_hi:[0,0,0]
	v_mfma_scale_f32_16x16x128_f8f6f4 v[112:115], v[24:31], v[218:225], v[112:115], v173, v173 op_sel_hi:[0,0,0]
	v_mfma_scale_f32_16x16x128_f8f6f4 v[100:103], v[16:23], v[226:233], v[100:103], v173, v173 op_sel_hi:[0,0,0]
	v_mfma_scale_f32_16x16x128_f8f6f4 v[96:99], v[24:31], v[226:233], v[96:99], v173, v173 op_sel_hi:[0,0,0]
	s_setprio 0
	s_and_b64 s[28:29], s[16:17], s[30:31]
	s_and_b64 s[28:29], s[28:29], exec
	s_cselect_b32 s28, s6, s4
	s_cselect_b32 s29, s7, s5
	s_add_u32 s28, s28, s57
	s_addc_u32 s29, s29, s56
	s_mov_b64 s[30:31], s[28:29]
	s_mov_b32 m0, s1
	s_barrier
	ds_read_b128 v[194:197], v190 offset:16384
	ds_read_b128 v[210:213], v190 offset:18432
	ds_read_b128 v[198:201], v191 offset:16384
	ds_read_b128 v[214:217], v191 offset:18432
	ds_read_b128 v[218:221], v190 offset:20480
	ds_read_b128 v[226:229], v190 offset:22528
	ds_read_b128 v[222:225], v191 offset:20480
	ds_read_b128 v[230:233], v191 offset:22528
	s_nop 0
	global_load_lds_dwordx4 v166, s[30:31]
	s_mov_b32 m0, s42
	s_nop 0
	global_load_lds_dwordx4 v162, s[30:31]
	s_barrier
	s_waitcnt lgkmcnt(0)
	s_setprio 1
	s_waitcnt lgkmcnt(0)
	v_mfma_scale_f32_16x16x128_f8f6f4 v[92:95], v[0:7], v[194:201], v[92:95], v173, v173 op_sel_hi:[0,0,0]
	v_mfma_scale_f32_16x16x128_f8f6f4 v[88:91], v[8:15], v[194:201], v[88:91], v173, v173 op_sel_hi:[0,0,0]
	v_mfma_scale_f32_16x16x128_f8f6f4 v[76:79], v[0:7], v[210:217], v[76:79], v173, v173 op_sel_hi:[0,0,0]
	v_mfma_scale_f32_16x16x128_f8f6f4 v[72:75], v[8:15], v[210:217], v[72:75], v173, v173 op_sel_hi:[0,0,0]
	v_mfma_scale_f32_16x16x128_f8f6f4 v[60:63], v[0:7], v[218:225], v[60:63], v173, v173 op_sel_hi:[0,0,0]
	v_mfma_scale_f32_16x16x128_f8f6f4 v[56:59], v[8:15], v[218:225], v[56:59], v173, v173 op_sel_hi:[0,0,0]
	v_mfma_scale_f32_16x16x128_f8f6f4 v[44:47], v[0:7], v[226:233], v[44:47], v173, v173 op_sel_hi:[0,0,0]
	v_mfma_scale_f32_16x16x128_f8f6f4 v[40:43], v[8:15], v[226:233], v[40:43], v173, v173 op_sel_hi:[0,0,0]
	s_setprio 0
	s_barrier
	s_add_u32 s30, s26, 0x20000
	s_addc_u32 s31, s27, 0
	s_mov_b32 m0, s43
	s_nop 0
	global_load_lds_dwordx4 v164, s[30:31]
	s_mov_b32 m0, s44
	s_nop 0
	global_load_lds_dwordx4 v160, s[30:31]
	s_waitcnt vmcnt(6)
	s_barrier
	s_setprio 1
	v_mfma_scale_f32_16x16x128_f8f6f4 v[84:87], v[16:23], v[194:201], v[84:87], v173, v173 op_sel_hi:[0,0,0]
	v_mfma_scale_f32_16x16x128_f8f6f4 v[80:83], v[24:31], v[194:201], v[80:83], v173, v173 op_sel_hi:[0,0,0]
	v_mfma_scale_f32_16x16x128_f8f6f4 v[68:71], v[16:23], v[210:217], v[68:71], v173, v173 op_sel_hi:[0,0,0]
	v_mfma_scale_f32_16x16x128_f8f6f4 v[64:67], v[24:31], v[210:217], v[64:67], v173, v173 op_sel_hi:[0,0,0]
	v_mfma_scale_f32_16x16x128_f8f6f4 v[52:55], v[16:23], v[218:225], v[52:55], v173, v173 op_sel_hi:[0,0,0]
	v_mfma_scale_f32_16x16x128_f8f6f4 v[48:51], v[24:31], v[218:225], v[48:51], v173, v173 op_sel_hi:[0,0,0]
	v_mfma_scale_f32_16x16x128_f8f6f4 v[36:39], v[16:23], v[226:233], v[36:39], v173, v173 op_sel_hi:[0,0,0]
	v_mfma_scale_f32_16x16x128_f8f6f4 v[32:35], v[24:31], v[226:233], v[32:35], v173, v173 op_sel_hi:[0,0,0]
	s_setprio 0
	s_barrier
	ds_read_b128 v[0:3], v178
	ds_read_b128 v[4:7], v179
	ds_read_b128 v[8:11], v186
	ds_read_b128 v[12:15], v187
	s_add_u32 s30, s28, 0x20000
	s_addc_u32 s31, s29, 0
	s_mov_b32 m0, s45
	ds_read_b128 v[16:19], v190 offset:32768
	ds_read_b128 v[24:27], v190 offset:34816
	ds_read_b128 v[20:23], v191 offset:32768
	ds_read_b128 v[28:31], v191 offset:34816
	ds_read_b128 v[194:197], v190 offset:36864
	ds_read_b128 v[210:213], v190 offset:38912
	ds_read_b128 v[198:201], v191 offset:36864
	ds_read_b128 v[214:217], v191 offset:38912
	s_nop 0
	global_load_lds_dwordx4 v166, s[30:31]
	s_mov_b32 m0, s46
	s_nop 0
	global_load_lds_dwordx4 v162, s[30:31]
	s_waitcnt lgkmcnt(8)
	s_barrier
	s_waitcnt lgkmcnt(0)
	s_setprio 1
	s_waitcnt lgkmcnt(0)
	v_mfma_scale_f32_16x16x128_f8f6f4 v[156:159], v[0:7], v[16:23], v[156:159], v173, v173 op_sel_hi:[0,0,0]
	v_mfma_scale_f32_16x16x128_f8f6f4 v[152:155], v[8:15], v[16:23], v[152:155], v173, v173 op_sel_hi:[0,0,0]
	v_mfma_scale_f32_16x16x128_f8f6f4 v[140:143], v[0:7], v[24:31], v[140:143], v173, v173 op_sel_hi:[0,0,0]
	v_mfma_scale_f32_16x16x128_f8f6f4 v[136:139], v[8:15], v[24:31], v[136:139], v173, v173 op_sel_hi:[0,0,0]
	v_mfma_scale_f32_16x16x128_f8f6f4 v[124:127], v[0:7], v[194:201], v[124:127], v173, v173 op_sel_hi:[0,0,0]
	v_mfma_scale_f32_16x16x128_f8f6f4 v[120:123], v[8:15], v[194:201], v[120:123], v173, v173 op_sel_hi:[0,0,0]
	v_mfma_scale_f32_16x16x128_f8f6f4 v[108:111], v[0:7], v[210:217], v[108:111], v173, v173 op_sel_hi:[0,0,0]
	v_mfma_scale_f32_16x16x128_f8f6f4 v[104:107], v[8:15], v[210:217], v[104:107], v173, v173 op_sel_hi:[0,0,0]
	s_setprio 0
	s_barrier
	s_add_u32 s30, s26, 0x80
	s_addc_u32 s31, s27, 0
	s_mov_b32 m0, s48
	ds_read_b128 v[218:221], v180
	ds_read_b128 v[222:225], v181
	ds_read_b128 v[226:229], v188
	ds_read_b128 v[230:233], v189
	s_nop 0
	global_load_lds_dwordx4 v164, s[30:31]
	s_mov_b32 m0, s49
	s_nop 0
	global_load_lds_dwordx4 v160, s[30:31]
	s_barrier
	s_waitcnt lgkmcnt(0)
	s_setprio 1
	s_waitcnt lgkmcnt(0)
	v_mfma_scale_f32_16x16x128_f8f6f4 v[148:151], v[218:225], v[16:23], v[148:151], v173, v173 op_sel_hi:[0,0,0]
	v_mfma_scale_f32_16x16x128_f8f6f4 v[144:147], v[226:233], v[16:23], v[144:147], v173, v173 op_sel_hi:[0,0,0]
	v_mfma_scale_f32_16x16x128_f8f6f4 v[132:135], v[218:225], v[24:31], v[132:135], v173, v173 op_sel_hi:[0,0,0]
	v_mfma_scale_f32_16x16x128_f8f6f4 v[128:131], v[226:233], v[24:31], v[128:131], v173, v173 op_sel_hi:[0,0,0]
	v_mfma_scale_f32_16x16x128_f8f6f4 v[116:119], v[218:225], v[194:201], v[116:119], v173, v173 op_sel_hi:[0,0,0]
	v_mfma_scale_f32_16x16x128_f8f6f4 v[112:115], v[226:233], v[194:201], v[112:115], v173, v173 op_sel_hi:[0,0,0]
	v_mfma_scale_f32_16x16x128_f8f6f4 v[100:103], v[218:225], v[210:217], v[100:103], v173, v173 op_sel_hi:[0,0,0]
	v_mfma_scale_f32_16x16x128_f8f6f4 v[96:99], v[226:233], v[210:217], v[96:99], v173, v173 op_sel_hi:[0,0,0]
	s_setprio 0
	s_add_u32 s28, s28, 0x80
	s_addc_u32 s29, s29, 0
	s_mov_b32 m0, s50
	s_barrier
	ds_read_b128 v[16:19], v190 offset:49152
	ds_read_b128 v[24:27], v190 offset:51200
	ds_read_b128 v[20:23], v191 offset:49152
	ds_read_b128 v[28:31], v191 offset:51200
	ds_read_b128 v[194:197], v190 offset:53248
	ds_read_b128 v[210:213], v190 offset:55296
	ds_read_b128 v[198:201], v191 offset:53248
	ds_read_b128 v[214:217], v191 offset:55296
	s_nop 0
	global_load_lds_dwordx4 v166, s[28:29]
	s_mov_b32 m0, s51
	s_nop 0
	global_load_lds_dwordx4 v162, s[28:29]
	s_barrier
	s_waitcnt lgkmcnt(0)
	s_setprio 1
	s_waitcnt lgkmcnt(0)
	v_mfma_scale_f32_16x16x128_f8f6f4 v[92:95], v[0:7], v[16:23], v[92:95], v173, v173 op_sel_hi:[0,0,0]
	v_mfma_scale_f32_16x16x128_f8f6f4 v[88:91], v[8:15], v[16:23], v[88:91], v173, v173 op_sel_hi:[0,0,0]
	v_mfma_scale_f32_16x16x128_f8f6f4 v[76:79], v[0:7], v[24:31], v[76:79], v173, v173 op_sel_hi:[0,0,0]
	v_mfma_scale_f32_16x16x128_f8f6f4 v[72:75], v[8:15], v[24:31], v[72:75], v173, v173 op_sel_hi:[0,0,0]
	v_mfma_scale_f32_16x16x128_f8f6f4 v[60:63], v[0:7], v[194:201], v[60:63], v173, v173 op_sel_hi:[0,0,0]
	v_mfma_scale_f32_16x16x128_f8f6f4 v[56:59], v[8:15], v[194:201], v[56:59], v173, v173 op_sel_hi:[0,0,0]
	v_mfma_scale_f32_16x16x128_f8f6f4 v[44:47], v[0:7], v[210:217], v[44:47], v173, v173 op_sel_hi:[0,0,0]
	v_mfma_scale_f32_16x16x128_f8f6f4 v[40:43], v[8:15], v[210:217], v[40:43], v173, v173 op_sel_hi:[0,0,0]
	s_setprio 0
	s_barrier
	s_add_u32 s26, s26, 0x20080
	s_addc_u32 s27, s27, 0
	s_mov_b32 m0, s52
	s_nop 0
	global_load_lds_dwordx4 v164, s[26:27]
	s_mov_b32 m0, s53
	s_nop 0
	global_load_lds_dwordx4 v160, s[26:27]
	s_waitcnt vmcnt(6)
	s_barrier
	s_setprio 1
	v_mfma_scale_f32_16x16x128_f8f6f4 v[84:87], v[218:225], v[16:23], v[84:87], v173, v173 op_sel_hi:[0,0,0]
	v_mfma_scale_f32_16x16x128_f8f6f4 v[80:83], v[226:233], v[16:23], v[80:83], v173, v173 op_sel_hi:[0,0,0]
	v_mfma_scale_f32_16x16x128_f8f6f4 v[68:71], v[218:225], v[24:31], v[68:71], v173, v173 op_sel_hi:[0,0,0]
	v_mfma_scale_f32_16x16x128_f8f6f4 v[64:67], v[226:233], v[24:31], v[64:67], v173, v173 op_sel_hi:[0,0,0]
	v_mfma_scale_f32_16x16x128_f8f6f4 v[52:55], v[218:225], v[194:201], v[52:55], v173, v173 op_sel_hi:[0,0,0]
	v_mfma_scale_f32_16x16x128_f8f6f4 v[48:51], v[226:233], v[194:201], v[48:51], v173, v173 op_sel_hi:[0,0,0]
	v_mfma_scale_f32_16x16x128_f8f6f4 v[36:39], v[218:225], v[210:217], v[36:39], v173, v173 op_sel_hi:[0,0,0]
	v_mfma_scale_f32_16x16x128_f8f6f4 v[32:35], v[226:233], v[210:217], v[32:35], v173, v173 op_sel_hi:[0,0,0]
	s_setprio 0
	s_add_i32 s33, s33, 2
	s_cmp_gt_u32 s33, 5
	s_mov_b64 s[28:29], s[24:25]
	s_barrier
	s_cbranch_scc0 .LBB0_2059
	v_mov_b32_e32 v0, v172
	s_nop 15
	s_nop 15
	s_ashr_i32 s2, s0, 31
	v_ashrrev_i32_e32 v1, 2, v0
	v_and_b32_e32 v1, 0xffffffc0, v1
	v_lshl_add_u32 v1, s22, 8, v1
	v_and_or_b32 v6, v0, 15, v1
	v_ashrrev_i32_e32 v7, 31, v6
	v_lshl_add_u64 v[2:3], v[6:7], 2, s[8:9]
	global_load_dword v14, v[2:3], off
	global_load_dword v194, v[2:3], off offset:64
	global_load_dword v195, v[2:3], off offset:128
	global_load_dword v196, v[2:3], off offset:192
	global_load_dword v197, v[2:3], off offset:512
	global_load_dword v198, v[2:3], off offset:576
	global_load_dword v199, v[2:3], off offset:640
	global_load_dword v200, v[2:3], off offset:704
	s_lshr_b32 s2, s2, 30
	s_add_i32 s2, s0, s2
	v_lshrrev_b32_e32 v0, 1, v0
	s_and_b32 s2, s2, 0xfffffc
	v_and_b32_e32 v0, 0x78, v0
	s_sub_i32 s0, s0, s2
	v_lshl_or_b32 v4, s0, 8, v0
	v_lshlrev_b64 v[0:1], 10, v[6:7]
	v_mov_b32_e32 v8, 0
	v_mov_b32_e32 v9, 0
	v_mov_b32_e32 v10, 0
	v_mov_b32_e32 v11, 0
	v_ashrrev_i32_e32 v5, 31, v4
	v_or_b32_e32 v12, 16, v6
	v_lshl_add_u64 v[0:1], s[10:11], 0, v[0:1]
	v_ashrrev_i32_e32 v13, 31, v12
	v_lshl_add_u64 v[0:1], v[0:1], 0, v[4:5]
	s_mov_b32 s0, 0x20000
	s_mov_b64 s[2:3], 0x20000
	s_mov_b64 s[4:5], s[6:7]
	s_mov_b64 s[6:7], 0x2c000
	s_mov_b32 s13, 0x2c000
	s_mov_b32 s22, s12
	s_waitcnt vmcnt(0)
	v_mul_f32_e32 v7, 0x3d000000, v14
	v_mul_f32_e32 v14, 0x42000000, v7
	v_pk_mul_f32 v[18:19], v[156:157], v[14:15] op_sel_hi:[1,0]
	v_pk_mul_f32 v[22:23], v[152:153], v[14:15] op_sel_hi:[1,0]
	v_pk_mul_f32 v[16:17], v[158:159], v[14:15] op_sel_hi:[1,0]
	v_pk_mul_f32 v[20:21], v[154:155], v[14:15] op_sel_hi:[1,0]
	v_pk_mul_f32 v[24:25], v[150:151], v[14:15] op_sel_hi:[1,0]
	v_pk_mul_f32 v[26:27], v[148:149], v[14:15] op_sel_hi:[1,0]
	v_pk_mul_f32 v[28:29], v[146:147], v[14:15] op_sel_hi:[1,0]
	v_pk_mul_f32 v[14:15], v[144:145], v[14:15] op_sel_hi:[1,0]
	v_med3_f32 v7, v18, s55, v192
	v_med3_f32 v18, v22, s55, v192
	v_med3_f32 v19, v19, s55, v192
	v_med3_f32 v22, v23, s55, v192
	v_med3_f32 v23, v26, s55, v192
	v_med3_f32 v14, v14, s55, v192
	v_med3_f32 v26, v27, s55, v192
	v_med3_f32 v15, v15, s55, v192
	v_cvt_pk_fp8_f32 v8, v7, v19
	v_cvt_pk_fp8_f32 v9, v18, v22
	v_cvt_pk_fp8_f32 v10, v23, v26
	v_cvt_pk_fp8_f32 v11, v14, v15
	v_med3_f32 v16, v16, s55, v192
	v_med3_f32 v20, v20, s55, v192
	v_med3_f32 v17, v17, s55, v192
	v_med3_f32 v21, v21, s55, v192
	v_med3_f32 v24, v24, s55, v192
	v_med3_f32 v27, v28, s55, v192
	v_med3_f32 v25, v25, s55, v192
	v_med3_f32 v28, v29, s55, v192
	v_cvt_pk_fp8_f32 v8, v16, v17 op_sel:[0,0,1]
	v_cvt_pk_fp8_f32 v9, v20, v21 op_sel:[0,0,1]
	v_cvt_pk_fp8_f32 v10, v24, v25 op_sel:[0,0,1]
	v_cvt_pk_fp8_f32 v11, v27, v28 op_sel:[0,0,1]
	v_lshl_add_u64 v[14:15], v[12:13], 2, s[8:9]
	global_store_dwordx2 v[0:1], v[8:9], off
	global_store_dwordx2 v[0:1], v[10:11], off offset:128
	v_mov_b32_e32 v8, 0
	v_mov_b32_e32 v9, 0
	v_mov_b32_e32 v10, 0
	v_mov_b32_e32 v11, 0
	v_lshlrev_b64 v[12:13], 10, v[12:13]
	v_or_b32_e32 v14, 32, v6
	v_lshl_add_u64 v[12:13], s[10:11], 0, v[12:13]
	v_ashrrev_i32_e32 v15, 31, v14
	v_lshl_add_u64 v[12:13], v[12:13], 0, v[4:5]
	v_lshl_add_u64 v[16:17], v[14:15], 2, s[8:9]
	v_or_b32_e32 v6, 48, v6
	v_mul_f32_e32 v7, 0x3d000000, v194
	v_mul_f32_e32 v18, 0x42000000, v7
	v_pk_mul_f32 v[22:23], v[140:141], v[18:19] op_sel_hi:[1,0]
	v_pk_mul_f32 v[26:27], v[136:137], v[18:19] op_sel_hi:[1,0]
	v_pk_mul_f32 v[20:21], v[142:143], v[18:19] op_sel_hi:[1,0]
	v_pk_mul_f32 v[24:25], v[138:139], v[18:19] op_sel_hi:[1,0]
	v_pk_mul_f32 v[28:29], v[134:135], v[18:19] op_sel_hi:[1,0]
	v_pk_mul_f32 v[30:31], v[132:133], v[18:19] op_sel_hi:[1,0]
	v_pk_mul_f32 v[130:131], v[130:131], v[18:19] op_sel_hi:[1,0]
	v_pk_mul_f32 v[18:19], v[128:129], v[18:19] op_sel_hi:[1,0]
	v_med3_f32 v7, v22, s55, v192
	v_med3_f32 v22, v26, s55, v192
	v_med3_f32 v23, v23, s55, v192
	v_med3_f32 v26, v27, s55, v192
	v_med3_f32 v27, v30, s55, v192
	v_med3_f32 v18, v18, s55, v192
	v_med3_f32 v30, v31, s55, v192
	v_med3_f32 v19, v19, s55, v192
	v_cvt_pk_fp8_f32 v8, v7, v23
	v_cvt_pk_fp8_f32 v9, v22, v26
	v_cvt_pk_fp8_f32 v10, v27, v30
	v_cvt_pk_fp8_f32 v11, v18, v19
	v_med3_f32 v20, v20, s55, v192
	v_med3_f32 v24, v24, s55, v192
	v_med3_f32 v21, v21, s55, v192
	v_med3_f32 v25, v25, s55, v192
	v_med3_f32 v28, v28, s55, v192
	v_med3_f32 v31, v130, s55, v192
	v_med3_f32 v29, v29, s55, v192
	v_med3_f32 v128, v131, s55, v192
	v_cvt_pk_fp8_f32 v8, v20, v21 op_sel:[0,0,1]
	v_cvt_pk_fp8_f32 v9, v24, v25 op_sel:[0,0,1]
	v_cvt_pk_fp8_f32 v10, v28, v29 op_sel:[0,0,1]
	v_cvt_pk_fp8_f32 v11, v31, v128 op_sel:[0,0,1]
	global_store_dwordx2 v[12:13], v[8:9], off
	global_store_dwordx2 v[12:13], v[10:11], off offset:128
	v_mov_b32_e32 v8, 0
	v_mov_b32_e32 v9, 0
	v_mov_b32_e32 v10, 0
	v_mov_b32_e32 v11, 0
	v_lshlrev_b64 v[12:13], 10, v[14:15]
	v_lshl_add_u64 v[12:13], s[10:11], 0, v[12:13]
	v_ashrrev_i32_e32 v7, 31, v6
	v_lshl_add_u64 v[12:13], v[12:13], 0, v[4:5]
	v_lshl_add_u64 v[14:15], v[6:7], 2, s[8:9]
	v_lshlrev_b64 v[6:7], 10, v[6:7]
	v_lshl_add_u64 v[6:7], s[10:11], 0, v[6:7]
	v_lshl_add_u64 v[4:5], v[6:7], 0, v[4:5]
	v_mov_b32_e32 v6, 0
	v_mov_b32_e32 v7, 0
	v_mul_f32_e32 v16, 0x3d000000, v195
	v_mul_f32_e32 v16, 0x42000000, v16
	v_pk_mul_f32 v[20:21], v[124:125], v[16:17] op_sel_hi:[1,0]
	v_pk_mul_f32 v[24:25], v[120:121], v[16:17] op_sel_hi:[1,0]
	v_pk_mul_f32 v[18:19], v[126:127], v[16:17] op_sel_hi:[1,0]
	v_pk_mul_f32 v[22:23], v[122:123], v[16:17] op_sel_hi:[1,0]
	v_pk_mul_f32 v[26:27], v[118:119], v[16:17] op_sel_hi:[1,0]
	v_pk_mul_f32 v[28:29], v[116:117], v[16:17] op_sel_hi:[1,0]
	v_pk_mul_f32 v[30:31], v[114:115], v[16:17] op_sel_hi:[1,0]
	v_pk_mul_f32 v[16:17], v[112:113], v[16:17] op_sel_hi:[1,0]
	v_med3_f32 v20, v20, s55, v192
	v_med3_f32 v24, v24, s55, v192
	v_med3_f32 v21, v21, s55, v192
	v_med3_f32 v25, v25, s55, v192
	v_med3_f32 v28, v28, s55, v192
	v_med3_f32 v16, v16, s55, v192
	v_med3_f32 v29, v29, s55, v192
	v_med3_f32 v17, v17, s55, v192
	v_cvt_pk_fp8_f32 v8, v20, v21
	v_cvt_pk_fp8_f32 v9, v24, v25
	v_cvt_pk_fp8_f32 v10, v28, v29
	v_cvt_pk_fp8_f32 v11, v16, v17
	v_med3_f32 v18, v18, s55, v192
	v_med3_f32 v22, v22, s55, v192
	v_med3_f32 v19, v19, s55, v192
	v_med3_f32 v23, v23, s55, v192
	v_med3_f32 v26, v26, s55, v192
	v_med3_f32 v30, v30, s55, v192
	v_med3_f32 v27, v27, s55, v192
	v_med3_f32 v31, v31, s55, v192
	v_cvt_pk_fp8_f32 v8, v18, v19 op_sel:[0,0,1]
	v_cvt_pk_fp8_f32 v9, v22, v23 op_sel:[0,0,1]
	v_cvt_pk_fp8_f32 v10, v26, v27 op_sel:[0,0,1]
	v_cvt_pk_fp8_f32 v11, v30, v31 op_sel:[0,0,1]
	global_store_dwordx2 v[12:13], v[8:9], off
	global_store_dwordx2 v[12:13], v[10:11], off offset:128
	v_mov_b32_e32 v8, 0
	v_mov_b32_e32 v9, 0
	v_mov_b32_e32 v10, 0
	v_mov_b32_e32 v11, 0
	v_mul_f32_e32 v12, 0x3d000000, v196
	v_mul_f32_e32 v12, 0x42000000, v12
	v_pk_mul_f32 v[16:17], v[108:109], v[12:13] op_sel_hi:[1,0]
	v_pk_mul_f32 v[20:21], v[104:105], v[12:13] op_sel_hi:[1,0]
	v_pk_mul_f32 v[14:15], v[110:111], v[12:13] op_sel_hi:[1,0]
	v_pk_mul_f32 v[18:19], v[106:107], v[12:13] op_sel_hi:[1,0]
	v_pk_mul_f32 v[22:23], v[102:103], v[12:13] op_sel_hi:[1,0]
	v_pk_mul_f32 v[24:25], v[100:101], v[12:13] op_sel_hi:[1,0]
	v_pk_mul_f32 v[26:27], v[98:99], v[12:13] op_sel_hi:[1,0]
	v_pk_mul_f32 v[12:13], v[96:97], v[12:13] op_sel_hi:[1,0]
	v_med3_f32 v16, v16, s55, v192
	v_med3_f32 v20, v20, s55, v192
	v_med3_f32 v17, v17, s55, v192
	v_med3_f32 v21, v21, s55, v192
	v_med3_f32 v24, v24, s55, v192
	v_med3_f32 v12, v12, s55, v192
	v_med3_f32 v25, v25, s55, v192
	v_med3_f32 v13, v13, s55, v192
	v_cvt_pk_fp8_f32 v8, v16, v17
	v_cvt_pk_fp8_f32 v9, v20, v21
	v_cvt_pk_fp8_f32 v10, v24, v25
	v_cvt_pk_fp8_f32 v11, v12, v13
	v_med3_f32 v14, v14, s55, v192
	v_med3_f32 v18, v18, s55, v192
	v_med3_f32 v15, v15, s55, v192
	v_med3_f32 v19, v19, s55, v192
	v_med3_f32 v22, v22, s55, v192
	v_med3_f32 v26, v26, s55, v192
	v_med3_f32 v23, v23, s55, v192
	v_med3_f32 v27, v27, s55, v192
	v_cvt_pk_fp8_f32 v8, v14, v15 op_sel:[0,0,1]
	v_cvt_pk_fp8_f32 v9, v18, v19 op_sel:[0,0,1]
	v_cvt_pk_fp8_f32 v10, v22, v23 op_sel:[0,0,1]
	v_cvt_pk_fp8_f32 v11, v26, v27 op_sel:[0,0,1]
	global_store_dwordx2 v[4:5], v[8:9], off
	global_store_dwordx2 v[4:5], v[10:11], off offset:128
	v_mov_b32_e32 v4, 0
	v_mov_b32_e32 v5, 0
	v_lshl_add_u64 v[8:9], v[0:1], 0, s[2:3]
	s_mov_b64 s[2:3], 0x24000
	v_mul_f32_e32 v10, 0x3d000000, v197
	v_mul_f32_e32 v10, 0x42000000, v10
	v_pk_mul_f32 v[14:15], v[92:93], v[10:11] op_sel_hi:[1,0]
	v_pk_mul_f32 v[18:19], v[88:89], v[10:11] op_sel_hi:[1,0]
	v_pk_mul_f32 v[12:13], v[94:95], v[10:11] op_sel_hi:[1,0]
	v_pk_mul_f32 v[16:17], v[90:91], v[10:11] op_sel_hi:[1,0]
	v_pk_mul_f32 v[20:21], v[86:87], v[10:11] op_sel_hi:[1,0]
	v_pk_mul_f32 v[22:23], v[84:85], v[10:11] op_sel_hi:[1,0]
	v_pk_mul_f32 v[24:25], v[82:83], v[10:11] op_sel_hi:[1,0]
	v_pk_mul_f32 v[10:11], v[80:81], v[10:11] op_sel_hi:[1,0]
	v_med3_f32 v14, v14, s55, v192
	v_med3_f32 v18, v18, s55, v192
	v_med3_f32 v15, v15, s55, v192
	v_med3_f32 v19, v19, s55, v192
	v_med3_f32 v22, v22, s55, v192
	v_med3_f32 v10, v10, s55, v192
	v_med3_f32 v23, v23, s55, v192
	v_med3_f32 v11, v11, s55, v192
	v_cvt_pk_fp8_f32 v4, v14, v15
	v_cvt_pk_fp8_f32 v5, v18, v19
	v_cvt_pk_fp8_f32 v6, v22, v23
	v_cvt_pk_fp8_f32 v7, v10, v11
	v_med3_f32 v12, v12, s55, v192
	v_med3_f32 v16, v16, s55, v192
	v_med3_f32 v13, v13, s55, v192
	v_med3_f32 v17, v17, s55, v192
	v_med3_f32 v20, v20, s55, v192
	v_med3_f32 v24, v24, s55, v192
	v_med3_f32 v21, v21, s55, v192
	v_med3_f32 v25, v25, s55, v192
	v_cvt_pk_fp8_f32 v4, v12, v13 op_sel:[0,0,1]
	v_cvt_pk_fp8_f32 v5, v16, v17 op_sel:[0,0,1]
	v_cvt_pk_fp8_f32 v6, v20, v21 op_sel:[0,0,1]
	v_cvt_pk_fp8_f32 v7, v24, v25 op_sel:[0,0,1]
	v_add_co_u32_e32 v10, vcc, s0, v0
	s_mov_b32 s0, 0x24000
	s_nop 0
	v_addc_co_u32_e32 v11, vcc, 0, v1, vcc
	global_store_dwordx2 v[10:11], v[4:5], off
	global_store_dwordx2 v[8:9], v[6:7], off offset:128
	v_mov_b32_e32 v4, 0
	v_mov_b32_e32 v5, 0
	v_mov_b32_e32 v6, 0
	v_mov_b32_e32 v7, 0
	v_lshl_add_u64 v[8:9], v[0:1], 0, s[2:3]
	s_mov_b64 s[2:3], 0x28000
	v_mul_f32_e32 v10, 0x3d000000, v198
	v_mul_f32_e32 v10, 0x42000000, v10
	v_pk_mul_f32 v[14:15], v[76:77], v[10:11] op_sel_hi:[1,0]
	v_pk_mul_f32 v[18:19], v[72:73], v[10:11] op_sel_hi:[1,0]
	v_pk_mul_f32 v[12:13], v[78:79], v[10:11] op_sel_hi:[1,0]
	v_pk_mul_f32 v[16:17], v[74:75], v[10:11] op_sel_hi:[1,0]
	v_pk_mul_f32 v[20:21], v[70:71], v[10:11] op_sel_hi:[1,0]
	v_pk_mul_f32 v[22:23], v[68:69], v[10:11] op_sel_hi:[1,0]
	v_pk_mul_f32 v[24:25], v[66:67], v[10:11] op_sel_hi:[1,0]
	v_pk_mul_f32 v[10:11], v[64:65], v[10:11] op_sel_hi:[1,0]
	v_med3_f32 v14, v14, s55, v192
	v_med3_f32 v18, v18, s55, v192
	v_med3_f32 v15, v15, s55, v192
	v_med3_f32 v19, v19, s55, v192
	v_med3_f32 v22, v22, s55, v192
	v_med3_f32 v10, v10, s55, v192
	v_med3_f32 v23, v23, s55, v192
	v_med3_f32 v11, v11, s55, v192
	v_cvt_pk_fp8_f32 v4, v14, v15
	v_cvt_pk_fp8_f32 v5, v18, v19
	v_cvt_pk_fp8_f32 v6, v22, v23
	v_cvt_pk_fp8_f32 v7, v10, v11
	v_med3_f32 v12, v12, s55, v192
	v_med3_f32 v16, v16, s55, v192
	v_med3_f32 v13, v13, s55, v192
	v_med3_f32 v17, v17, s55, v192
	v_med3_f32 v20, v20, s55, v192
	v_med3_f32 v24, v24, s55, v192
	v_med3_f32 v21, v21, s55, v192
	v_med3_f32 v25, v25, s55, v192
	v_cvt_pk_fp8_f32 v4, v12, v13 op_sel:[0,0,1]
	v_cvt_pk_fp8_f32 v5, v16, v17 op_sel:[0,0,1]
	v_cvt_pk_fp8_f32 v6, v20, v21 op_sel:[0,0,1]
	v_cvt_pk_fp8_f32 v7, v24, v25 op_sel:[0,0,1]
	v_add_co_u32_e32 v10, vcc, s0, v0
	s_mov_b32 s0, 0x28000
	s_nop 0
	v_addc_co_u32_e32 v11, vcc, 0, v1, vcc
	global_store_dwordx2 v[10:11], v[4:5], off
	global_store_dwordx2 v[8:9], v[6:7], off offset:128
	v_mov_b32_e32 v4, 0
	v_mov_b32_e32 v5, 0
	v_mov_b32_e32 v6, 0
	v_mov_b32_e32 v7, 0
	v_lshl_add_u64 v[8:9], v[0:1], 0, s[2:3]
	s_mov_b64 s[2:3], s[20:21]
	v_mul_f32_e32 v10, 0x3d000000, v199
	v_mul_f32_e32 v10, 0x42000000, v10
	v_pk_mul_f32 v[14:15], v[60:61], v[10:11] op_sel_hi:[1,0]
	v_pk_mul_f32 v[18:19], v[56:57], v[10:11] op_sel_hi:[1,0]
	v_pk_mul_f32 v[12:13], v[62:63], v[10:11] op_sel_hi:[1,0]
	v_pk_mul_f32 v[16:17], v[58:59], v[10:11] op_sel_hi:[1,0]
	v_pk_mul_f32 v[20:21], v[54:55], v[10:11] op_sel_hi:[1,0]
	v_pk_mul_f32 v[22:23], v[52:53], v[10:11] op_sel_hi:[1,0]
	v_pk_mul_f32 v[24:25], v[50:51], v[10:11] op_sel_hi:[1,0]
	v_pk_mul_f32 v[10:11], v[48:49], v[10:11] op_sel_hi:[1,0]
	v_med3_f32 v14, v14, s55, v192
	v_med3_f32 v18, v18, s55, v192
	v_med3_f32 v15, v15, s55, v192
	v_med3_f32 v19, v19, s55, v192
	v_med3_f32 v22, v22, s55, v192
	v_med3_f32 v10, v10, s55, v192
	v_med3_f32 v23, v23, s55, v192
	v_med3_f32 v11, v11, s55, v192
	v_cvt_pk_fp8_f32 v4, v14, v15
	v_cvt_pk_fp8_f32 v5, v18, v19
	v_cvt_pk_fp8_f32 v6, v22, v23
	v_cvt_pk_fp8_f32 v7, v10, v11
	v_med3_f32 v12, v12, s55, v192
	v_med3_f32 v16, v16, s55, v192
	v_med3_f32 v13, v13, s55, v192
	v_med3_f32 v17, v17, s55, v192
	v_med3_f32 v20, v20, s55, v192
	v_med3_f32 v24, v24, s55, v192
	v_med3_f32 v21, v21, s55, v192
	v_med3_f32 v25, v25, s55, v192
	v_cvt_pk_fp8_f32 v4, v12, v13 op_sel:[0,0,1]
	v_cvt_pk_fp8_f32 v5, v16, v17 op_sel:[0,0,1]
	v_cvt_pk_fp8_f32 v6, v20, v21 op_sel:[0,0,1]
	v_cvt_pk_fp8_f32 v7, v24, v25 op_sel:[0,0,1]
	v_add_co_u32_e32 v10, vcc, s0, v0
	s_mov_b32 s0, s18
	s_nop 0
	v_addc_co_u32_e32 v11, vcc, 0, v1, vcc
	global_store_dwordx2 v[10:11], v[4:5], off
	global_store_dwordx2 v[8:9], v[6:7], off offset:128
	v_mov_b32_e32 v2, 0
	v_mov_b32_e32 v3, 0
	v_mov_b32_e32 v4, 0
	v_mov_b32_e32 v5, 0
	v_lshl_add_u64 v[6:7], v[0:1], 0, s[6:7]
	v_add_co_u32_e64 v0, s[6:7], s13, v0
	s_and_b64 vcc, exec, s[14:15]
	s_nop 0
	v_addc_co_u32_e64 v1, s[6:7], 0, v1, s[6:7]
	v_mul_f32_e32 v8, 0x3d000000, v200
	v_mul_f32_e32 v8, 0x42000000, v8
	v_pk_mul_f32 v[12:13], v[44:45], v[8:9] op_sel_hi:[1,0]
	v_pk_mul_f32 v[16:17], v[40:41], v[8:9] op_sel_hi:[1,0]
	v_pk_mul_f32 v[10:11], v[46:47], v[8:9] op_sel_hi:[1,0]
	v_pk_mul_f32 v[14:15], v[42:43], v[8:9] op_sel_hi:[1,0]
	v_pk_mul_f32 v[18:19], v[38:39], v[8:9] op_sel_hi:[1,0]
	v_pk_mul_f32 v[20:21], v[36:37], v[8:9] op_sel_hi:[1,0]
	v_pk_mul_f32 v[22:23], v[34:35], v[8:9] op_sel_hi:[1,0]
	v_pk_mul_f32 v[8:9], v[32:33], v[8:9] op_sel_hi:[1,0]
	v_med3_f32 v12, v12, s55, v192
	v_med3_f32 v16, v16, s55, v192
	v_med3_f32 v13, v13, s55, v192
	v_med3_f32 v17, v17, s55, v192
	v_med3_f32 v20, v20, s55, v192
	v_med3_f32 v8, v8, s55, v192
	v_med3_f32 v21, v21, s55, v192
	v_med3_f32 v9, v9, s55, v192
	v_cvt_pk_fp8_f32 v2, v12, v13
	v_cvt_pk_fp8_f32 v3, v16, v17
	v_cvt_pk_fp8_f32 v4, v20, v21
	v_cvt_pk_fp8_f32 v5, v8, v9
	v_med3_f32 v10, v10, s55, v192
	v_med3_f32 v14, v14, s55, v192
	v_med3_f32 v11, v11, s55, v192
	v_med3_f32 v15, v15, s55, v192
	v_med3_f32 v18, v18, s55, v192
	v_med3_f32 v22, v22, s55, v192
	v_med3_f32 v19, v19, s55, v192
	v_med3_f32 v23, v23, s55, v192
	v_cvt_pk_fp8_f32 v2, v10, v11 op_sel:[0,0,1]
	v_cvt_pk_fp8_f32 v3, v14, v15 op_sel:[0,0,1]
	v_cvt_pk_fp8_f32 v4, v18, v19 op_sel:[0,0,1]
	v_cvt_pk_fp8_f32 v5, v22, v23 op_sel:[0,0,1]
	global_store_dwordx2 v[0:1], v[2:3], off
	global_store_dwordx2 v[6:7], v[4:5], off offset:128
	s_cbranch_vccz .LBB0_2056
	s_waitcnt vmcnt(0)
	v_readlane_b32 s54, v242, 34
	s_cmpk_gt_u32 s34, 0xff
	v_readlane_b32 s55, v242, 35
	s_cbranch_scc1 .LBB0_2063
	s_barrier

.LBB0_2199:
	s_ashr_i32 s23, s22, 31
	s_lshl_b64 s[24:25], s[22:23], 19
	s_add_u32 s24, s38, s24
	s_addc_u32 s25, s39, s25
	s_ashr_i32 s21, s20, 31
	s_lshl_b64 s[26:27], s[20:21], 19
	s_add_u32 s26, s40, s26
	s_addc_u32 s27, s41, s27
	s_and_b64 s[28:29], s[16:17], exec
	v_mov_b32_e32 v0, 0
	s_cselect_b32 s21, s27, s13
	s_cselect_b32 s23, s26, s12
	s_mov_b32 s61, -2
	s_mov_b64 s[28:29], 0
	v_mov_b32_e32 v1, 0
	v_mov_b64_e32 v[2:3], 0
	v_mov_b64_e32 v[4:5], 0
	v_mov_b64_e32 v[6:7], 0
	v_mov_b64_e32 v[8:9], 0
	v_mov_b64_e32 v[10:11], 0
	v_mov_b64_e32 v[12:13], 0
	v_mov_b64_e32 v[14:15], 0
	v_mov_b64_e32 v[16:17], 0
	v_mov_b64_e32 v[18:19], 0
	v_mov_b64_e32 v[20:21], 0
	v_mov_b64_e32 v[22:23], 0
	v_mov_b64_e32 v[24:25], 0
	v_mov_b64_e32 v[26:27], 0
	v_mov_b64_e32 v[28:29], 0
	v_mov_b64_e32 v[30:31], 0
	v_mov_b64_e32 v[32:33], 0
	v_mov_b64_e32 v[34:35], 0
	v_mov_b64_e32 v[36:37], 0
	v_mov_b64_e32 v[38:39], 0
	v_mov_b64_e32 v[40:41], 0
	v_mov_b64_e32 v[42:43], 0
	v_mov_b64_e32 v[44:45], 0
	v_mov_b64_e32 v[46:47], 0
	v_mov_b64_e32 v[48:49], 0
	v_mov_b64_e32 v[50:51], 0
	v_mov_b64_e32 v[52:53], 0
	v_mov_b64_e32 v[54:55], 0
	v_mov_b64_e32 v[56:57], 0
	v_mov_b64_e32 v[58:59], 0
	v_mov_b64_e32 v[60:61], 0
	v_mov_b64_e32 v[62:63], 0
	v_mov_b64_e32 v[64:65], 0
	v_mov_b64_e32 v[66:67], 0
	v_mov_b64_e32 v[68:69], 0
	v_mov_b64_e32 v[70:71], 0
	v_mov_b64_e32 v[72:73], 0
	v_mov_b64_e32 v[74:75], 0
	v_mov_b64_e32 v[76:77], 0
	v_mov_b64_e32 v[78:79], 0
	v_mov_b64_e32 v[80:81], 0
	v_mov_b64_e32 v[82:83], 0
	v_mov_b64_e32 v[84:85], 0
	v_mov_b64_e32 v[86:87], 0
	v_mov_b64_e32 v[88:89], 0
	v_mov_b64_e32 v[90:91], 0
	v_mov_b64_e32 v[92:93], 0
	v_mov_b64_e32 v[94:95], 0
	v_mov_b64_e32 v[96:97], 0
	v_mov_b64_e32 v[98:99], 0
	v_mov_b64_e32 v[100:101], 0
	v_mov_b64_e32 v[102:103], 0
	v_mov_b64_e32 v[104:105], 0
	v_mov_b64_e32 v[106:107], 0
	v_mov_b64_e32 v[108:109], 0
	v_mov_b64_e32 v[110:111], 0
	v_mov_b64_e32 v[112:113], 0
	v_mov_b64_e32 v[114:115], 0
	v_mov_b64_e32 v[116:117], 0
	v_mov_b64_e32 v[118:119], 0
	v_mov_b64_e32 v[120:121], 0
	v_mov_b64_e32 v[122:123], 0
	v_mov_b64_e32 v[124:125], 0
	v_mov_b64_e32 v[126:127], 0

.LBB0_2525:
	s_ashr_i32 s27, s26, 31
	s_lshl_b64 s[28:29], s[26:27], 19
	s_add_u32 s28, s43, s28
	s_addc_u32 s29, s44, s29
	s_ashr_i32 s25, s24, 31
	s_lshl_b64 s[30:31], s[24:25], 19
	s_add_u32 s30, s45, s30
	s_addc_u32 s31, s46, s31
	s_and_b64 s[34:35], s[14:15], exec
	v_mov_b32_e32 v0, 0
	s_cselect_b32 s1, s31, s3
	s_cselect_b32 s20, s30, s2
	s_mov_b32 s25, -2
	s_mov_b64 s[34:35], 0
	s_waitcnt lgkmcnt(0)
	v_mov_b32_e32 v1, v0
	v_mov_b32_e32 v2, v0
	v_mov_b32_e32 v3, v0
	v_mov_b32_e32 v4, v0
	v_mov_b32_e32 v5, v0
	v_mov_b32_e32 v6, v0
	v_mov_b32_e32 v7, v0
	v_mov_b32_e32 v16, v0
	v_mov_b32_e32 v17, v0
	v_mov_b32_e32 v18, v0
	v_mov_b32_e32 v19, v0
	v_mov_b32_e32 v20, v0
	v_mov_b32_e32 v21, v0
	v_mov_b32_e32 v22, v0
	v_mov_b32_e32 v23, v0
	v_mov_b32_e32 v32, v0
	v_mov_b32_e32 v33, v0
	v_mov_b32_e32 v34, v0
	v_mov_b32_e32 v35, v0
	v_mov_b32_e32 v36, v0
	v_mov_b32_e32 v37, v0
	v_mov_b32_e32 v38, v0
	v_mov_b32_e32 v39, v0
	v_mov_b32_e32 v48, v0
	v_mov_b32_e32 v49, v0
	v_mov_b32_e32 v50, v0
	v_mov_b32_e32 v51, v0
	s_waitcnt vmcnt(0)
	v_mov_b64_e32 v[8:9], 0
	v_mov_b64_e32 v[10:11], 0
	v_mov_b64_e32 v[12:13], 0
	v_mov_b64_e32 v[14:15], 0
	v_mov_b64_e32 v[24:25], 0
	v_mov_b64_e32 v[26:27], 0
	v_mov_b64_e32 v[28:29], 0
	v_mov_b64_e32 v[30:31], 0
	v_mov_b64_e32 v[40:41], 0
	v_mov_b64_e32 v[42:43], 0
	v_mov_b64_e32 v[44:45], 0
	v_mov_b64_e32 v[46:47], 0
	v_mov_b64_e32 v[52:53], 0
	v_mov_b64_e32 v[54:55], 0
	v_mov_b64_e32 v[56:57], 0
	v_mov_b64_e32 v[58:59], 0
	v_mov_b64_e32 v[60:61], 0
	v_mov_b64_e32 v[62:63], 0
	v_mov_b64_e32 v[64:65], 0
	v_mov_b64_e32 v[66:67], 0
	v_mov_b64_e32 v[68:69], 0
	v_mov_b64_e32 v[70:71], 0
	v_mov_b64_e32 v[72:73], 0
	v_mov_b64_e32 v[74:75], 0
	v_mov_b64_e32 v[76:77], 0
	v_mov_b64_e32 v[78:79], 0
	v_mov_b64_e32 v[80:81], 0
	v_mov_b64_e32 v[82:83], 0
	v_mov_b64_e32 v[84:85], 0
	v_mov_b64_e32 v[86:87], 0
	v_mov_b64_e32 v[88:89], 0
	v_mov_b64_e32 v[90:91], 0
	v_mov_b64_e32 v[96:97], 0
	v_mov_b64_e32 v[98:99], 0
	v_mov_b64_e32 v[112:113], 0
	v_mov_b64_e32 v[114:115], 0
	v_mov_b64_e32 v[116:117], 0
	v_mov_b64_e32 v[118:119], 0
	v_mov_b64_e32 v[120:121], 0
	v_mov_b64_e32 v[122:123], 0
	v_mov_b64_e32 v[124:125], 0
	v_mov_b64_e32 v[126:127], 0
	v_mov_b64_e32 v[128:129], 0
	v_mov_b64_e32 v[130:131], 0
	v_mov_b64_e32 v[132:133], 0
	v_mov_b64_e32 v[134:135], 0
	v_mov_b64_e32 v[136:137], 0
	v_mov_b64_e32 v[138:139], 0
	v_mov_b64_e32 v[140:141], 0
	v_mov_b64_e32 v[142:143], 0

.LBB0_2958:
	v_mov_b32_e32 v0, v209
	s_nop 15
	s_nop 15
	s_mov_b32 s101, 0x44800000
	s_ashr_i32 s2, s0, 31
	v_ashrrev_i32_e32 v1, 2, v0
	v_and_b32_e32 v1, 0xffffffc0, v1
	v_lshl_add_u32 v1, s33, 8, v1
	v_and_or_b32 v4, v0, 15, v1
	v_lshrrev_b32_e32 v2, 1, v0
	s_lshr_b32 s2, s2, 29
	s_add_i32 s2, s0, s2
	s_and_b32 s2, s2, 0x1fffff8
	s_sub_i32 s0, s0, s2
	v_and_b32_e32 v2, 0x78, v2
	v_ashrrev_i32_e32 v5, 31, v4
	v_lshl_or_b32 v2, s0, 7, v2
	v_lshlrev_b64 v[0:1], 10, v[4:5]
	v_ashrrev_i32_e32 v3, 31, v2
	v_lshl_add_u64 v[0:1], s[8:9], 0, v[0:1]
	v_lshl_add_u64 v[0:1], v[0:1], 0, v[2:3]
	v_mul_f32_e32 v10, 0xbd38aa3b, v188
	v_mul_f32_e32 v11, 0xbd38aa3b, v189
	v_mul_f32_e32 v12, 0xbd38aa3b, v190
	v_mul_f32_e32 v13, 0xbd38aa3b, v191
	v_mul_f32_e32 v14, 0xbd38aa3b, v180
	v_mul_f32_e32 v15, 0xbd38aa3b, v181
	v_mul_f32_e32 v16, 0xbd38aa3b, v182
	v_mul_f32_e32 v17, 0xbd38aa3b, v183
	v_exp_f32_e32 v10, v10
	v_exp_f32_e32 v11, v11
	v_exp_f32_e32 v12, v12
	v_exp_f32_e32 v13, v13
	v_exp_f32_e32 v14, v14
	v_exp_f32_e32 v15, v15
	v_exp_f32_e32 v16, v16
	v_exp_f32_e32 v17, v17
	v_fma_f32 v10, v10, s101, s101
	v_fma_f32 v11, v11, s101, s101
	v_fma_f32 v12, v12, s101, s101
	v_fma_f32 v13, v13, s101, s101
	v_fma_f32 v14, v14, s101, s101
	v_fma_f32 v15, v15, s101, s101
	v_fma_f32 v16, v16, s101, s101
	v_fma_f32 v17, v17, s101, s101
	v_rcp_f32_e32 v10, v10
	v_rcp_f32_e32 v11, v11
	v_rcp_f32_e32 v12, v12
	v_rcp_f32_e32 v13, v13
	v_rcp_f32_e32 v14, v14
	v_rcp_f32_e32 v15, v15
	v_rcp_f32_e32 v16, v16
	v_rcp_f32_e32 v17, v17
	v_mul_f32_e32 v10, v188, v10
	v_mul_f32_e32 v11, v189, v11
	v_mul_f32_e32 v12, v190, v12
	v_mul_f32_e32 v13, v191, v13
	v_mul_f32_e32 v14, v180, v14
	v_mul_f32_e32 v15, v181, v15
	v_mul_f32_e32 v16, v182, v16
	v_mul_f32_e32 v17, v183, v17
	v_mul_f32_e32 v10, v10, v184
	v_mul_f32_e32 v11, v11, v185
	v_mul_f32_e32 v12, v12, v186
	v_mul_f32_e32 v13, v13, v187
	v_mul_f32_e32 v14, v14, v176
	v_mul_f32_e32 v15, v15, v177
	v_mul_f32_e32 v16, v16, v178
	v_mul_f32_e32 v17, v17, v179
	v_cvt_pk_fp8_f32 v18, v10, v11
	v_cvt_pk_fp8_f32 v19, v14, v15
	v_cvt_pk_fp8_f32 v18, v12, v13 op_sel:[0,0,1]
	v_cvt_pk_fp8_f32 v19, v16, v17 op_sel:[0,0,1]
	s_nop 0
	global_store_dwordx2 v[0:1], v[18:19], off
	v_or_b32_e32 v8, 16, v4
	v_ashrrev_i32_e32 v9, 31, v8
	v_lshlrev_b64 v[8:9], 10, v[8:9]
	v_lshl_add_u64 v[8:9], s[8:9], 0, v[8:9]
	v_lshl_add_u64 v[8:9], v[8:9], 0, v[2:3]
	v_mul_f32_e32 v10, 0xbd38aa3b, v172
	v_mul_f32_e32 v11, 0xbd38aa3b, v173
	v_mul_f32_e32 v12, 0xbd38aa3b, v174
	v_mul_f32_e32 v13, 0xbd38aa3b, v175
	v_mul_f32_e32 v14, 0xbd38aa3b, v164
	v_mul_f32_e32 v15, 0xbd38aa3b, v165
	v_mul_f32_e32 v16, 0xbd38aa3b, v166
	v_mul_f32_e32 v17, 0xbd38aa3b, v167
	v_exp_f32_e32 v10, v10
	v_exp_f32_e32 v11, v11
	v_exp_f32_e32 v12, v12
	v_exp_f32_e32 v13, v13
	v_exp_f32_e32 v14, v14
	v_exp_f32_e32 v15, v15
	v_exp_f32_e32 v16, v16
	v_exp_f32_e32 v17, v17
	v_fma_f32 v10, v10, s101, s101
	v_fma_f32 v11, v11, s101, s101
	v_fma_f32 v12, v12, s101, s101
	v_fma_f32 v13, v13, s101, s101
	v_fma_f32 v14, v14, s101, s101
	v_fma_f32 v15, v15, s101, s101
	v_fma_f32 v16, v16, s101, s101
	v_fma_f32 v17, v17, s101, s101
	v_rcp_f32_e32 v10, v10
	v_rcp_f32_e32 v11, v11
	v_rcp_f32_e32 v12, v12
	v_rcp_f32_e32 v13, v13
	v_rcp_f32_e32 v14, v14
	v_rcp_f32_e32 v15, v15
	v_rcp_f32_e32 v16, v16
	v_rcp_f32_e32 v17, v17
	v_mul_f32_e32 v10, v172, v10
	v_mul_f32_e32 v11, v173, v11
	v_mul_f32_e32 v12, v174, v12
	v_mul_f32_e32 v13, v175, v13
	v_mul_f32_e32 v14, v164, v14
	v_mul_f32_e32 v15, v165, v15
	v_mul_f32_e32 v16, v166, v16
	v_mul_f32_e32 v17, v167, v17
	v_mul_f32_e32 v10, v10, v168
	v_mul_f32_e32 v11, v11, v169
	v_mul_f32_e32 v12, v12, v170
	v_mul_f32_e32 v13, v13, v171
	v_mul_f32_e32 v14, v14, v160
	v_mul_f32_e32 v15, v15, v161
	v_mul_f32_e32 v16, v16, v162
	v_mul_f32_e32 v17, v17, v163
	v_cvt_pk_fp8_f32 v18, v10, v11
	v_cvt_pk_fp8_f32 v19, v14, v15
	v_cvt_pk_fp8_f32 v18, v12, v13 op_sel:[0,0,1]
	v_cvt_pk_fp8_f32 v19, v16, v17 op_sel:[0,0,1]
	s_nop 0
	global_store_dwordx2 v[8:9], v[18:19], off
	v_or_b32_e32 v8, 32, v4
	v_ashrrev_i32_e32 v9, 31, v8
	v_or_b32_e32 v4, 48, v4
	v_lshlrev_b64 v[6:7], 10, v[8:9]
	v_lshl_add_u64 v[6:7], s[8:9], 0, v[6:7]
	v_lshl_add_u64 v[6:7], v[6:7], 0, v[2:3]
	v_mul_f32_e32 v10, 0xbd38aa3b, v156
	v_mul_f32_e32 v11, 0xbd38aa3b, v157
	v_mul_f32_e32 v12, 0xbd38aa3b, v158
	v_mul_f32_e32 v13, 0xbd38aa3b, v159
	v_mul_f32_e32 v14, 0xbd38aa3b, v148
	v_mul_f32_e32 v15, 0xbd38aa3b, v149
	v_mul_f32_e32 v16, 0xbd38aa3b, v150
	v_mul_f32_e32 v17, 0xbd38aa3b, v151
	v_exp_f32_e32 v10, v10
	v_exp_f32_e32 v11, v11
	v_exp_f32_e32 v12, v12
	v_exp_f32_e32 v13, v13
	v_exp_f32_e32 v14, v14
	v_exp_f32_e32 v15, v15
	v_exp_f32_e32 v16, v16
	v_exp_f32_e32 v17, v17
	v_fma_f32 v10, v10, s101, s101
	v_fma_f32 v11, v11, s101, s101
	v_fma_f32 v12, v12, s101, s101
	v_fma_f32 v13, v13, s101, s101
	v_fma_f32 v14, v14, s101, s101
	v_fma_f32 v15, v15, s101, s101
	v_fma_f32 v16, v16, s101, s101
	v_fma_f32 v17, v17, s101, s101
	v_rcp_f32_e32 v10, v10
	v_rcp_f32_e32 v11, v11
	v_rcp_f32_e32 v12, v12
	v_rcp_f32_e32 v13, v13
	v_rcp_f32_e32 v14, v14
	v_rcp_f32_e32 v15, v15
	v_rcp_f32_e32 v16, v16
	v_rcp_f32_e32 v17, v17
	v_mul_f32_e32 v10, v156, v10
	v_mul_f32_e32 v11, v157, v11
	v_mul_f32_e32 v12, v158, v12
	v_mul_f32_e32 v13, v159, v13
	v_mul_f32_e32 v14, v148, v14
	v_mul_f32_e32 v15, v149, v15
	v_mul_f32_e32 v16, v150, v16
	v_mul_f32_e32 v17, v151, v17
	v_mul_f32_e32 v10, v10, v152
	v_mul_f32_e32 v11, v11, v153
	v_mul_f32_e32 v12, v12, v154
	v_mul_f32_e32 v13, v13, v155
	v_mul_f32_e32 v14, v14, v144
	v_mul_f32_e32 v15, v15, v145
	v_mul_f32_e32 v16, v16, v146
	v_mul_f32_e32 v17, v17, v147
	v_cvt_pk_fp8_f32 v18, v10, v11
	v_cvt_pk_fp8_f32 v19, v14, v15
	v_cvt_pk_fp8_f32 v18, v12, v13 op_sel:[0,0,1]
	v_cvt_pk_fp8_f32 v19, v16, v17 op_sel:[0,0,1]
	s_nop 0
	global_store_dwordx2 v[6:7], v[18:19], off
	v_ashrrev_i32_e32 v5, 31, v4
	v_lshlrev_b64 v[4:5], 10, v[4:5]
	v_lshl_add_u64 v[4:5], s[8:9], 0, v[4:5]
	v_lshl_add_u64 v[2:3], v[4:5], 0, v[2:3]
	s_mov_b32 s33, s52
	v_mul_f32_e32 v10, 0xbd38aa3b, v140
	v_mul_f32_e32 v11, 0xbd38aa3b, v141
	v_mul_f32_e32 v12, 0xbd38aa3b, v142
	v_mul_f32_e32 v13, 0xbd38aa3b, v143
	v_mul_f32_e32 v14, 0xbd38aa3b, v132
	v_mul_f32_e32 v15, 0xbd38aa3b, v133
	v_mul_f32_e32 v16, 0xbd38aa3b, v134
	v_mul_f32_e32 v17, 0xbd38aa3b, v135
	v_exp_f32_e32 v10, v10
	v_exp_f32_e32 v11, v11
	v_exp_f32_e32 v12, v12
	v_exp_f32_e32 v13, v13
	v_exp_f32_e32 v14, v14
	v_exp_f32_e32 v15, v15
	v_exp_f32_e32 v16, v16
	v_exp_f32_e32 v17, v17
	v_fma_f32 v10, v10, s101, s101
	v_fma_f32 v11, v11, s101, s101
	v_fma_f32 v12, v12, s101, s101
	v_fma_f32 v13, v13, s101, s101
	v_fma_f32 v14, v14, s101, s101
	v_fma_f32 v15, v15, s101, s101
	v_fma_f32 v16, v16, s101, s101
	v_fma_f32 v17, v17, s101, s101
	v_rcp_f32_e32 v10, v10
	v_rcp_f32_e32 v11, v11
	v_rcp_f32_e32 v12, v12
	v_rcp_f32_e32 v13, v13
	v_rcp_f32_e32 v14, v14
	v_rcp_f32_e32 v15, v15
	v_rcp_f32_e32 v16, v16
	v_rcp_f32_e32 v17, v17
	v_mul_f32_e32 v10, v140, v10
	v_mul_f32_e32 v11, v141, v11
	v_mul_f32_e32 v12, v142, v12
	v_mul_f32_e32 v13, v143, v13
	v_mul_f32_e32 v14, v132, v14
	v_mul_f32_e32 v15, v133, v15
	v_mul_f32_e32 v16, v134, v16
	v_mul_f32_e32 v17, v135, v17
	v_mul_f32_e32 v10, v10, v136
	v_mul_f32_e32 v11, v11, v137
	v_mul_f32_e32 v12, v12, v138
	v_mul_f32_e32 v13, v13, v139
	v_mul_f32_e32 v14, v14, v128
	v_mul_f32_e32 v15, v15, v129
	v_mul_f32_e32 v16, v16, v130
	v_mul_f32_e32 v17, v17, v131
	v_cvt_pk_fp8_f32 v18, v10, v11
	v_cvt_pk_fp8_f32 v19, v14, v15
	v_cvt_pk_fp8_f32 v18, v12, v13 op_sel:[0,0,1]
	v_cvt_pk_fp8_f32 v19, v16, v17 op_sel:[0,0,1]
	s_nop 0
	global_store_dwordx2 v[2:3], v[18:19], off
	s_mov_b32 s0, s16
	v_add_co_u32_e32 v6, vcc, s49, v0
	v_addc_co_u32_e32 v7, vcc, 0, v1, vcc
	v_mul_f32_e32 v10, 0xbd38aa3b, v124
	v_mul_f32_e32 v11, 0xbd38aa3b, v125
	v_mul_f32_e32 v12, 0xbd38aa3b, v126
	v_mul_f32_e32 v13, 0xbd38aa3b, v127
	v_mul_f32_e32 v14, 0xbd38aa3b, v116
	v_mul_f32_e32 v15, 0xbd38aa3b, v117
	v_mul_f32_e32 v16, 0xbd38aa3b, v118
	v_mul_f32_e32 v17, 0xbd38aa3b, v119
	v_exp_f32_e32 v10, v10
	v_exp_f32_e32 v11, v11
	v_exp_f32_e32 v12, v12
	v_exp_f32_e32 v13, v13
	v_exp_f32_e32 v14, v14
	v_exp_f32_e32 v15, v15
	v_exp_f32_e32 v16, v16
	v_exp_f32_e32 v17, v17
	v_fma_f32 v10, v10, s101, s101
	v_fma_f32 v11, v11, s101, s101
	v_fma_f32 v12, v12, s101, s101
	v_fma_f32 v13, v13, s101, s101
	v_fma_f32 v14, v14, s101, s101
	v_fma_f32 v15, v15, s101, s101
	v_fma_f32 v16, v16, s101, s101
	v_fma_f32 v17, v17, s101, s101
	v_rcp_f32_e32 v10, v10
	v_rcp_f32_e32 v11, v11
	v_rcp_f32_e32 v12, v12
	v_rcp_f32_e32 v13, v13
	v_rcp_f32_e32 v14, v14
	v_rcp_f32_e32 v15, v15
	v_rcp_f32_e32 v16, v16
	v_rcp_f32_e32 v17, v17
	v_mul_f32_e32 v10, v124, v10
	v_mul_f32_e32 v11, v125, v11
	v_mul_f32_e32 v12, v126, v12
	v_mul_f32_e32 v13, v127, v13
	v_mul_f32_e32 v14, v116, v14
	v_mul_f32_e32 v15, v117, v15
	v_mul_f32_e32 v16, v118, v16
	v_mul_f32_e32 v17, v119, v17
	v_mul_f32_e32 v10, v10, v120
	v_mul_f32_e32 v11, v11, v121
	v_mul_f32_e32 v12, v12, v122
	v_mul_f32_e32 v13, v13, v123
	v_mul_f32_e32 v14, v14, v112
	v_mul_f32_e32 v15, v15, v113
	v_mul_f32_e32 v16, v16, v114
	v_mul_f32_e32 v17, v17, v115
	v_cvt_pk_fp8_f32 v18, v10, v11
	v_cvt_pk_fp8_f32 v19, v14, v15
	v_cvt_pk_fp8_f32 v18, v12, v13 op_sel:[0,0,1]
	v_cvt_pk_fp8_f32 v19, v16, v17 op_sel:[0,0,1]
	s_nop 0
	global_store_dwordx2 v[6:7], v[18:19], off
	v_add_co_u32_e32 v6, vcc, s50, v0
	v_addc_co_u32_e32 v7, vcc, 0, v1, vcc
	v_mul_f32_e32 v10, 0xbd38aa3b, v108
	v_mul_f32_e32 v11, 0xbd38aa3b, v109
	v_mul_f32_e32 v12, 0xbd38aa3b, v110
	v_mul_f32_e32 v13, 0xbd38aa3b, v111
	v_mul_f32_e32 v14, 0xbd38aa3b, v100
	v_mul_f32_e32 v15, 0xbd38aa3b, v101
	v_mul_f32_e32 v16, 0xbd38aa3b, v102
	v_mul_f32_e32 v17, 0xbd38aa3b, v103
	v_exp_f32_e32 v10, v10
	v_exp_f32_e32 v11, v11
	v_exp_f32_e32 v12, v12
	v_exp_f32_e32 v13, v13
	v_exp_f32_e32 v14, v14
	v_exp_f32_e32 v15, v15
	v_exp_f32_e32 v16, v16
	v_exp_f32_e32 v17, v17
	v_fma_f32 v10, v10, s101, s101
	v_fma_f32 v11, v11, s101, s101
	v_fma_f32 v12, v12, s101, s101
	v_fma_f32 v13, v13, s101, s101
	v_fma_f32 v14, v14, s101, s101
	v_fma_f32 v15, v15, s101, s101
	v_fma_f32 v16, v16, s101, s101
	v_fma_f32 v17, v17, s101, s101
	v_rcp_f32_e32 v10, v10
	v_rcp_f32_e32 v11, v11
	v_rcp_f32_e32 v12, v12
	v_rcp_f32_e32 v13, v13
	v_rcp_f32_e32 v14, v14
	v_rcp_f32_e32 v15, v15
	v_rcp_f32_e32 v16, v16
	v_rcp_f32_e32 v17, v17
	v_mul_f32_e32 v10, v108, v10
	v_mul_f32_e32 v11, v109, v11
	v_mul_f32_e32 v12, v110, v12
	v_mul_f32_e32 v13, v111, v13
	v_mul_f32_e32 v14, v100, v14
	v_mul_f32_e32 v15, v101, v15
	v_mul_f32_e32 v16, v102, v16
	v_mul_f32_e32 v17, v103, v17
	v_mul_f32_e32 v10, v10, v104
	v_mul_f32_e32 v11, v11, v105
	v_mul_f32_e32 v12, v12, v106
	v_mul_f32_e32 v13, v13, v107
	v_mul_f32_e32 v14, v14, v96
	v_mul_f32_e32 v15, v15, v97
	v_mul_f32_e32 v16, v16, v98
	v_mul_f32_e32 v17, v17, v99
	v_cvt_pk_fp8_f32 v18, v10, v11
	v_cvt_pk_fp8_f32 v19, v14, v15
	v_cvt_pk_fp8_f32 v18, v12, v13 op_sel:[0,0,1]
	v_cvt_pk_fp8_f32 v19, v16, v17 op_sel:[0,0,1]
	s_nop 0
	global_store_dwordx2 v[6:7], v[18:19], off
	v_add_co_u32_e32 v6, vcc, s51, v0
	v_addc_co_u32_e32 v7, vcc, 0, v1, vcc
	v_mul_f32_e32 v10, 0xbd38aa3b, v92
	v_mul_f32_e32 v11, 0xbd38aa3b, v93
	v_mul_f32_e32 v12, 0xbd38aa3b, v94
	v_mul_f32_e32 v13, 0xbd38aa3b, v95
	v_mul_f32_e32 v14, 0xbd38aa3b, v84
	v_mul_f32_e32 v15, 0xbd38aa3b, v85
	v_mul_f32_e32 v16, 0xbd38aa3b, v86
	v_mul_f32_e32 v17, 0xbd38aa3b, v87
	v_exp_f32_e32 v10, v10
	v_exp_f32_e32 v11, v11
	v_exp_f32_e32 v12, v12
	v_exp_f32_e32 v13, v13
	v_exp_f32_e32 v14, v14
	v_exp_f32_e32 v15, v15
	v_exp_f32_e32 v16, v16
	v_exp_f32_e32 v17, v17
	v_fma_f32 v10, v10, s101, s101
	v_fma_f32 v11, v11, s101, s101
	v_fma_f32 v12, v12, s101, s101
	v_fma_f32 v13, v13, s101, s101
	v_fma_f32 v14, v14, s101, s101
	v_fma_f32 v15, v15, s101, s101
	v_fma_f32 v16, v16, s101, s101
	v_fma_f32 v17, v17, s101, s101
	v_rcp_f32_e32 v10, v10
	v_rcp_f32_e32 v11, v11
	v_rcp_f32_e32 v12, v12
	v_rcp_f32_e32 v13, v13
	v_rcp_f32_e32 v14, v14
	v_rcp_f32_e32 v15, v15
	v_rcp_f32_e32 v16, v16
	v_rcp_f32_e32 v17, v17
	v_mul_f32_e32 v10, v92, v10
	v_mul_f32_e32 v11, v93, v11
	v_mul_f32_e32 v12, v94, v12
	v_mul_f32_e32 v13, v95, v13
	v_mul_f32_e32 v14, v84, v14
	v_mul_f32_e32 v15, v85, v15
	v_mul_f32_e32 v16, v86, v16
	v_mul_f32_e32 v17, v87, v17
	v_mul_f32_e32 v10, v10, v88
	v_mul_f32_e32 v11, v11, v89
	v_mul_f32_e32 v12, v12, v90
	v_mul_f32_e32 v13, v13, v91
	v_mul_f32_e32 v14, v14, v80
	v_mul_f32_e32 v15, v15, v81
	v_mul_f32_e32 v16, v16, v82
	v_mul_f32_e32 v17, v17, v83
	v_cvt_pk_fp8_f32 v18, v10, v11
	v_cvt_pk_fp8_f32 v19, v14, v15
	v_cvt_pk_fp8_f32 v18, v12, v13 op_sel:[0,0,1]
	v_cvt_pk_fp8_f32 v19, v16, v17 op_sel:[0,0,1]
	s_nop 0
	global_store_dwordx2 v[6:7], v[18:19], off
	v_add_co_u32_e32 v0, vcc, 0x2c000, v0
	s_mov_b64 s[2:3], s[18:19]
	s_nop 0
	v_addc_co_u32_e32 v1, vcc, 0, v1, vcc
	s_and_b64 vcc, exec, s[10:11]
	v_mul_f32_e32 v10, 0xbd38aa3b, v76
	v_mul_f32_e32 v11, 0xbd38aa3b, v77
	v_mul_f32_e32 v12, 0xbd38aa3b, v78
	v_mul_f32_e32 v13, 0xbd38aa3b, v79
	v_mul_f32_e32 v14, 0xbd38aa3b, v68
	v_mul_f32_e32 v15, 0xbd38aa3b, v69
	v_mul_f32_e32 v16, 0xbd38aa3b, v70
	v_mul_f32_e32 v17, 0xbd38aa3b, v71
	v_exp_f32_e32 v10, v10
	v_exp_f32_e32 v11, v11
	v_exp_f32_e32 v12, v12
	v_exp_f32_e32 v13, v13
	v_exp_f32_e32 v14, v14
	v_exp_f32_e32 v15, v15
	v_exp_f32_e32 v16, v16
	v_exp_f32_e32 v17, v17
	v_fma_f32 v10, v10, s101, s101
	v_fma_f32 v11, v11, s101, s101
	v_fma_f32 v12, v12, s101, s101
	v_fma_f32 v13, v13, s101, s101
	v_fma_f32 v14, v14, s101, s101
	v_fma_f32 v15, v15, s101, s101
	v_fma_f32 v16, v16, s101, s101
	v_fma_f32 v17, v17, s101, s101
	v_rcp_f32_e32 v10, v10
	v_rcp_f32_e32 v11, v11
	v_rcp_f32_e32 v12, v12
	v_rcp_f32_e32 v13, v13
	v_rcp_f32_e32 v14, v14
	v_rcp_f32_e32 v15, v15
	v_rcp_f32_e32 v16, v16
	v_rcp_f32_e32 v17, v17
	v_mul_f32_e32 v10, v76, v10
	v_mul_f32_e32 v11, v77, v11
	v_mul_f32_e32 v12, v78, v12
	v_mul_f32_e32 v13, v79, v13
	v_mul_f32_e32 v14, v68, v14
	v_mul_f32_e32 v15, v69, v15
	v_mul_f32_e32 v16, v70, v16
	v_mul_f32_e32 v17, v71, v17
	v_mul_f32_e32 v10, v10, v72
	v_mul_f32_e32 v11, v11, v73
	v_mul_f32_e32 v12, v12, v74
	v_mul_f32_e32 v13, v13, v75
	v_mul_f32_e32 v14, v14, v64
	v_mul_f32_e32 v15, v15, v65
	v_mul_f32_e32 v16, v16, v66
	v_mul_f32_e32 v17, v17, v67
	v_cvt_pk_fp8_f32 v18, v10, v11
	v_cvt_pk_fp8_f32 v19, v14, v15
	v_cvt_pk_fp8_f32 v18, v12, v13 op_sel:[0,0,1]
	v_cvt_pk_fp8_f32 v19, v16, v17 op_sel:[0,0,1]
	s_nop 0
	global_store_dwordx2 v[0:1], v[18:19], off
	s_cbranch_vccnz .LBB0_2965

.LBB0_2961:
	s_ashr_i32 s17, s16, 31
	s_lshl_b64 s[18:19], s[16:17], 18
	s_add_u32 s18, s28, s18
	s_addc_u32 s19, s29, s19
	s_and_b64 s[20:21], s[12:13], exec
	s_cselect_b32 s17, s19, s3
	s_cselect_b32 s53, s18, s2
	s_lshl_b32 s20, s41, 10
	s_add_i32 s20, s20, 0
	s_add_i32 s20, s20, 0x20010
	v_mov_b32_e32 v64, 0
	v_add3_u32 v233, s20, v213, v214
	v_add3_u32 v234, s20, v215, v216
	s_mov_b32 s54, -2
	s_mov_b64 s[20:21], 0xdbff000
	v_mov_b32_e32 v65, 0
	v_mov_b64_e32 v[66:67], 0
	v_mov_b64_e32 v[68:69], 0
	v_mov_b64_e32 v[70:71], 0
	v_mov_b64_e32 v[72:73], 0
	v_mov_b64_e32 v[74:75], 0
	v_mov_b64_e32 v[76:77], 0
	v_mov_b64_e32 v[78:79], 0
	v_mov_b64_e32 v[80:81], 0
	v_mov_b64_e32 v[82:83], 0
	v_mov_b64_e32 v[84:85], 0
	v_mov_b64_e32 v[86:87], 0
	v_mov_b64_e32 v[88:89], 0
	v_mov_b64_e32 v[90:91], 0
	v_mov_b64_e32 v[92:93], 0
	v_mov_b64_e32 v[94:95], 0
	v_mov_b64_e32 v[96:97], 0
	v_mov_b64_e32 v[98:99], 0
	v_mov_b64_e32 v[100:101], 0
	v_mov_b64_e32 v[102:103], 0
	v_mov_b64_e32 v[104:105], 0
	v_mov_b64_e32 v[106:107], 0
	v_mov_b64_e32 v[108:109], 0
	v_mov_b64_e32 v[110:111], 0
	v_mov_b64_e32 v[112:113], 0
	v_mov_b64_e32 v[114:115], 0
	v_mov_b64_e32 v[116:117], 0
	v_mov_b64_e32 v[118:119], 0
	v_mov_b64_e32 v[120:121], 0
	v_mov_b64_e32 v[122:123], 0
	v_mov_b64_e32 v[124:125], 0
	v_mov_b64_e32 v[126:127], 0
	v_mov_b64_e32 v[128:129], 0
	v_mov_b64_e32 v[130:131], 0
	v_mov_b64_e32 v[132:133], 0
	v_mov_b64_e32 v[134:135], 0
	v_mov_b64_e32 v[136:137], 0
	v_mov_b64_e32 v[138:139], 0
	v_mov_b64_e32 v[140:141], 0
	v_mov_b64_e32 v[142:143], 0
	v_mov_b64_e32 v[144:145], 0
	v_mov_b64_e32 v[146:147], 0
	v_mov_b64_e32 v[148:149], 0
	v_mov_b64_e32 v[150:151], 0
	v_mov_b64_e32 v[152:153], 0
	v_mov_b64_e32 v[154:155], 0
	v_mov_b64_e32 v[156:157], 0
	v_mov_b64_e32 v[158:159], 0
	v_mov_b64_e32 v[160:161], 0
	v_mov_b64_e32 v[162:163], 0
	v_mov_b64_e32 v[164:165], 0
	v_mov_b64_e32 v[166:167], 0
	v_mov_b64_e32 v[168:169], 0
	v_mov_b64_e32 v[170:171], 0
	v_mov_b64_e32 v[172:173], 0
	v_mov_b64_e32 v[174:175], 0
	v_mov_b64_e32 v[176:177], 0
	v_mov_b64_e32 v[178:179], 0
	v_mov_b64_e32 v[180:181], 0
	v_mov_b64_e32 v[182:183], 0
	v_mov_b64_e32 v[184:185], 0
	v_mov_b64_e32 v[186:187], 0
	v_mov_b64_e32 v[188:189], 0
	v_mov_b64_e32 v[190:191], 0
	s_branch .LBB0_2963

.LBB0_3026:
	s_ashr_i32 s21, s20, 31
	s_lshl_b64 s[6:7], s[20:21], 18
	s_add_u32 s6, s43, s6
	s_addc_u32 s7, s44, s7
	s_ashr_i32 s23, s22, 31
	s_lshl_b64 s[24:25], s[22:23], 18
	s_add_u32 s24, s41, s24
	s_addc_u32 s25, s42, s25
	s_and_b64 s[30:31], s[12:13], exec
	v_mov_b32_e32 v32, 0
	s_cselect_b32 s21, s25, s27
	s_cselect_b32 s23, s24, s26
	s_mov_b32 s33, -2
	s_mov_b64 s[36:37], 0
	v_mov_b32_e32 v33, 0
	v_mov_b64_e32 v[34:35], 0
	v_mov_b64_e32 v[36:37], 0
	v_mov_b64_e32 v[38:39], 0
	v_mov_b64_e32 v[40:41], 0
	v_mov_b64_e32 v[42:43], 0
	v_mov_b64_e32 v[44:45], 0
	v_mov_b64_e32 v[46:47], 0
	v_mov_b64_e32 v[48:49], 0
	v_mov_b64_e32 v[50:51], 0
	v_mov_b64_e32 v[52:53], 0
	v_mov_b64_e32 v[54:55], 0
	v_mov_b64_e32 v[56:57], 0
	v_mov_b64_e32 v[58:59], 0
	v_mov_b64_e32 v[60:61], 0
	v_mov_b64_e32 v[62:63], 0
	v_mov_b64_e32 v[64:65], 0
	v_mov_b64_e32 v[66:67], 0
	v_mov_b64_e32 v[68:69], 0
	v_mov_b64_e32 v[70:71], 0
	v_mov_b64_e32 v[72:73], 0
	v_mov_b64_e32 v[74:75], 0
	v_mov_b64_e32 v[76:77], 0
	v_mov_b64_e32 v[78:79], 0
	v_mov_b64_e32 v[80:81], 0
	v_mov_b64_e32 v[82:83], 0
	v_mov_b64_e32 v[84:85], 0
	v_mov_b64_e32 v[86:87], 0
	v_mov_b64_e32 v[88:89], 0
	v_mov_b64_e32 v[90:91], 0
	v_mov_b64_e32 v[92:93], 0
	v_mov_b64_e32 v[94:95], 0
	v_mov_b64_e32 v[96:97], 0
	v_mov_b64_e32 v[98:99], 0
	v_mov_b64_e32 v[100:101], 0
	v_mov_b64_e32 v[102:103], 0
	v_mov_b64_e32 v[104:105], 0
	v_mov_b64_e32 v[106:107], 0
	v_mov_b64_e32 v[108:109], 0
	v_mov_b64_e32 v[110:111], 0
	v_mov_b64_e32 v[112:113], 0
	v_mov_b64_e32 v[114:115], 0
	v_mov_b64_e32 v[116:117], 0
	v_mov_b64_e32 v[118:119], 0
	v_mov_b64_e32 v[120:121], 0
	v_mov_b64_e32 v[122:123], 0
	v_mov_b64_e32 v[124:125], 0
	v_mov_b64_e32 v[126:127], 0
	v_mov_b64_e32 v[128:129], 0
	v_mov_b64_e32 v[130:131], 0
	v_mov_b64_e32 v[132:133], 0
	v_mov_b64_e32 v[134:135], 0
	v_mov_b64_e32 v[136:137], 0
	v_mov_b64_e32 v[138:139], 0
	v_mov_b64_e32 v[140:141], 0
	v_mov_b64_e32 v[142:143], 0
	v_mov_b64_e32 v[144:145], 0
	v_mov_b64_e32 v[146:147], 0
	v_mov_b64_e32 v[148:149], 0
	v_mov_b64_e32 v[150:151], 0
	v_mov_b64_e32 v[152:153], 0
	v_mov_b64_e32 v[154:155], 0
	v_mov_b64_e32 v[156:157], 0
	v_mov_b64_e32 v[158:159], 0
.LBB0_3027:
	s_add_u32 s30, s36, 0x100
	ds_read_b128 v[0:3], v174
	ds_read_b128 v[4:7], v175
	ds_read_b128 v[8:11], v182
	ds_read_b128 v[12:15], v183
	s_addc_u32 s31, s37, 0
	s_and_b32 s66, s30, 0x300
	s_add_u32 s65, s26, s66
	s_addc_u32 s67, s27, 0
	s_cmp_eq_u32 s33, 4
	s_cselect_b64 s[38:39], -1, 0
	s_and_b64 s[34:35], s[38:39], exec
	s_cselect_b32 s35, s21, s67
	s_cselect_b32 s34, s23, s65
	s_cselect_b32 s65, 0, 0
	s_cselect_b32 s66, 0, s66
	s_add_u32 s36, s28, s36
	s_addc_u32 s37, s29, s37
	s_add_u32 s36, s36, 0x20080
	s_addc_u32 s37, s37, 0
	ds_read_b128 v[194:197], v190
	ds_read_b128 v[210:213], v190 offset:2048
	ds_read_b128 v[198:201], v191
	ds_read_b128 v[214:217], v191 offset:2048
	ds_read_b128 v[218:221], v190 offset:4096
	ds_read_b128 v[226:229], v190 offset:6144
	ds_read_b128 v[222:225], v191 offset:4096
	ds_read_b128 v[230:233], v191 offset:6144
	s_add_i32 m0, s1, 0xc000
	s_nop 0
	global_load_lds_dwordx4 v166, s[36:37]
	s_add_i32 m0, s1, 0xe000
	s_nop 0
	global_load_lds_dwordx4 v162, s[36:37]
	s_waitcnt lgkmcnt(8)
	s_barrier
	s_waitcnt lgkmcnt(0)
	s_setprio 1
	s_waitcnt lgkmcnt(0)
	v_mfma_scale_f32_16x16x128_f8f6f4 v[156:159], v[0:7], v[194:201], v[156:159], v173, v173 op_sel_hi:[0,0,0]
	v_mfma_scale_f32_16x16x128_f8f6f4 v[152:155], v[8:15], v[194:201], v[152:155], v173, v173 op_sel_hi:[0,0,0]
	v_mfma_scale_f32_16x16x128_f8f6f4 v[140:143], v[0:7], v[210:217], v[140:143], v173, v173 op_sel_hi:[0,0,0]
	v_mfma_scale_f32_16x16x128_f8f6f4 v[136:139], v[8:15], v[210:217], v[136:139], v173, v173 op_sel_hi:[0,0,0]
	v_mfma_scale_f32_16x16x128_f8f6f4 v[124:127], v[0:7], v[218:225], v[124:127], v173, v173 op_sel_hi:[0,0,0]
	v_mfma_scale_f32_16x16x128_f8f6f4 v[120:123], v[8:15], v[218:225], v[120:123], v173, v173 op_sel_hi:[0,0,0]
	v_mfma_scale_f32_16x16x128_f8f6f4 v[108:111], v[0:7], v[226:233], v[108:111], v173, v173 op_sel_hi:[0,0,0]
	v_mfma_scale_f32_16x16x128_f8f6f4 v[104:107], v[8:15], v[226:233], v[104:107], v173, v173 op_sel_hi:[0,0,0]
	s_setprio 0
	s_barrier
	s_mov_b64 s[36:37], s[34:35]
	s_mov_b32 m0, s3
	ds_read_b128 v[16:19], v176
	ds_read_b128 v[20:23], v177
	ds_read_b128 v[24:27], v184
	ds_read_b128 v[28:31], v185
	s_nop 0
	global_load_lds_dwordx4 v164, s[36:37]
	s_mov_b32 m0, s47
	s_nop 0
	global_load_lds_dwordx4 v160, s[36:37]
	s_barrier
	s_waitcnt lgkmcnt(0)
	s_setprio 1
	s_waitcnt lgkmcnt(0)
	v_mfma_scale_f32_16x16x128_f8f6f4 v[148:151], v[16:23], v[194:201], v[148:151], v173, v173 op_sel_hi:[0,0,0]
	v_mfma_scale_f32_16x16x128_f8f6f4 v[144:147], v[24:31], v[194:201], v[144:147], v173, v173 op_sel_hi:[0,0,0]
	v_mfma_scale_f32_16x16x128_f8f6f4 v[132:135], v[16:23], v[210:217], v[132:135], v173, v173 op_sel_hi:[0,0,0]
	v_mfma_scale_f32_16x16x128_f8f6f4 v[128:131], v[24:31], v[210:217], v[128:131], v173, v173 op_sel_hi:[0,0,0]
	v_mfma_scale_f32_16x16x128_f8f6f4 v[116:119], v[16:23], v[218:225], v[116:119], v173, v173 op_sel_hi:[0,0,0]
	v_mfma_scale_f32_16x16x128_f8f6f4 v[112:115], v[24:31], v[218:225], v[112:115], v173, v173 op_sel_hi:[0,0,0]
	v_mfma_scale_f32_16x16x128_f8f6f4 v[100:103], v[16:23], v[226:233], v[100:103], v173, v173 op_sel_hi:[0,0,0]
	v_mfma_scale_f32_16x16x128_f8f6f4 v[96:99], v[24:31], v[226:233], v[96:99], v173, v173 op_sel_hi:[0,0,0]
	s_setprio 0
	s_and_b64 s[36:37], s[12:13], s[38:39]
	s_and_b64 s[36:37], s[36:37], exec
	s_cselect_b32 s36, s6, s28
	s_cselect_b32 s37, s7, s29
	s_add_u32 s36, s36, s66
	s_addc_u32 s37, s37, s65
	s_mov_b64 s[38:39], s[36:37]
	s_mov_b32 m0, s1
	s_barrier
	ds_read_b128 v[194:197], v190 offset:16384
	ds_read_b128 v[210:213], v190 offset:18432
	ds_read_b128 v[198:201], v191 offset:16384
	ds_read_b128 v[214:217], v191 offset:18432
	ds_read_b128 v[218:221], v190 offset:20480
	ds_read_b128 v[226:229], v190 offset:22528
	ds_read_b128 v[222:225], v191 offset:20480
	ds_read_b128 v[230:233], v191 offset:22528
	s_nop 0
	global_load_lds_dwordx4 v166, s[38:39]
	s_mov_b32 m0, s48
	s_nop 0
	global_load_lds_dwordx4 v162, s[38:39]
	s_barrier
	s_waitcnt lgkmcnt(0)
	s_setprio 1
	s_waitcnt lgkmcnt(0)
	v_mfma_scale_f32_16x16x128_f8f6f4 v[92:95], v[0:7], v[194:201], v[92:95], v173, v173 op_sel_hi:[0,0,0]
	v_mfma_scale_f32_16x16x128_f8f6f4 v[88:91], v[8:15], v[194:201], v[88:91], v173, v173 op_sel_hi:[0,0,0]
	v_mfma_scale_f32_16x16x128_f8f6f4 v[76:79], v[0:7], v[210:217], v[76:79], v173, v173 op_sel_hi:[0,0,0]
	v_mfma_scale_f32_16x16x128_f8f6f4 v[72:75], v[8:15], v[210:217], v[72:75], v173, v173 op_sel_hi:[0,0,0]
	v_mfma_scale_f32_16x16x128_f8f6f4 v[60:63], v[0:7], v[218:225], v[60:63], v173, v173 op_sel_hi:[0,0,0]
	v_mfma_scale_f32_16x16x128_f8f6f4 v[56:59], v[8:15], v[218:225], v[56:59], v173, v173 op_sel_hi:[0,0,0]
	v_mfma_scale_f32_16x16x128_f8f6f4 v[44:47], v[0:7], v[226:233], v[44:47], v173, v173 op_sel_hi:[0,0,0]
	v_mfma_scale_f32_16x16x128_f8f6f4 v[40:43], v[8:15], v[226:233], v[40:43], v173, v173 op_sel_hi:[0,0,0]
	s_setprio 0
	s_barrier
	s_add_u32 s38, s34, 0x20000
	s_addc_u32 s39, s35, 0
	s_mov_b32 m0, s49
	s_nop 0
	global_load_lds_dwordx4 v164, s[38:39]
	s_mov_b32 m0, s50
	s_nop 0
	global_load_lds_dwordx4 v160, s[38:39]
	s_waitcnt vmcnt(6)
	s_barrier
	s_setprio 1
	v_mfma_scale_f32_16x16x128_f8f6f4 v[84:87], v[16:23], v[194:201], v[84:87], v173, v173 op_sel_hi:[0,0,0]
	v_mfma_scale_f32_16x16x128_f8f6f4 v[80:83], v[24:31], v[194:201], v[80:83], v173, v173 op_sel_hi:[0,0,0]
	v_mfma_scale_f32_16x16x128_f8f6f4 v[68:71], v[16:23], v[210:217], v[68:71], v173, v173 op_sel_hi:[0,0,0]
	v_mfma_scale_f32_16x16x128_f8f6f4 v[64:67], v[24:31], v[210:217], v[64:67], v173, v173 op_sel_hi:[0,0,0]
	v_mfma_scale_f32_16x16x128_f8f6f4 v[52:55], v[16:23], v[218:225], v[52:55], v173, v173 op_sel_hi:[0,0,0]
	v_mfma_scale_f32_16x16x128_f8f6f4 v[48:51], v[24:31], v[218:225], v[48:51], v173, v173 op_sel_hi:[0,0,0]
	v_mfma_scale_f32_16x16x128_f8f6f4 v[36:39], v[16:23], v[226:233], v[36:39], v173, v173 op_sel_hi:[0,0,0]
	v_mfma_scale_f32_16x16x128_f8f6f4 v[32:35], v[24:31], v[226:233], v[32:35], v173, v173 op_sel_hi:[0,0,0]
	s_setprio 0
	s_barrier
	ds_read_b128 v[0:3], v178
	ds_read_b128 v[4:7], v179
	ds_read_b128 v[8:11], v186
	ds_read_b128 v[12:15], v187
	s_add_u32 s38, s36, 0x20000
	s_addc_u32 s39, s37, 0
	s_mov_b32 m0, s51
	ds_read_b128 v[16:19], v190 offset:32768
	ds_read_b128 v[24:27], v190 offset:34816
	ds_read_b128 v[20:23], v191 offset:32768
	ds_read_b128 v[28:31], v191 offset:34816
	ds_read_b128 v[194:197], v190 offset:36864
	ds_read_b128 v[210:213], v190 offset:38912
	ds_read_b128 v[198:201], v191 offset:36864
	ds_read_b128 v[214:217], v191 offset:38912
	s_nop 0
	global_load_lds_dwordx4 v166, s[38:39]
	s_mov_b32 m0, s52
	s_nop 0
	global_load_lds_dwordx4 v162, s[38:39]
	s_waitcnt lgkmcnt(8)
	s_barrier
	s_waitcnt lgkmcnt(0)
	s_setprio 1
	s_waitcnt lgkmcnt(0)
	v_mfma_scale_f32_16x16x128_f8f6f4 v[156:159], v[0:7], v[16:23], v[156:159], v173, v173 op_sel_hi:[0,0,0]
	v_mfma_scale_f32_16x16x128_f8f6f4 v[152:155], v[8:15], v[16:23], v[152:155], v173, v173 op_sel_hi:[0,0,0]
	v_mfma_scale_f32_16x16x128_f8f6f4 v[140:143], v[0:7], v[24:31], v[140:143], v173, v173 op_sel_hi:[0,0,0]
	v_mfma_scale_f32_16x16x128_f8f6f4 v[136:139], v[8:15], v[24:31], v[136:139], v173, v173 op_sel_hi:[0,0,0]
	v_mfma_scale_f32_16x16x128_f8f6f4 v[124:127], v[0:7], v[194:201], v[124:127], v173, v173 op_sel_hi:[0,0,0]
	v_mfma_scale_f32_16x16x128_f8f6f4 v[120:123], v[8:15], v[194:201], v[120:123], v173, v173 op_sel_hi:[0,0,0]
	v_mfma_scale_f32_16x16x128_f8f6f4 v[108:111], v[0:7], v[210:217], v[108:111], v173, v173 op_sel_hi:[0,0,0]
	v_mfma_scale_f32_16x16x128_f8f6f4 v[104:107], v[8:15], v[210:217], v[104:107], v173, v173 op_sel_hi:[0,0,0]
	s_setprio 0
	s_barrier
	s_add_u32 s38, s34, 0x80
	s_addc_u32 s39, s35, 0
	s_mov_b32 m0, s54
	ds_read_b128 v[218:221], v180
	ds_read_b128 v[222:225], v181
	ds_read_b128 v[226:229], v188
	ds_read_b128 v[230:233], v189
	s_nop 0
	global_load_lds_dwordx4 v164, s[38:39]
	s_mov_b32 m0, s55
	s_nop 0
	global_load_lds_dwordx4 v160, s[38:39]
	s_barrier
	s_waitcnt lgkmcnt(0)
	s_setprio 1
	s_waitcnt lgkmcnt(0)
	v_mfma_scale_f32_16x16x128_f8f6f4 v[148:151], v[218:225], v[16:23], v[148:151], v173, v173 op_sel_hi:[0,0,0]
	v_mfma_scale_f32_16x16x128_f8f6f4 v[144:147], v[226:233], v[16:23], v[144:147], v173, v173 op_sel_hi:[0,0,0]
	v_mfma_scale_f32_16x16x128_f8f6f4 v[132:135], v[218:225], v[24:31], v[132:135], v173, v173 op_sel_hi:[0,0,0]
	v_mfma_scale_f32_16x16x128_f8f6f4 v[128:131], v[226:233], v[24:31], v[128:131], v173, v173 op_sel_hi:[0,0,0]
	v_mfma_scale_f32_16x16x128_f8f6f4 v[116:119], v[218:225], v[194:201], v[116:119], v173, v173 op_sel_hi:[0,0,0]
	v_mfma_scale_f32_16x16x128_f8f6f4 v[112:115], v[226:233], v[194:201], v[112:115], v173, v173 op_sel_hi:[0,0,0]
	v_mfma_scale_f32_16x16x128_f8f6f4 v[100:103], v[218:225], v[210:217], v[100:103], v173, v173 op_sel_hi:[0,0,0]
	v_mfma_scale_f32_16x16x128_f8f6f4 v[96:99], v[226:233], v[210:217], v[96:99], v173, v173 op_sel_hi:[0,0,0]
	s_setprio 0
	s_add_u32 s36, s36, 0x80
	s_addc_u32 s37, s37, 0
	s_mov_b32 m0, s56
	s_barrier
	ds_read_b128 v[16:19], v190 offset:49152
	ds_read_b128 v[24:27], v190 offset:51200
	ds_read_b128 v[20:23], v191 offset:49152
	ds_read_b128 v[28:31], v191 offset:51200
	ds_read_b128 v[194:197], v190 offset:53248
	ds_read_b128 v[210:213], v190 offset:55296
	ds_read_b128 v[198:201], v191 offset:53248
	ds_read_b128 v[214:217], v191 offset:55296
	s_nop 0
	global_load_lds_dwordx4 v166, s[36:37]
	s_mov_b32 m0, s57
	s_nop 0
	global_load_lds_dwordx4 v162, s[36:37]
	s_barrier
	s_waitcnt lgkmcnt(0)
	s_setprio 1
	s_waitcnt lgkmcnt(0)
	v_mfma_scale_f32_16x16x128_f8f6f4 v[92:95], v[0:7], v[16:23], v[92:95], v173, v173 op_sel_hi:[0,0,0]
	v_mfma_scale_f32_16x16x128_f8f6f4 v[88:91], v[8:15], v[16:23], v[88:91], v173, v173 op_sel_hi:[0,0,0]
	v_mfma_scale_f32_16x16x128_f8f6f4 v[76:79], v[0:7], v[24:31], v[76:79], v173, v173 op_sel_hi:[0,0,0]
	v_mfma_scale_f32_16x16x128_f8f6f4 v[72:75], v[8:15], v[24:31], v[72:75], v173, v173 op_sel_hi:[0,0,0]
	v_mfma_scale_f32_16x16x128_f8f6f4 v[60:63], v[0:7], v[194:201], v[60:63], v173, v173 op_sel_hi:[0,0,0]
	v_mfma_scale_f32_16x16x128_f8f6f4 v[56:59], v[8:15], v[194:201], v[56:59], v173, v173 op_sel_hi:[0,0,0]
	v_mfma_scale_f32_16x16x128_f8f6f4 v[44:47], v[0:7], v[210:217], v[44:47], v173, v173 op_sel_hi:[0,0,0]
	v_mfma_scale_f32_16x16x128_f8f6f4 v[40:43], v[8:15], v[210:217], v[40:43], v173, v173 op_sel_hi:[0,0,0]
	s_setprio 0
	s_barrier
	s_add_u32 s34, s34, 0x20080
	s_addc_u32 s35, s35, 0
	s_mov_b32 m0, s58
	s_nop 0
	global_load_lds_dwordx4 v164, s[34:35]
	s_mov_b32 m0, s59
	s_nop 0
	global_load_lds_dwordx4 v160, s[34:35]
	s_waitcnt vmcnt(6)
	s_barrier
	s_setprio 1
	v_mfma_scale_f32_16x16x128_f8f6f4 v[84:87], v[218:225], v[16:23], v[84:87], v173, v173 op_sel_hi:[0,0,0]
	v_mfma_scale_f32_16x16x128_f8f6f4 v[80:83], v[226:233], v[16:23], v[80:83], v173, v173 op_sel_hi:[0,0,0]
	v_mfma_scale_f32_16x16x128_f8f6f4 v[68:71], v[218:225], v[24:31], v[68:71], v173, v173 op_sel_hi:[0,0,0]
	v_mfma_scale_f32_16x16x128_f8f6f4 v[64:67], v[226:233], v[24:31], v[64:67], v173, v173 op_sel_hi:[0,0,0]
	v_mfma_scale_f32_16x16x128_f8f6f4 v[52:55], v[218:225], v[194:201], v[52:55], v173, v173 op_sel_hi:[0,0,0]
	v_mfma_scale_f32_16x16x128_f8f6f4 v[48:51], v[226:233], v[194:201], v[48:51], v173, v173 op_sel_hi:[0,0,0]
	v_mfma_scale_f32_16x16x128_f8f6f4 v[36:39], v[218:225], v[210:217], v[36:39], v173, v173 op_sel_hi:[0,0,0]
	v_mfma_scale_f32_16x16x128_f8f6f4 v[32:35], v[226:233], v[210:217], v[32:35], v173, v173 op_sel_hi:[0,0,0]
	s_setprio 0
	s_add_i32 s33, s33, 2
	s_cmp_gt_u32 s33, 5
	s_mov_b64 s[36:37], s[30:31]
	s_barrier
	s_cbranch_scc0 .LBB0_3027
	v_mov_b32_e32 v2, v172
	s_nop 15
	s_nop 15
	v_mov_b32_e32 v8, 0
	v_ashrrev_i32_e32 v0, 2, v2
	v_and_b32_e32 v0, 0xffffffc0, v0
	v_lshl_add_u32 v0, s2, 8, v0
	v_and_or_b32 v6, v2, 15, v0
	v_ashrrev_i32_e32 v7, 31, v6
	v_lshl_add_u64 v[0:1], v[6:7], 2, s[4:5]
	global_load_dword v14, v[0:1], off
	global_load_dword v194, v[0:1], off offset:64
	global_load_dword v195, v[0:1], off offset:128
	global_load_dword v196, v[0:1], off offset:192
	global_load_dword v197, v[0:1], off offset:512
	global_load_dword v198, v[0:1], off offset:576
	global_load_dword v199, v[0:1], off offset:640
	global_load_dword v200, v[0:1], off offset:704
	s_ashr_i32 s2, s0, 31
	s_lshr_b32 s2, s2, 30
	s_add_i32 s2, s0, s2
	v_lshrrev_b32_e32 v2, 1, v2
	s_and_b32 s2, s2, 0xfffffc
	v_and_b32_e32 v2, 0x78, v2
	s_sub_i32 s0, s0, s2
	v_lshl_or_b32 v4, s0, 8, v2
	v_lshlrev_b64 v[2:3], 10, v[6:7]
	v_mov_b32_e32 v9, 0
	v_mov_b32_e32 v10, 0
	v_mov_b32_e32 v11, 0
	v_ashrrev_i32_e32 v5, 31, v4
	v_or_b32_e32 v12, 16, v6
	v_lshl_add_u64 v[2:3], s[8:9], 0, v[2:3]
	v_ashrrev_i32_e32 v13, 31, v12
	v_lshl_add_u64 v[2:3], v[2:3], 0, v[4:5]
	s_mov_b32 s0, 0x20000
	s_mov_b64 s[12:13], 0x20000
	s_mov_b64 s[28:29], s[6:7]
	s_mov_b64 s[26:27], s[24:25]
	s_mov_b32 s2, s20
	s_waitcnt vmcnt(0)
	v_mul_f32_e32 v7, 0x3d000000, v14
	v_mul_f32_e32 v14, 0x42000000, v7
	v_pk_mul_f32 v[18:19], v[156:157], v[14:15] op_sel_hi:[1,0]
	v_pk_mul_f32 v[22:23], v[152:153], v[14:15] op_sel_hi:[1,0]
	v_pk_mul_f32 v[16:17], v[158:159], v[14:15] op_sel_hi:[1,0]
	v_pk_mul_f32 v[20:21], v[154:155], v[14:15] op_sel_hi:[1,0]
	v_pk_mul_f32 v[24:25], v[150:151], v[14:15] op_sel_hi:[1,0]
	v_pk_mul_f32 v[26:27], v[148:149], v[14:15] op_sel_hi:[1,0]
	v_pk_mul_f32 v[28:29], v[146:147], v[14:15] op_sel_hi:[1,0]
	v_pk_mul_f32 v[14:15], v[144:145], v[14:15] op_sel_hi:[1,0]
	v_med3_f32 v7, v18, s61, v192
	v_med3_f32 v18, v22, s61, v192
	v_med3_f32 v19, v19, s61, v192
	v_med3_f32 v22, v23, s61, v192
	v_med3_f32 v23, v26, s61, v192
	v_med3_f32 v14, v14, s61, v192
	v_med3_f32 v26, v27, s61, v192
	v_med3_f32 v15, v15, s61, v192
	v_cvt_pk_fp8_f32 v8, v7, v19
	v_cvt_pk_fp8_f32 v9, v18, v22
	v_cvt_pk_fp8_f32 v10, v23, v26
	v_cvt_pk_fp8_f32 v11, v14, v15
	v_med3_f32 v16, v16, s61, v192
	v_med3_f32 v20, v20, s61, v192
	v_med3_f32 v17, v17, s61, v192
	v_med3_f32 v21, v21, s61, v192
	v_med3_f32 v24, v24, s61, v192
	v_med3_f32 v27, v28, s61, v192
	v_med3_f32 v25, v25, s61, v192
	v_med3_f32 v28, v29, s61, v192
	v_cvt_pk_fp8_f32 v8, v16, v17 op_sel:[0,0,1]
	v_cvt_pk_fp8_f32 v9, v20, v21 op_sel:[0,0,1]
	v_cvt_pk_fp8_f32 v10, v24, v25 op_sel:[0,0,1]
	v_cvt_pk_fp8_f32 v11, v27, v28 op_sel:[0,0,1]
	v_lshl_add_u64 v[14:15], v[12:13], 2, s[4:5]
	global_store_dwordx2 v[2:3], v[8:9], off
	global_store_dwordx2 v[2:3], v[10:11], off offset:128
	v_mov_b32_e32 v8, 0
	v_mov_b32_e32 v9, 0
	v_mov_b32_e32 v10, 0
	v_mov_b32_e32 v11, 0
	v_lshlrev_b64 v[12:13], 10, v[12:13]
	v_or_b32_e32 v14, 32, v6
	v_lshl_add_u64 v[12:13], s[8:9], 0, v[12:13]
	v_ashrrev_i32_e32 v15, 31, v14
	v_lshl_add_u64 v[12:13], v[12:13], 0, v[4:5]
	v_lshl_add_u64 v[16:17], v[14:15], 2, s[4:5]
	v_or_b32_e32 v6, 48, v6
	v_mul_f32_e32 v7, 0x3d000000, v194
	v_mul_f32_e32 v18, 0x42000000, v7
	v_pk_mul_f32 v[22:23], v[140:141], v[18:19] op_sel_hi:[1,0]
	v_pk_mul_f32 v[26:27], v[136:137], v[18:19] op_sel_hi:[1,0]
	v_pk_mul_f32 v[20:21], v[142:143], v[18:19] op_sel_hi:[1,0]
	v_pk_mul_f32 v[24:25], v[138:139], v[18:19] op_sel_hi:[1,0]
	v_pk_mul_f32 v[28:29], v[134:135], v[18:19] op_sel_hi:[1,0]
	v_pk_mul_f32 v[30:31], v[132:133], v[18:19] op_sel_hi:[1,0]
	v_pk_mul_f32 v[130:131], v[130:131], v[18:19] op_sel_hi:[1,0]
	v_pk_mul_f32 v[18:19], v[128:129], v[18:19] op_sel_hi:[1,0]
	v_med3_f32 v7, v22, s61, v192
	v_med3_f32 v22, v26, s61, v192
	v_med3_f32 v23, v23, s61, v192
	v_med3_f32 v26, v27, s61, v192
	v_med3_f32 v27, v30, s61, v192
	v_med3_f32 v18, v18, s61, v192
	v_med3_f32 v30, v31, s61, v192
	v_med3_f32 v19, v19, s61, v192
	v_cvt_pk_fp8_f32 v8, v7, v23
	v_cvt_pk_fp8_f32 v9, v22, v26
	v_cvt_pk_fp8_f32 v10, v27, v30
	v_cvt_pk_fp8_f32 v11, v18, v19
	v_med3_f32 v20, v20, s61, v192
	v_med3_f32 v24, v24, s61, v192
	v_med3_f32 v21, v21, s61, v192
	v_med3_f32 v25, v25, s61, v192
	v_med3_f32 v28, v28, s61, v192
	v_med3_f32 v31, v130, s61, v192
	v_med3_f32 v29, v29, s61, v192
	v_med3_f32 v128, v131, s61, v192
	v_cvt_pk_fp8_f32 v8, v20, v21 op_sel:[0,0,1]
	v_cvt_pk_fp8_f32 v9, v24, v25 op_sel:[0,0,1]
	v_cvt_pk_fp8_f32 v10, v28, v29 op_sel:[0,0,1]
	v_cvt_pk_fp8_f32 v11, v31, v128 op_sel:[0,0,1]
	global_store_dwordx2 v[12:13], v[8:9], off
	global_store_dwordx2 v[12:13], v[10:11], off offset:128
	v_mov_b32_e32 v8, 0
	v_mov_b32_e32 v9, 0
	v_mov_b32_e32 v10, 0
	v_mov_b32_e32 v11, 0
	v_lshlrev_b64 v[12:13], 10, v[14:15]
	v_lshl_add_u64 v[12:13], s[8:9], 0, v[12:13]
	v_ashrrev_i32_e32 v7, 31, v6
	v_lshl_add_u64 v[12:13], v[12:13], 0, v[4:5]
	v_lshl_add_u64 v[14:15], v[6:7], 2, s[4:5]
	v_lshlrev_b64 v[6:7], 10, v[6:7]
	v_lshl_add_u64 v[6:7], s[8:9], 0, v[6:7]
	v_lshl_add_u64 v[4:5], v[6:7], 0, v[4:5]
	v_mov_b32_e32 v6, 0
	v_mov_b32_e32 v7, 0
	v_mul_f32_e32 v16, 0x3d000000, v195
	v_mul_f32_e32 v16, 0x42000000, v16
	v_pk_mul_f32 v[20:21], v[124:125], v[16:17] op_sel_hi:[1,0]
	v_pk_mul_f32 v[24:25], v[120:121], v[16:17] op_sel_hi:[1,0]
	v_pk_mul_f32 v[18:19], v[126:127], v[16:17] op_sel_hi:[1,0]
	v_pk_mul_f32 v[22:23], v[122:123], v[16:17] op_sel_hi:[1,0]
	v_pk_mul_f32 v[26:27], v[118:119], v[16:17] op_sel_hi:[1,0]
	v_pk_mul_f32 v[28:29], v[116:117], v[16:17] op_sel_hi:[1,0]
	v_pk_mul_f32 v[30:31], v[114:115], v[16:17] op_sel_hi:[1,0]
	v_pk_mul_f32 v[16:17], v[112:113], v[16:17] op_sel_hi:[1,0]
	v_med3_f32 v20, v20, s61, v192
	v_med3_f32 v24, v24, s61, v192
	v_med3_f32 v21, v21, s61, v192
	v_med3_f32 v25, v25, s61, v192
	v_med3_f32 v28, v28, s61, v192
	v_med3_f32 v16, v16, s61, v192
	v_med3_f32 v29, v29, s61, v192
	v_med3_f32 v17, v17, s61, v192
	v_cvt_pk_fp8_f32 v8, v20, v21
	v_cvt_pk_fp8_f32 v9, v24, v25
	v_cvt_pk_fp8_f32 v10, v28, v29
	v_cvt_pk_fp8_f32 v11, v16, v17
	v_med3_f32 v18, v18, s61, v192
	v_med3_f32 v22, v22, s61, v192
	v_med3_f32 v19, v19, s61, v192
	v_med3_f32 v23, v23, s61, v192
	v_med3_f32 v26, v26, s61, v192
	v_med3_f32 v30, v30, s61, v192
	v_med3_f32 v27, v27, s61, v192
	v_med3_f32 v31, v31, s61, v192
	v_cvt_pk_fp8_f32 v8, v18, v19 op_sel:[0,0,1]
	v_cvt_pk_fp8_f32 v9, v22, v23 op_sel:[0,0,1]
	v_cvt_pk_fp8_f32 v10, v26, v27 op_sel:[0,0,1]
	v_cvt_pk_fp8_f32 v11, v30, v31 op_sel:[0,0,1]
	global_store_dwordx2 v[12:13], v[8:9], off
	global_store_dwordx2 v[12:13], v[10:11], off offset:128
	v_mov_b32_e32 v8, 0
	v_mov_b32_e32 v9, 0
	v_mov_b32_e32 v10, 0
	v_mov_b32_e32 v11, 0
	v_mul_f32_e32 v12, 0x3d000000, v196
	v_mul_f32_e32 v12, 0x42000000, v12
	v_pk_mul_f32 v[16:17], v[108:109], v[12:13] op_sel_hi:[1,0]
	v_pk_mul_f32 v[20:21], v[104:105], v[12:13] op_sel_hi:[1,0]
	v_pk_mul_f32 v[14:15], v[110:111], v[12:13] op_sel_hi:[1,0]
	v_pk_mul_f32 v[18:19], v[106:107], v[12:13] op_sel_hi:[1,0]
	v_pk_mul_f32 v[22:23], v[102:103], v[12:13] op_sel_hi:[1,0]
	v_pk_mul_f32 v[24:25], v[100:101], v[12:13] op_sel_hi:[1,0]
	v_pk_mul_f32 v[26:27], v[98:99], v[12:13] op_sel_hi:[1,0]
	v_pk_mul_f32 v[12:13], v[96:97], v[12:13] op_sel_hi:[1,0]
	v_med3_f32 v16, v16, s61, v192
	v_med3_f32 v20, v20, s61, v192
	v_med3_f32 v17, v17, s61, v192
	v_med3_f32 v21, v21, s61, v192
	v_med3_f32 v24, v24, s61, v192
	v_med3_f32 v12, v12, s61, v192
	v_med3_f32 v25, v25, s61, v192
	v_med3_f32 v13, v13, s61, v192
	v_cvt_pk_fp8_f32 v8, v16, v17
	v_cvt_pk_fp8_f32 v9, v20, v21
	v_cvt_pk_fp8_f32 v10, v24, v25
	v_cvt_pk_fp8_f32 v11, v12, v13
	v_med3_f32 v14, v14, s61, v192
	v_med3_f32 v18, v18, s61, v192
	v_med3_f32 v15, v15, s61, v192
	v_med3_f32 v19, v19, s61, v192
	v_med3_f32 v22, v22, s61, v192
	v_med3_f32 v26, v26, s61, v192
	v_med3_f32 v23, v23, s61, v192
	v_med3_f32 v27, v27, s61, v192
	v_cvt_pk_fp8_f32 v8, v14, v15 op_sel:[0,0,1]
	v_cvt_pk_fp8_f32 v9, v18, v19 op_sel:[0,0,1]
	v_cvt_pk_fp8_f32 v10, v22, v23 op_sel:[0,0,1]
	v_cvt_pk_fp8_f32 v11, v26, v27 op_sel:[0,0,1]
	global_store_dwordx2 v[4:5], v[8:9], off
	global_store_dwordx2 v[4:5], v[10:11], off offset:128
	v_mov_b32_e32 v4, 0
	v_mov_b32_e32 v5, 0
	v_lshl_add_u64 v[8:9], v[2:3], 0, s[12:13]
	v_mul_f32_e32 v10, 0x3d000000, v197
	v_mul_f32_e32 v10, 0x42000000, v10
	v_pk_mul_f32 v[14:15], v[92:93], v[10:11] op_sel_hi:[1,0]
	v_pk_mul_f32 v[18:19], v[88:89], v[10:11] op_sel_hi:[1,0]
	v_pk_mul_f32 v[12:13], v[94:95], v[10:11] op_sel_hi:[1,0]
	v_pk_mul_f32 v[16:17], v[90:91], v[10:11] op_sel_hi:[1,0]
	v_pk_mul_f32 v[20:21], v[86:87], v[10:11] op_sel_hi:[1,0]
	v_pk_mul_f32 v[22:23], v[84:85], v[10:11] op_sel_hi:[1,0]
	v_pk_mul_f32 v[24:25], v[82:83], v[10:11] op_sel_hi:[1,0]
	v_pk_mul_f32 v[10:11], v[80:81], v[10:11] op_sel_hi:[1,0]
	v_med3_f32 v14, v14, s61, v192
	v_med3_f32 v18, v18, s61, v192
	v_med3_f32 v15, v15, s61, v192
	v_med3_f32 v19, v19, s61, v192
	v_med3_f32 v22, v22, s61, v192
	v_med3_f32 v10, v10, s61, v192
	v_med3_f32 v23, v23, s61, v192
	v_med3_f32 v11, v11, s61, v192
	v_cvt_pk_fp8_f32 v4, v14, v15
	v_cvt_pk_fp8_f32 v5, v18, v19
	v_cvt_pk_fp8_f32 v6, v22, v23
	v_cvt_pk_fp8_f32 v7, v10, v11
	v_med3_f32 v12, v12, s61, v192
	v_med3_f32 v16, v16, s61, v192
	v_med3_f32 v13, v13, s61, v192
	v_med3_f32 v17, v17, s61, v192
	v_med3_f32 v20, v20, s61, v192
	v_med3_f32 v24, v24, s61, v192
	v_med3_f32 v21, v21, s61, v192
	v_med3_f32 v25, v25, s61, v192
	v_cvt_pk_fp8_f32 v4, v12, v13 op_sel:[0,0,1]
	v_cvt_pk_fp8_f32 v5, v16, v17 op_sel:[0,0,1]
	v_cvt_pk_fp8_f32 v6, v20, v21 op_sel:[0,0,1]
	v_cvt_pk_fp8_f32 v7, v24, v25 op_sel:[0,0,1]
	v_add_co_u32_e32 v10, vcc, s0, v2
	s_mov_b32 s0, s22
	s_nop 0
	v_addc_co_u32_e32 v11, vcc, 0, v3, vcc
	global_store_dwordx2 v[10:11], v[4:5], off
	global_store_dwordx2 v[8:9], v[6:7], off offset:128
	v_mov_b32_e32 v4, 0
	v_mov_b32_e32 v5, 0
	v_mov_b32_e32 v6, 0
	v_mov_b32_e32 v7, 0
	v_lshl_add_u64 v[8:9], v[2:3], 0, s[14:15]
	v_mul_f32_e32 v10, 0x3d000000, v198
	v_mul_f32_e32 v10, 0x42000000, v10
	v_pk_mul_f32 v[14:15], v[76:77], v[10:11] op_sel_hi:[1,0]
	v_pk_mul_f32 v[18:19], v[72:73], v[10:11] op_sel_hi:[1,0]
	v_pk_mul_f32 v[12:13], v[78:79], v[10:11] op_sel_hi:[1,0]
	v_pk_mul_f32 v[16:17], v[74:75], v[10:11] op_sel_hi:[1,0]
	v_pk_mul_f32 v[20:21], v[70:71], v[10:11] op_sel_hi:[1,0]
	v_pk_mul_f32 v[22:23], v[68:69], v[10:11] op_sel_hi:[1,0]
	v_pk_mul_f32 v[24:25], v[66:67], v[10:11] op_sel_hi:[1,0]
	v_pk_mul_f32 v[10:11], v[64:65], v[10:11] op_sel_hi:[1,0]
	v_med3_f32 v14, v14, s61, v192
	v_med3_f32 v18, v18, s61, v192
	v_med3_f32 v15, v15, s61, v192
	v_med3_f32 v19, v19, s61, v192
	v_med3_f32 v22, v22, s61, v192
	v_med3_f32 v10, v10, s61, v192
	v_med3_f32 v23, v23, s61, v192
	v_med3_f32 v11, v11, s61, v192
	v_cvt_pk_fp8_f32 v4, v14, v15
	v_cvt_pk_fp8_f32 v5, v18, v19
	v_cvt_pk_fp8_f32 v6, v22, v23
	v_cvt_pk_fp8_f32 v7, v10, v11
	v_med3_f32 v12, v12, s61, v192
	v_med3_f32 v16, v16, s61, v192
	v_med3_f32 v13, v13, s61, v192
	v_med3_f32 v17, v17, s61, v192
	v_med3_f32 v20, v20, s61, v192
	v_med3_f32 v24, v24, s61, v192
	v_med3_f32 v21, v21, s61, v192
	v_med3_f32 v25, v25, s61, v192
	v_cvt_pk_fp8_f32 v4, v12, v13 op_sel:[0,0,1]
	v_cvt_pk_fp8_f32 v5, v16, v17 op_sel:[0,0,1]
	v_cvt_pk_fp8_f32 v6, v20, v21 op_sel:[0,0,1]
	v_cvt_pk_fp8_f32 v7, v24, v25 op_sel:[0,0,1]
	v_add_co_u32_e32 v10, vcc, s62, v2
	s_nop 1
	v_addc_co_u32_e32 v11, vcc, 0, v3, vcc
	global_store_dwordx2 v[10:11], v[4:5], off
	global_store_dwordx2 v[8:9], v[6:7], off offset:128
	v_mov_b32_e32 v4, 0
	v_mov_b32_e32 v5, 0
	v_mov_b32_e32 v6, 0
	v_mov_b32_e32 v7, 0
	v_lshl_add_u64 v[8:9], v[2:3], 0, s[16:17]
	v_mul_f32_e32 v10, 0x3d000000, v199
	v_mul_f32_e32 v10, 0x42000000, v10
	v_pk_mul_f32 v[14:15], v[60:61], v[10:11] op_sel_hi:[1,0]
	v_pk_mul_f32 v[18:19], v[56:57], v[10:11] op_sel_hi:[1,0]
	v_pk_mul_f32 v[12:13], v[62:63], v[10:11] op_sel_hi:[1,0]
	v_pk_mul_f32 v[16:17], v[58:59], v[10:11] op_sel_hi:[1,0]
	v_pk_mul_f32 v[20:21], v[54:55], v[10:11] op_sel_hi:[1,0]
	v_pk_mul_f32 v[22:23], v[52:53], v[10:11] op_sel_hi:[1,0]
	v_pk_mul_f32 v[24:25], v[50:51], v[10:11] op_sel_hi:[1,0]
	v_pk_mul_f32 v[10:11], v[48:49], v[10:11] op_sel_hi:[1,0]
	v_med3_f32 v14, v14, s61, v192
	v_med3_f32 v18, v18, s61, v192
	v_med3_f32 v15, v15, s61, v192
	v_med3_f32 v19, v19, s61, v192
	v_med3_f32 v22, v22, s61, v192
	v_med3_f32 v10, v10, s61, v192
	v_med3_f32 v23, v23, s61, v192
	v_med3_f32 v11, v11, s61, v192
	v_cvt_pk_fp8_f32 v4, v14, v15
	v_cvt_pk_fp8_f32 v5, v18, v19
	v_cvt_pk_fp8_f32 v6, v22, v23
	v_cvt_pk_fp8_f32 v7, v10, v11
	v_med3_f32 v12, v12, s61, v192
	v_med3_f32 v16, v16, s61, v192
	v_med3_f32 v13, v13, s61, v192
	v_med3_f32 v17, v17, s61, v192
	v_med3_f32 v20, v20, s61, v192
	v_med3_f32 v24, v24, s61, v192
	v_med3_f32 v21, v21, s61, v192
	v_med3_f32 v25, v25, s61, v192
	v_cvt_pk_fp8_f32 v4, v12, v13 op_sel:[0,0,1]
	v_cvt_pk_fp8_f32 v5, v16, v17 op_sel:[0,0,1]
	v_cvt_pk_fp8_f32 v6, v20, v21 op_sel:[0,0,1]
	v_cvt_pk_fp8_f32 v7, v24, v25 op_sel:[0,0,1]
	v_add_co_u32_e32 v10, vcc, s63, v2
	s_nop 1
	v_addc_co_u32_e32 v11, vcc, 0, v3, vcc
	global_store_dwordx2 v[10:11], v[4:5], off
	global_store_dwordx2 v[8:9], v[6:7], off offset:128
	v_mov_b32_e32 v0, 0
	v_mov_b32_e32 v1, 0
	v_mov_b32_e32 v4, 0
	v_mov_b32_e32 v5, 0
	v_lshl_add_u64 v[6:7], v[2:3], 0, s[18:19]
	v_add_co_u32_e64 v2, s[6:7], s64, v2
	s_and_b64 vcc, exec, s[10:11]
	s_nop 0
	v_addc_co_u32_e64 v3, s[6:7], 0, v3, s[6:7]
	v_mul_f32_e32 v8, 0x3d000000, v200
	v_mul_f32_e32 v8, 0x42000000, v8
	v_pk_mul_f32 v[12:13], v[44:45], v[8:9] op_sel_hi:[1,0]
	v_pk_mul_f32 v[16:17], v[40:41], v[8:9] op_sel_hi:[1,0]
	v_pk_mul_f32 v[10:11], v[46:47], v[8:9] op_sel_hi:[1,0]
	v_pk_mul_f32 v[14:15], v[42:43], v[8:9] op_sel_hi:[1,0]
	v_pk_mul_f32 v[18:19], v[38:39], v[8:9] op_sel_hi:[1,0]
	v_pk_mul_f32 v[20:21], v[36:37], v[8:9] op_sel_hi:[1,0]
	v_pk_mul_f32 v[22:23], v[34:35], v[8:9] op_sel_hi:[1,0]
	v_pk_mul_f32 v[8:9], v[32:33], v[8:9] op_sel_hi:[1,0]
	v_med3_f32 v12, v12, s61, v192
	v_med3_f32 v16, v16, s61, v192
	v_med3_f32 v13, v13, s61, v192
	v_med3_f32 v17, v17, s61, v192
	v_med3_f32 v20, v20, s61, v192
	v_med3_f32 v8, v8, s61, v192
	v_med3_f32 v21, v21, s61, v192
	v_med3_f32 v9, v9, s61, v192
	v_cvt_pk_fp8_f32 v0, v12, v13
	v_cvt_pk_fp8_f32 v1, v16, v17
	v_cvt_pk_fp8_f32 v4, v20, v21
	v_cvt_pk_fp8_f32 v5, v8, v9
	v_med3_f32 v10, v10, s61, v192
	v_med3_f32 v14, v14, s61, v192
	v_med3_f32 v11, v11, s61, v192
	v_med3_f32 v15, v15, s61, v192
	v_med3_f32 v18, v18, s61, v192
	v_med3_f32 v22, v22, s61, v192
	v_med3_f32 v19, v19, s61, v192
	v_med3_f32 v23, v23, s61, v192
	v_cvt_pk_fp8_f32 v0, v10, v11 op_sel:[0,0,1]
	v_cvt_pk_fp8_f32 v1, v14, v15 op_sel:[0,0,1]
	v_cvt_pk_fp8_f32 v4, v18, v19 op_sel:[0,0,1]
	v_cvt_pk_fp8_f32 v5, v22, v23 op_sel:[0,0,1]
	global_store_dwordx2 v[2:3], v[0:1], off
	global_store_dwordx2 v[6:7], v[4:5], off offset:128
	s_cbranch_vccz .LBB0_3024
	s_waitcnt vmcnt(0)
	s_cmpk_gt_u32 s40, 0xff
	v_readlane_b32 s58, v242, 45
	v_readlane_b32 s59, v242, 46
	s_cbranch_scc1 .LBB0_3031
	s_barrier

.LBB0_3167:
	s_ashr_i32 s27, s26, 31
	s_lshl_b64 s[28:29], s[26:27], 19
	s_add_u32 s28, s42, s28
	s_addc_u32 s29, s43, s29
	s_ashr_i32 s23, s22, 31
	s_lshl_b64 s[30:31], s[22:23], 19
	s_add_u32 s30, s44, s30
	s_addc_u32 s31, s45, s31
	s_and_b64 s[34:35], s[10:11], exec
	v_mov_b32_e32 v0, 0
	s_cselect_b32 s23, s31, s21
	s_cselect_b32 s27, s30, s20
	s_mov_b32 s67, -2
	s_mov_b64 s[34:35], 0
	v_mov_b32_e32 v1, 0
	v_mov_b64_e32 v[2:3], 0
	v_mov_b64_e32 v[4:5], 0
	v_mov_b64_e32 v[6:7], 0
	v_mov_b64_e32 v[8:9], 0
	v_mov_b64_e32 v[10:11], 0
	v_mov_b64_e32 v[12:13], 0
	v_mov_b64_e32 v[14:15], 0
	v_mov_b64_e32 v[16:17], 0
	v_mov_b64_e32 v[18:19], 0
	v_mov_b64_e32 v[20:21], 0
	v_mov_b64_e32 v[22:23], 0
	v_mov_b64_e32 v[24:25], 0
	v_mov_b64_e32 v[26:27], 0
	v_mov_b64_e32 v[28:29], 0
	v_mov_b64_e32 v[30:31], 0
	v_mov_b64_e32 v[32:33], 0
	v_mov_b64_e32 v[34:35], 0
	v_mov_b64_e32 v[36:37], 0
	v_mov_b64_e32 v[38:39], 0
	v_mov_b64_e32 v[40:41], 0
	v_mov_b64_e32 v[42:43], 0
	v_mov_b64_e32 v[44:45], 0
	v_mov_b64_e32 v[46:47], 0
	v_mov_b64_e32 v[48:49], 0
	v_mov_b64_e32 v[50:51], 0
	v_mov_b64_e32 v[52:53], 0
	v_mov_b64_e32 v[54:55], 0
	v_mov_b64_e32 v[56:57], 0
	v_mov_b64_e32 v[58:59], 0
	v_mov_b64_e32 v[60:61], 0
	v_mov_b64_e32 v[62:63], 0
	v_mov_b64_e32 v[64:65], 0
	v_mov_b64_e32 v[66:67], 0
	v_mov_b64_e32 v[68:69], 0
	v_mov_b64_e32 v[70:71], 0
	v_mov_b64_e32 v[72:73], 0
	v_mov_b64_e32 v[74:75], 0
	v_mov_b64_e32 v[76:77], 0
	v_mov_b64_e32 v[78:79], 0
	v_mov_b64_e32 v[80:81], 0
	v_mov_b64_e32 v[82:83], 0
	v_mov_b64_e32 v[84:85], 0
	v_mov_b64_e32 v[86:87], 0
	v_mov_b64_e32 v[88:89], 0
	v_mov_b64_e32 v[90:91], 0
	v_mov_b64_e32 v[92:93], 0
	v_mov_b64_e32 v[94:95], 0
	v_mov_b64_e32 v[96:97], 0
	v_mov_b64_e32 v[98:99], 0
	v_mov_b64_e32 v[100:101], 0
	v_mov_b64_e32 v[102:103], 0
	v_mov_b64_e32 v[104:105], 0
	v_mov_b64_e32 v[106:107], 0
	v_mov_b64_e32 v[108:109], 0
	v_mov_b64_e32 v[110:111], 0
	v_mov_b64_e32 v[112:113], 0
	v_mov_b64_e32 v[114:115], 0
	v_mov_b64_e32 v[116:117], 0
	v_mov_b64_e32 v[118:119], 0
	v_mov_b64_e32 v[120:121], 0
	v_mov_b64_e32 v[122:123], 0
	v_mov_b64_e32 v[124:125], 0
	v_mov_b64_e32 v[126:127], 0

.LBB0_3520:
	s_ashr_i32 s35, s34, 31
	s_lshl_b64 s[36:37], s[34:35], 19
	s_add_u32 s36, s53, s36
	s_addc_u32 s37, s54, s37
	s_ashr_i32 s31, s30, 31
	s_lshl_b64 s[38:39], s[30:31], 19
	s_add_u32 s38, s55, s38
	s_addc_u32 s39, s56, s39
	s_and_b64 s[44:45], s[6:7], exec
	v_mov_b32_e32 v0, 0
	s_cselect_b32 s1, s39, s41
	s_cselect_b32 s3, s38, s40
	s_mov_b32 s16, -2
	s_mov_b64 s[44:45], 0
	s_waitcnt lgkmcnt(0)
	v_mov_b32_e32 v1, 0
	v_mov_b64_e32 v[2:3], 0
	v_mov_b64_e32 v[4:5], 0
	v_mov_b64_e32 v[6:7], 0
	v_mov_b64_e32 v[8:9], 0
	v_mov_b64_e32 v[10:11], 0
	v_mov_b64_e32 v[12:13], 0
	v_mov_b64_e32 v[14:15], 0
	v_mov_b64_e32 v[16:17], 0
	v_mov_b64_e32 v[18:19], 0
	v_mov_b64_e32 v[20:21], 0
	v_mov_b64_e32 v[22:23], 0
	v_mov_b64_e32 v[24:25], 0
	v_mov_b64_e32 v[26:27], 0
	v_mov_b64_e32 v[28:29], 0
	v_mov_b64_e32 v[30:31], 0
	v_mov_b64_e32 v[32:33], 0
	v_mov_b64_e32 v[34:35], 0
	v_mov_b64_e32 v[36:37], 0
	v_mov_b64_e32 v[38:39], 0
	v_mov_b64_e32 v[40:41], 0
	v_mov_b64_e32 v[42:43], 0
	v_mov_b64_e32 v[44:45], 0
	v_mov_b64_e32 v[46:47], 0
	v_mov_b64_e32 v[48:49], 0
	v_mov_b64_e32 v[50:51], 0
	v_mov_b64_e32 v[52:53], 0
	v_mov_b64_e32 v[54:55], 0
	v_mov_b64_e32 v[56:57], 0
	v_mov_b64_e32 v[58:59], 0
	v_mov_b64_e32 v[60:61], 0
	v_mov_b64_e32 v[62:63], 0
	v_mov_b64_e32 v[64:65], 0
	v_mov_b64_e32 v[66:67], 0
	v_mov_b64_e32 v[68:69], 0
	v_mov_b64_e32 v[70:71], 0
	v_mov_b64_e32 v[96:97], 0
	v_mov_b64_e32 v[98:99], 0
	v_mov_b64_e32 v[100:101], 0
	v_mov_b64_e32 v[102:103], 0
	v_mov_b64_e32 v[112:113], 0
	v_mov_b32_e32 v114, 0
	s_waitcnt vmcnt(0)
	v_mov_b64_e32 v[72:73], 0
	v_mov_b64_e32 v[74:75], 0
	v_mov_b64_e32 v[76:77], 0
	v_mov_b64_e32 v[78:79], 0
	v_mov_b64_e32 v[104:105], 0
	v_mov_b64_e32 v[106:107], 0
	v_mov_b64_e32 v[108:109], 0
	v_mov_b64_e32 v[110:111], 0
	v_mov_b32_e32 v115, 0
	v_mov_b64_e32 v[116:117], 0
	v_mov_b64_e32 v[118:119], 0
	v_mov_b64_e32 v[120:121], 0
	v_mov_b64_e32 v[122:123], 0
	v_mov_b64_e32 v[124:125], 0
	v_mov_b64_e32 v[126:127], 0
	v_mov_b64_e32 v[128:129], 0
	v_mov_b64_e32 v[130:131], 0
	v_mov_b64_e32 v[132:133], 0
	v_mov_b64_e32 v[134:135], 0
	v_mov_b64_e32 v[136:137], 0
	v_mov_b64_e32 v[138:139], 0
	v_mov_b64_e32 v[140:141], 0
	v_mov_b64_e32 v[142:143], 0

.LBB0_3910:
	v_mov_b32_e32 v0, v209
	s_nop 15
	s_nop 15
	s_mov_b32 s101, 0x44800000
	s_ashr_i32 s2, s0, 31
	v_ashrrev_i32_e32 v1, 2, v0
	v_and_b32_e32 v1, 0xffffffc0, v1
	v_lshl_add_u32 v1, s33, 8, v1
	v_and_or_b32 v4, v0, 15, v1
	v_lshrrev_b32_e32 v2, 1, v0
	s_lshr_b32 s2, s2, 29
	s_add_i32 s2, s0, s2
	s_and_b32 s2, s2, 0x1fffff8
	s_sub_i32 s0, s0, s2
	v_and_b32_e32 v2, 0x78, v2
	v_ashrrev_i32_e32 v5, 31, v4
	v_lshl_or_b32 v2, s0, 7, v2
	v_lshlrev_b64 v[0:1], 10, v[4:5]
	v_ashrrev_i32_e32 v3, 31, v2
	v_lshl_add_u64 v[0:1], s[12:13], 0, v[0:1]
	v_lshl_add_u64 v[0:1], v[0:1], 0, v[2:3]
	v_mul_f32_e32 v10, 0xbd38aa3b, v188
	v_mul_f32_e32 v11, 0xbd38aa3b, v189
	v_mul_f32_e32 v12, 0xbd38aa3b, v190
	v_mul_f32_e32 v13, 0xbd38aa3b, v191
	v_mul_f32_e32 v14, 0xbd38aa3b, v180
	v_mul_f32_e32 v15, 0xbd38aa3b, v181
	v_mul_f32_e32 v16, 0xbd38aa3b, v182
	v_mul_f32_e32 v17, 0xbd38aa3b, v183
	v_exp_f32_e32 v10, v10
	v_exp_f32_e32 v11, v11
	v_exp_f32_e32 v12, v12
	v_exp_f32_e32 v13, v13
	v_exp_f32_e32 v14, v14
	v_exp_f32_e32 v15, v15
	v_exp_f32_e32 v16, v16
	v_exp_f32_e32 v17, v17
	v_fma_f32 v10, v10, s101, s101
	v_fma_f32 v11, v11, s101, s101
	v_fma_f32 v12, v12, s101, s101
	v_fma_f32 v13, v13, s101, s101
	v_fma_f32 v14, v14, s101, s101
	v_fma_f32 v15, v15, s101, s101
	v_fma_f32 v16, v16, s101, s101
	v_fma_f32 v17, v17, s101, s101
	v_rcp_f32_e32 v10, v10
	v_rcp_f32_e32 v11, v11
	v_rcp_f32_e32 v12, v12
	v_rcp_f32_e32 v13, v13
	v_rcp_f32_e32 v14, v14
	v_rcp_f32_e32 v15, v15
	v_rcp_f32_e32 v16, v16
	v_rcp_f32_e32 v17, v17
	v_mul_f32_e32 v10, v188, v10
	v_mul_f32_e32 v11, v189, v11
	v_mul_f32_e32 v12, v190, v12
	v_mul_f32_e32 v13, v191, v13
	v_mul_f32_e32 v14, v180, v14
	v_mul_f32_e32 v15, v181, v15
	v_mul_f32_e32 v16, v182, v16
	v_mul_f32_e32 v17, v183, v17
	v_mul_f32_e32 v10, v10, v184
	v_mul_f32_e32 v11, v11, v185
	v_mul_f32_e32 v12, v12, v186
	v_mul_f32_e32 v13, v13, v187
	v_mul_f32_e32 v14, v14, v176
	v_mul_f32_e32 v15, v15, v177
	v_mul_f32_e32 v16, v16, v178
	v_mul_f32_e32 v17, v17, v179
	v_cvt_pk_fp8_f32 v18, v10, v11
	v_cvt_pk_fp8_f32 v19, v14, v15
	v_cvt_pk_fp8_f32 v18, v12, v13 op_sel:[0,0,1]
	v_cvt_pk_fp8_f32 v19, v16, v17 op_sel:[0,0,1]
	s_nop 0
	global_store_dwordx2 v[0:1], v[18:19], off
	v_or_b32_e32 v8, 16, v4
	v_ashrrev_i32_e32 v9, 31, v8
	v_lshlrev_b64 v[8:9], 10, v[8:9]
	v_lshl_add_u64 v[8:9], s[12:13], 0, v[8:9]
	v_lshl_add_u64 v[8:9], v[8:9], 0, v[2:3]
	v_mul_f32_e32 v10, 0xbd38aa3b, v172
	v_mul_f32_e32 v11, 0xbd38aa3b, v173
	v_mul_f32_e32 v12, 0xbd38aa3b, v174
	v_mul_f32_e32 v13, 0xbd38aa3b, v175
	v_mul_f32_e32 v14, 0xbd38aa3b, v164
	v_mul_f32_e32 v15, 0xbd38aa3b, v165
	v_mul_f32_e32 v16, 0xbd38aa3b, v166
	v_mul_f32_e32 v17, 0xbd38aa3b, v167
	v_exp_f32_e32 v10, v10
	v_exp_f32_e32 v11, v11
	v_exp_f32_e32 v12, v12
	v_exp_f32_e32 v13, v13
	v_exp_f32_e32 v14, v14
	v_exp_f32_e32 v15, v15
	v_exp_f32_e32 v16, v16
	v_exp_f32_e32 v17, v17
	v_fma_f32 v10, v10, s101, s101
	v_fma_f32 v11, v11, s101, s101
	v_fma_f32 v12, v12, s101, s101
	v_fma_f32 v13, v13, s101, s101
	v_fma_f32 v14, v14, s101, s101
	v_fma_f32 v15, v15, s101, s101
	v_fma_f32 v16, v16, s101, s101
	v_fma_f32 v17, v17, s101, s101
	v_rcp_f32_e32 v10, v10
	v_rcp_f32_e32 v11, v11
	v_rcp_f32_e32 v12, v12
	v_rcp_f32_e32 v13, v13
	v_rcp_f32_e32 v14, v14
	v_rcp_f32_e32 v15, v15
	v_rcp_f32_e32 v16, v16
	v_rcp_f32_e32 v17, v17
	v_mul_f32_e32 v10, v172, v10
	v_mul_f32_e32 v11, v173, v11
	v_mul_f32_e32 v12, v174, v12
	v_mul_f32_e32 v13, v175, v13
	v_mul_f32_e32 v14, v164, v14
	v_mul_f32_e32 v15, v165, v15
	v_mul_f32_e32 v16, v166, v16
	v_mul_f32_e32 v17, v167, v17
	v_mul_f32_e32 v10, v10, v168
	v_mul_f32_e32 v11, v11, v169
	v_mul_f32_e32 v12, v12, v170
	v_mul_f32_e32 v13, v13, v171
	v_mul_f32_e32 v14, v14, v160
	v_mul_f32_e32 v15, v15, v161
	v_mul_f32_e32 v16, v16, v162
	v_mul_f32_e32 v17, v17, v163
	v_cvt_pk_fp8_f32 v18, v10, v11
	v_cvt_pk_fp8_f32 v19, v14, v15
	v_cvt_pk_fp8_f32 v18, v12, v13 op_sel:[0,0,1]
	v_cvt_pk_fp8_f32 v19, v16, v17 op_sel:[0,0,1]
	s_nop 0
	global_store_dwordx2 v[8:9], v[18:19], off
	v_or_b32_e32 v8, 32, v4
	v_ashrrev_i32_e32 v9, 31, v8
	v_or_b32_e32 v4, 48, v4
	v_lshlrev_b64 v[6:7], 10, v[8:9]
	v_lshl_add_u64 v[6:7], s[12:13], 0, v[6:7]
	v_lshl_add_u64 v[6:7], v[6:7], 0, v[2:3]
	v_mul_f32_e32 v10, 0xbd38aa3b, v156
	v_mul_f32_e32 v11, 0xbd38aa3b, v157
	v_mul_f32_e32 v12, 0xbd38aa3b, v158
	v_mul_f32_e32 v13, 0xbd38aa3b, v159
	v_mul_f32_e32 v14, 0xbd38aa3b, v148
	v_mul_f32_e32 v15, 0xbd38aa3b, v149
	v_mul_f32_e32 v16, 0xbd38aa3b, v150
	v_mul_f32_e32 v17, 0xbd38aa3b, v151
	v_exp_f32_e32 v10, v10
	v_exp_f32_e32 v11, v11
	v_exp_f32_e32 v12, v12
	v_exp_f32_e32 v13, v13
	v_exp_f32_e32 v14, v14
	v_exp_f32_e32 v15, v15
	v_exp_f32_e32 v16, v16
	v_exp_f32_e32 v17, v17
	v_fma_f32 v10, v10, s101, s101
	v_fma_f32 v11, v11, s101, s101
	v_fma_f32 v12, v12, s101, s101
	v_fma_f32 v13, v13, s101, s101
	v_fma_f32 v14, v14, s101, s101
	v_fma_f32 v15, v15, s101, s101
	v_fma_f32 v16, v16, s101, s101
	v_fma_f32 v17, v17, s101, s101
	v_rcp_f32_e32 v10, v10
	v_rcp_f32_e32 v11, v11
	v_rcp_f32_e32 v12, v12
	v_rcp_f32_e32 v13, v13
	v_rcp_f32_e32 v14, v14
	v_rcp_f32_e32 v15, v15
	v_rcp_f32_e32 v16, v16
	v_rcp_f32_e32 v17, v17
	v_mul_f32_e32 v10, v156, v10
	v_mul_f32_e32 v11, v157, v11
	v_mul_f32_e32 v12, v158, v12
	v_mul_f32_e32 v13, v159, v13
	v_mul_f32_e32 v14, v148, v14
	v_mul_f32_e32 v15, v149, v15
	v_mul_f32_e32 v16, v150, v16
	v_mul_f32_e32 v17, v151, v17
	v_mul_f32_e32 v10, v10, v152
	v_mul_f32_e32 v11, v11, v153
	v_mul_f32_e32 v12, v12, v154
	v_mul_f32_e32 v13, v13, v155
	v_mul_f32_e32 v14, v14, v144
	v_mul_f32_e32 v15, v15, v145
	v_mul_f32_e32 v16, v16, v146
	v_mul_f32_e32 v17, v17, v147
	v_cvt_pk_fp8_f32 v18, v10, v11
	v_cvt_pk_fp8_f32 v19, v14, v15
	v_cvt_pk_fp8_f32 v18, v12, v13 op_sel:[0,0,1]
	v_cvt_pk_fp8_f32 v19, v16, v17 op_sel:[0,0,1]
	s_nop 0
	global_store_dwordx2 v[6:7], v[18:19], off
	v_ashrrev_i32_e32 v5, 31, v4
	v_lshlrev_b64 v[4:5], 10, v[4:5]
	v_lshl_add_u64 v[4:5], s[12:13], 0, v[4:5]
	v_lshl_add_u64 v[2:3], v[4:5], 0, v[2:3]
	s_mov_b32 s33, s52
	v_mul_f32_e32 v10, 0xbd38aa3b, v140
	v_mul_f32_e32 v11, 0xbd38aa3b, v141
	v_mul_f32_e32 v12, 0xbd38aa3b, v142
	v_mul_f32_e32 v13, 0xbd38aa3b, v143
	v_mul_f32_e32 v14, 0xbd38aa3b, v132
	v_mul_f32_e32 v15, 0xbd38aa3b, v133
	v_mul_f32_e32 v16, 0xbd38aa3b, v134
	v_mul_f32_e32 v17, 0xbd38aa3b, v135
	v_exp_f32_e32 v10, v10
	v_exp_f32_e32 v11, v11
	v_exp_f32_e32 v12, v12
	v_exp_f32_e32 v13, v13
	v_exp_f32_e32 v14, v14
	v_exp_f32_e32 v15, v15
	v_exp_f32_e32 v16, v16
	v_exp_f32_e32 v17, v17
	v_fma_f32 v10, v10, s101, s101
	v_fma_f32 v11, v11, s101, s101
	v_fma_f32 v12, v12, s101, s101
	v_fma_f32 v13, v13, s101, s101
	v_fma_f32 v14, v14, s101, s101
	v_fma_f32 v15, v15, s101, s101
	v_fma_f32 v16, v16, s101, s101
	v_fma_f32 v17, v17, s101, s101
	v_rcp_f32_e32 v10, v10
	v_rcp_f32_e32 v11, v11
	v_rcp_f32_e32 v12, v12
	v_rcp_f32_e32 v13, v13
	v_rcp_f32_e32 v14, v14
	v_rcp_f32_e32 v15, v15
	v_rcp_f32_e32 v16, v16
	v_rcp_f32_e32 v17, v17
	v_mul_f32_e32 v10, v140, v10
	v_mul_f32_e32 v11, v141, v11
	v_mul_f32_e32 v12, v142, v12
	v_mul_f32_e32 v13, v143, v13
	v_mul_f32_e32 v14, v132, v14
	v_mul_f32_e32 v15, v133, v15
	v_mul_f32_e32 v16, v134, v16
	v_mul_f32_e32 v17, v135, v17
	v_mul_f32_e32 v10, v10, v136
	v_mul_f32_e32 v11, v11, v137
	v_mul_f32_e32 v12, v12, v138
	v_mul_f32_e32 v13, v13, v139
	v_mul_f32_e32 v14, v14, v128
	v_mul_f32_e32 v15, v15, v129
	v_mul_f32_e32 v16, v16, v130
	v_mul_f32_e32 v17, v17, v131
	v_cvt_pk_fp8_f32 v18, v10, v11
	v_cvt_pk_fp8_f32 v19, v14, v15
	v_cvt_pk_fp8_f32 v18, v12, v13 op_sel:[0,0,1]
	v_cvt_pk_fp8_f32 v19, v16, v17 op_sel:[0,0,1]
	s_nop 0
	global_store_dwordx2 v[2:3], v[18:19], off
	s_mov_b32 s0, s16
	v_add_co_u32_e32 v6, vcc, s49, v0
	v_addc_co_u32_e32 v7, vcc, 0, v1, vcc
	v_mul_f32_e32 v10, 0xbd38aa3b, v124
	v_mul_f32_e32 v11, 0xbd38aa3b, v125
	v_mul_f32_e32 v12, 0xbd38aa3b, v126
	v_mul_f32_e32 v13, 0xbd38aa3b, v127
	v_mul_f32_e32 v14, 0xbd38aa3b, v116
	v_mul_f32_e32 v15, 0xbd38aa3b, v117
	v_mul_f32_e32 v16, 0xbd38aa3b, v118
	v_mul_f32_e32 v17, 0xbd38aa3b, v119
	v_exp_f32_e32 v10, v10
	v_exp_f32_e32 v11, v11
	v_exp_f32_e32 v12, v12
	v_exp_f32_e32 v13, v13
	v_exp_f32_e32 v14, v14
	v_exp_f32_e32 v15, v15
	v_exp_f32_e32 v16, v16
	v_exp_f32_e32 v17, v17
	v_fma_f32 v10, v10, s101, s101
	v_fma_f32 v11, v11, s101, s101
	v_fma_f32 v12, v12, s101, s101
	v_fma_f32 v13, v13, s101, s101
	v_fma_f32 v14, v14, s101, s101
	v_fma_f32 v15, v15, s101, s101
	v_fma_f32 v16, v16, s101, s101
	v_fma_f32 v17, v17, s101, s101
	v_rcp_f32_e32 v10, v10
	v_rcp_f32_e32 v11, v11
	v_rcp_f32_e32 v12, v12
	v_rcp_f32_e32 v13, v13
	v_rcp_f32_e32 v14, v14
	v_rcp_f32_e32 v15, v15
	v_rcp_f32_e32 v16, v16
	v_rcp_f32_e32 v17, v17
	v_mul_f32_e32 v10, v124, v10
	v_mul_f32_e32 v11, v125, v11
	v_mul_f32_e32 v12, v126, v12
	v_mul_f32_e32 v13, v127, v13
	v_mul_f32_e32 v14, v116, v14
	v_mul_f32_e32 v15, v117, v15
	v_mul_f32_e32 v16, v118, v16
	v_mul_f32_e32 v17, v119, v17
	v_mul_f32_e32 v10, v10, v120
	v_mul_f32_e32 v11, v11, v121
	v_mul_f32_e32 v12, v12, v122
	v_mul_f32_e32 v13, v13, v123
	v_mul_f32_e32 v14, v14, v112
	v_mul_f32_e32 v15, v15, v113
	v_mul_f32_e32 v16, v16, v114
	v_mul_f32_e32 v17, v17, v115
	v_cvt_pk_fp8_f32 v18, v10, v11
	v_cvt_pk_fp8_f32 v19, v14, v15
	v_cvt_pk_fp8_f32 v18, v12, v13 op_sel:[0,0,1]
	v_cvt_pk_fp8_f32 v19, v16, v17 op_sel:[0,0,1]
	s_nop 0
	global_store_dwordx2 v[6:7], v[18:19], off
	v_add_co_u32_e32 v6, vcc, s50, v0
	v_addc_co_u32_e32 v7, vcc, 0, v1, vcc
	v_mul_f32_e32 v10, 0xbd38aa3b, v108
	v_mul_f32_e32 v11, 0xbd38aa3b, v109
	v_mul_f32_e32 v12, 0xbd38aa3b, v110
	v_mul_f32_e32 v13, 0xbd38aa3b, v111
	v_mul_f32_e32 v14, 0xbd38aa3b, v100
	v_mul_f32_e32 v15, 0xbd38aa3b, v101
	v_mul_f32_e32 v16, 0xbd38aa3b, v102
	v_mul_f32_e32 v17, 0xbd38aa3b, v103
	v_exp_f32_e32 v10, v10
	v_exp_f32_e32 v11, v11
	v_exp_f32_e32 v12, v12
	v_exp_f32_e32 v13, v13
	v_exp_f32_e32 v14, v14
	v_exp_f32_e32 v15, v15
	v_exp_f32_e32 v16, v16
	v_exp_f32_e32 v17, v17
	v_fma_f32 v10, v10, s101, s101
	v_fma_f32 v11, v11, s101, s101
	v_fma_f32 v12, v12, s101, s101
	v_fma_f32 v13, v13, s101, s101
	v_fma_f32 v14, v14, s101, s101
	v_fma_f32 v15, v15, s101, s101
	v_fma_f32 v16, v16, s101, s101
	v_fma_f32 v17, v17, s101, s101
	v_rcp_f32_e32 v10, v10
	v_rcp_f32_e32 v11, v11
	v_rcp_f32_e32 v12, v12
	v_rcp_f32_e32 v13, v13
	v_rcp_f32_e32 v14, v14
	v_rcp_f32_e32 v15, v15
	v_rcp_f32_e32 v16, v16
	v_rcp_f32_e32 v17, v17
	v_mul_f32_e32 v10, v108, v10
	v_mul_f32_e32 v11, v109, v11
	v_mul_f32_e32 v12, v110, v12
	v_mul_f32_e32 v13, v111, v13
	v_mul_f32_e32 v14, v100, v14
	v_mul_f32_e32 v15, v101, v15
	v_mul_f32_e32 v16, v102, v16
	v_mul_f32_e32 v17, v103, v17
	v_mul_f32_e32 v10, v10, v104
	v_mul_f32_e32 v11, v11, v105
	v_mul_f32_e32 v12, v12, v106
	v_mul_f32_e32 v13, v13, v107
	v_mul_f32_e32 v14, v14, v96
	v_mul_f32_e32 v15, v15, v97
	v_mul_f32_e32 v16, v16, v98
	v_mul_f32_e32 v17, v17, v99
	v_cvt_pk_fp8_f32 v18, v10, v11
	v_cvt_pk_fp8_f32 v19, v14, v15
	v_cvt_pk_fp8_f32 v18, v12, v13 op_sel:[0,0,1]
	v_cvt_pk_fp8_f32 v19, v16, v17 op_sel:[0,0,1]
	s_nop 0
	global_store_dwordx2 v[6:7], v[18:19], off
	v_add_co_u32_e32 v6, vcc, s51, v0
	v_addc_co_u32_e32 v7, vcc, 0, v1, vcc
	v_mul_f32_e32 v10, 0xbd38aa3b, v92
	v_mul_f32_e32 v11, 0xbd38aa3b, v93
	v_mul_f32_e32 v12, 0xbd38aa3b, v94
	v_mul_f32_e32 v13, 0xbd38aa3b, v95
	v_mul_f32_e32 v14, 0xbd38aa3b, v84
	v_mul_f32_e32 v15, 0xbd38aa3b, v85
	v_mul_f32_e32 v16, 0xbd38aa3b, v86
	v_mul_f32_e32 v17, 0xbd38aa3b, v87
	v_exp_f32_e32 v10, v10
	v_exp_f32_e32 v11, v11
	v_exp_f32_e32 v12, v12
	v_exp_f32_e32 v13, v13
	v_exp_f32_e32 v14, v14
	v_exp_f32_e32 v15, v15
	v_exp_f32_e32 v16, v16
	v_exp_f32_e32 v17, v17
	v_fma_f32 v10, v10, s101, s101
	v_fma_f32 v11, v11, s101, s101
	v_fma_f32 v12, v12, s101, s101
	v_fma_f32 v13, v13, s101, s101
	v_fma_f32 v14, v14, s101, s101
	v_fma_f32 v15, v15, s101, s101
	v_fma_f32 v16, v16, s101, s101
	v_fma_f32 v17, v17, s101, s101
	v_rcp_f32_e32 v10, v10
	v_rcp_f32_e32 v11, v11
	v_rcp_f32_e32 v12, v12
	v_rcp_f32_e32 v13, v13
	v_rcp_f32_e32 v14, v14
	v_rcp_f32_e32 v15, v15
	v_rcp_f32_e32 v16, v16
	v_rcp_f32_e32 v17, v17
	v_mul_f32_e32 v10, v92, v10
	v_mul_f32_e32 v11, v93, v11
	v_mul_f32_e32 v12, v94, v12
	v_mul_f32_e32 v13, v95, v13
	v_mul_f32_e32 v14, v84, v14
	v_mul_f32_e32 v15, v85, v15
	v_mul_f32_e32 v16, v86, v16
	v_mul_f32_e32 v17, v87, v17
	v_mul_f32_e32 v10, v10, v88
	v_mul_f32_e32 v11, v11, v89
	v_mul_f32_e32 v12, v12, v90
	v_mul_f32_e32 v13, v13, v91
	v_mul_f32_e32 v14, v14, v80
	v_mul_f32_e32 v15, v15, v81
	v_mul_f32_e32 v16, v16, v82
	v_mul_f32_e32 v17, v17, v83
	v_cvt_pk_fp8_f32 v18, v10, v11
	v_cvt_pk_fp8_f32 v19, v14, v15
	v_cvt_pk_fp8_f32 v18, v12, v13 op_sel:[0,0,1]
	v_cvt_pk_fp8_f32 v19, v16, v17 op_sel:[0,0,1]
	s_nop 0
	global_store_dwordx2 v[6:7], v[18:19], off
	v_add_co_u32_e32 v0, vcc, 0x2c000, v0
	s_mov_b64 s[2:3], s[18:19]
	s_nop 0
	v_addc_co_u32_e32 v1, vcc, 0, v1, vcc
	s_and_b64 vcc, exec, s[4:5]
	v_mul_f32_e32 v10, 0xbd38aa3b, v76
	v_mul_f32_e32 v11, 0xbd38aa3b, v77
	v_mul_f32_e32 v12, 0xbd38aa3b, v78
	v_mul_f32_e32 v13, 0xbd38aa3b, v79
	v_mul_f32_e32 v14, 0xbd38aa3b, v68
	v_mul_f32_e32 v15, 0xbd38aa3b, v69
	v_mul_f32_e32 v16, 0xbd38aa3b, v70
	v_mul_f32_e32 v17, 0xbd38aa3b, v71
	v_exp_f32_e32 v10, v10
	v_exp_f32_e32 v11, v11
	v_exp_f32_e32 v12, v12
	v_exp_f32_e32 v13, v13
	v_exp_f32_e32 v14, v14
	v_exp_f32_e32 v15, v15
	v_exp_f32_e32 v16, v16
	v_exp_f32_e32 v17, v17
	v_fma_f32 v10, v10, s101, s101
	v_fma_f32 v11, v11, s101, s101
	v_fma_f32 v12, v12, s101, s101
	v_fma_f32 v13, v13, s101, s101
	v_fma_f32 v14, v14, s101, s101
	v_fma_f32 v15, v15, s101, s101
	v_fma_f32 v16, v16, s101, s101
	v_fma_f32 v17, v17, s101, s101
	v_rcp_f32_e32 v10, v10
	v_rcp_f32_e32 v11, v11
	v_rcp_f32_e32 v12, v12
	v_rcp_f32_e32 v13, v13
	v_rcp_f32_e32 v14, v14
	v_rcp_f32_e32 v15, v15
	v_rcp_f32_e32 v16, v16
	v_rcp_f32_e32 v17, v17
	v_mul_f32_e32 v10, v76, v10
	v_mul_f32_e32 v11, v77, v11
	v_mul_f32_e32 v12, v78, v12
	v_mul_f32_e32 v13, v79, v13
	v_mul_f32_e32 v14, v68, v14
	v_mul_f32_e32 v15, v69, v15
	v_mul_f32_e32 v16, v70, v16
	v_mul_f32_e32 v17, v71, v17
	v_mul_f32_e32 v10, v10, v72
	v_mul_f32_e32 v11, v11, v73
	v_mul_f32_e32 v12, v12, v74
	v_mul_f32_e32 v13, v13, v75
	v_mul_f32_e32 v14, v14, v64
	v_mul_f32_e32 v15, v15, v65
	v_mul_f32_e32 v16, v16, v66
	v_mul_f32_e32 v17, v17, v67
	v_cvt_pk_fp8_f32 v18, v10, v11
	v_cvt_pk_fp8_f32 v19, v14, v15
	v_cvt_pk_fp8_f32 v18, v12, v13 op_sel:[0,0,1]
	v_cvt_pk_fp8_f32 v19, v16, v17 op_sel:[0,0,1]
	s_nop 0
	global_store_dwordx2 v[0:1], v[18:19], off
	s_cbranch_vccnz .LBB0_3917

.LBB0_3913:
	s_ashr_i32 s17, s16, 31
	s_lshl_b64 s[18:19], s[16:17], 18
	s_add_u32 s18, s28, s18
	s_addc_u32 s19, s29, s19
	s_and_b64 s[20:21], s[6:7], exec
	s_cselect_b32 s17, s19, s3
	s_cselect_b32 s53, s18, s2
	s_lshl_b32 s20, s41, 10
	s_add_i32 s20, s20, 0
	s_add_i32 s20, s20, 0x20010
	v_mov_b32_e32 v64, 0
	v_add3_u32 v233, s20, v213, v214
	v_add3_u32 v234, s20, v215, v216
	s_mov_b32 s54, -2
	s_mov_b64 s[20:21], 0xdbff000
	v_mov_b32_e32 v65, 0
	v_mov_b64_e32 v[66:67], 0
	v_mov_b64_e32 v[68:69], 0
	v_mov_b64_e32 v[70:71], 0
	v_mov_b64_e32 v[72:73], 0
	v_mov_b64_e32 v[74:75], 0
	v_mov_b64_e32 v[76:77], 0
	v_mov_b64_e32 v[78:79], 0
	v_mov_b64_e32 v[80:81], 0
	v_mov_b64_e32 v[82:83], 0
	v_mov_b64_e32 v[84:85], 0
	v_mov_b64_e32 v[86:87], 0
	v_mov_b64_e32 v[88:89], 0
	v_mov_b64_e32 v[90:91], 0
	v_mov_b64_e32 v[92:93], 0
	v_mov_b64_e32 v[94:95], 0
	v_mov_b64_e32 v[96:97], 0
	v_mov_b64_e32 v[98:99], 0
	v_mov_b64_e32 v[100:101], 0
	v_mov_b64_e32 v[102:103], 0
	v_mov_b64_e32 v[104:105], 0
	v_mov_b64_e32 v[106:107], 0
	v_mov_b64_e32 v[108:109], 0
	v_mov_b64_e32 v[110:111], 0
	v_mov_b64_e32 v[112:113], 0
	v_mov_b64_e32 v[114:115], 0
	v_mov_b64_e32 v[116:117], 0
	v_mov_b64_e32 v[118:119], 0
	v_mov_b64_e32 v[120:121], 0
	v_mov_b64_e32 v[122:123], 0
	v_mov_b64_e32 v[124:125], 0
	v_mov_b64_e32 v[126:127], 0
	v_mov_b64_e32 v[128:129], 0
	v_mov_b64_e32 v[130:131], 0
	v_mov_b64_e32 v[132:133], 0
	v_mov_b64_e32 v[134:135], 0
	v_mov_b64_e32 v[136:137], 0
	v_mov_b64_e32 v[138:139], 0
	v_mov_b64_e32 v[140:141], 0
	v_mov_b64_e32 v[142:143], 0
	v_mov_b64_e32 v[144:145], 0
	v_mov_b64_e32 v[146:147], 0
	v_mov_b64_e32 v[148:149], 0
	v_mov_b64_e32 v[150:151], 0
	v_mov_b64_e32 v[152:153], 0
	v_mov_b64_e32 v[154:155], 0
	v_mov_b64_e32 v[156:157], 0
	v_mov_b64_e32 v[158:159], 0
	v_mov_b64_e32 v[160:161], 0
	v_mov_b64_e32 v[162:163], 0
	v_mov_b64_e32 v[164:165], 0
	v_mov_b64_e32 v[166:167], 0
	v_mov_b64_e32 v[168:169], 0
	v_mov_b64_e32 v[170:171], 0
	v_mov_b64_e32 v[172:173], 0
	v_mov_b64_e32 v[174:175], 0
	v_mov_b64_e32 v[176:177], 0
	v_mov_b64_e32 v[178:179], 0
	v_mov_b64_e32 v[180:181], 0
	v_mov_b64_e32 v[182:183], 0
	v_mov_b64_e32 v[184:185], 0
	v_mov_b64_e32 v[186:187], 0
	v_mov_b64_e32 v[188:189], 0
	v_mov_b64_e32 v[190:191], 0
	s_branch .LBB0_3915

.LBB0_3978:
	s_ashr_i32 s21, s20, 31
	s_lshl_b64 s[24:25], s[20:21], 18
	s_add_u32 s24, s45, s24
	s_addc_u32 s25, s46, s25
	s_ashr_i32 s23, s22, 31
	s_lshl_b64 s[26:27], s[22:23], 18
	s_add_u32 s26, s43, s26
	s_addc_u32 s27, s44, s27
	s_and_b64 s[34:35], s[6:7], exec
	v_mov_b32_e32 v32, 0
	s_cselect_b32 s21, s27, s29
	s_cselect_b32 s23, s26, s28
	s_mov_b32 s33, -2
	s_mov_b64 s[38:39], 0
	v_mov_b32_e32 v33, 0
	v_mov_b64_e32 v[34:35], 0
	v_mov_b64_e32 v[36:37], 0
	v_mov_b64_e32 v[38:39], 0
	v_mov_b64_e32 v[40:41], 0
	v_mov_b64_e32 v[42:43], 0
	v_mov_b64_e32 v[44:45], 0
	v_mov_b64_e32 v[46:47], 0
	v_mov_b64_e32 v[48:49], 0
	v_mov_b64_e32 v[50:51], 0
	v_mov_b64_e32 v[52:53], 0
	v_mov_b64_e32 v[54:55], 0
	v_mov_b64_e32 v[56:57], 0
	v_mov_b64_e32 v[58:59], 0
	v_mov_b64_e32 v[60:61], 0
	v_mov_b64_e32 v[62:63], 0
	v_mov_b64_e32 v[64:65], 0
	v_mov_b64_e32 v[66:67], 0
	v_mov_b64_e32 v[68:69], 0
	v_mov_b64_e32 v[70:71], 0
	v_mov_b64_e32 v[72:73], 0
	v_mov_b64_e32 v[74:75], 0
	v_mov_b64_e32 v[76:77], 0
	v_mov_b64_e32 v[78:79], 0
	v_mov_b64_e32 v[80:81], 0
	v_mov_b64_e32 v[82:83], 0
	v_mov_b64_e32 v[84:85], 0
	v_mov_b64_e32 v[86:87], 0
	v_mov_b64_e32 v[88:89], 0
	v_mov_b64_e32 v[90:91], 0
	v_mov_b64_e32 v[92:93], 0
	v_mov_b64_e32 v[94:95], 0
	v_mov_b64_e32 v[96:97], 0
	v_mov_b64_e32 v[98:99], 0
	v_mov_b64_e32 v[100:101], 0
	v_mov_b64_e32 v[102:103], 0
	v_mov_b64_e32 v[104:105], 0
	v_mov_b64_e32 v[106:107], 0
	v_mov_b64_e32 v[108:109], 0
	v_mov_b64_e32 v[110:111], 0
	v_mov_b64_e32 v[112:113], 0
	v_mov_b64_e32 v[114:115], 0
	v_mov_b64_e32 v[116:117], 0
	v_mov_b64_e32 v[118:119], 0
	v_mov_b64_e32 v[120:121], 0
	v_mov_b64_e32 v[122:123], 0
	v_mov_b64_e32 v[124:125], 0
	v_mov_b64_e32 v[126:127], 0
	v_mov_b64_e32 v[128:129], 0
	v_mov_b64_e32 v[130:131], 0
	v_mov_b64_e32 v[132:133], 0
	v_mov_b64_e32 v[134:135], 0
	v_mov_b64_e32 v[136:137], 0
	v_mov_b64_e32 v[138:139], 0
	v_mov_b64_e32 v[140:141], 0
	v_mov_b64_e32 v[142:143], 0
	v_mov_b64_e32 v[144:145], 0
	v_mov_b64_e32 v[146:147], 0
	v_mov_b64_e32 v[148:149], 0
	v_mov_b64_e32 v[150:151], 0
	v_mov_b64_e32 v[152:153], 0
	v_mov_b64_e32 v[154:155], 0
	v_mov_b64_e32 v[156:157], 0
	v_mov_b64_e32 v[158:159], 0
.LBB0_3979:
	s_add_u32 s34, s38, 0x100
	ds_read_b128 v[0:3], v174
	ds_read_b128 v[4:7], v175
	ds_read_b128 v[8:11], v182
	ds_read_b128 v[12:15], v183
	s_addc_u32 s35, s39, 0
	s_and_b32 s69, s34, 0x300
	s_add_u32 s68, s28, s69
	s_addc_u32 s70, s29, 0
	s_cmp_eq_u32 s33, 4
	s_cselect_b64 s[40:41], -1, 0
	s_and_b64 s[36:37], s[40:41], exec
	s_cselect_b32 s37, s21, s70
	s_cselect_b32 s36, s23, s68
	s_cselect_b32 s68, 0, 0
	s_cselect_b32 s69, 0, s69
	s_add_u32 s38, s30, s38
	s_addc_u32 s39, s31, s39
	s_add_u32 s38, s38, 0x20080
	s_addc_u32 s39, s39, 0
	ds_read_b128 v[194:197], v190
	ds_read_b128 v[210:213], v190 offset:2048
	ds_read_b128 v[198:201], v191
	ds_read_b128 v[214:217], v191 offset:2048
	ds_read_b128 v[218:221], v190 offset:4096
	ds_read_b128 v[226:229], v190 offset:6144
	ds_read_b128 v[222:225], v191 offset:4096
	ds_read_b128 v[230:233], v191 offset:6144
	s_add_i32 m0, s1, 0xc000
	s_nop 0
	global_load_lds_dwordx4 v166, s[38:39]
	s_add_i32 m0, s1, 0xe000
	s_nop 0
	global_load_lds_dwordx4 v162, s[38:39]
	s_waitcnt lgkmcnt(8)
	s_barrier
	s_waitcnt lgkmcnt(0)
	s_setprio 1
	s_waitcnt lgkmcnt(0)
	v_mfma_scale_f32_16x16x128_f8f6f4 v[156:159], v[0:7], v[194:201], v[156:159], v173, v173 op_sel_hi:[0,0,0]
	v_mfma_scale_f32_16x16x128_f8f6f4 v[152:155], v[8:15], v[194:201], v[152:155], v173, v173 op_sel_hi:[0,0,0]
	v_mfma_scale_f32_16x16x128_f8f6f4 v[140:143], v[0:7], v[210:217], v[140:143], v173, v173 op_sel_hi:[0,0,0]
	v_mfma_scale_f32_16x16x128_f8f6f4 v[136:139], v[8:15], v[210:217], v[136:139], v173, v173 op_sel_hi:[0,0,0]
	v_mfma_scale_f32_16x16x128_f8f6f4 v[124:127], v[0:7], v[218:225], v[124:127], v173, v173 op_sel_hi:[0,0,0]
	v_mfma_scale_f32_16x16x128_f8f6f4 v[120:123], v[8:15], v[218:225], v[120:123], v173, v173 op_sel_hi:[0,0,0]
	v_mfma_scale_f32_16x16x128_f8f6f4 v[108:111], v[0:7], v[226:233], v[108:111], v173, v173 op_sel_hi:[0,0,0]
	v_mfma_scale_f32_16x16x128_f8f6f4 v[104:107], v[8:15], v[226:233], v[104:107], v173, v173 op_sel_hi:[0,0,0]
	s_setprio 0
	s_barrier
	s_mov_b64 s[38:39], s[36:37]
	s_mov_b32 m0, s3
	ds_read_b128 v[16:19], v176
	ds_read_b128 v[20:23], v177
	ds_read_b128 v[24:27], v184
	ds_read_b128 v[28:31], v185
	s_nop 0
	global_load_lds_dwordx4 v164, s[38:39]
	s_mov_b32 m0, s49
	s_nop 0
	global_load_lds_dwordx4 v160, s[38:39]
	s_barrier
	s_waitcnt lgkmcnt(0)
	s_setprio 1
	s_waitcnt lgkmcnt(0)
	v_mfma_scale_f32_16x16x128_f8f6f4 v[148:151], v[16:23], v[194:201], v[148:151], v173, v173 op_sel_hi:[0,0,0]
	v_mfma_scale_f32_16x16x128_f8f6f4 v[144:147], v[24:31], v[194:201], v[144:147], v173, v173 op_sel_hi:[0,0,0]
	v_mfma_scale_f32_16x16x128_f8f6f4 v[132:135], v[16:23], v[210:217], v[132:135], v173, v173 op_sel_hi:[0,0,0]
	v_mfma_scale_f32_16x16x128_f8f6f4 v[128:131], v[24:31], v[210:217], v[128:131], v173, v173 op_sel_hi:[0,0,0]
	v_mfma_scale_f32_16x16x128_f8f6f4 v[116:119], v[16:23], v[218:225], v[116:119], v173, v173 op_sel_hi:[0,0,0]
	v_mfma_scale_f32_16x16x128_f8f6f4 v[112:115], v[24:31], v[218:225], v[112:115], v173, v173 op_sel_hi:[0,0,0]
	v_mfma_scale_f32_16x16x128_f8f6f4 v[100:103], v[16:23], v[226:233], v[100:103], v173, v173 op_sel_hi:[0,0,0]
	v_mfma_scale_f32_16x16x128_f8f6f4 v[96:99], v[24:31], v[226:233], v[96:99], v173, v173 op_sel_hi:[0,0,0]
	s_setprio 0
	s_and_b64 s[38:39], s[6:7], s[40:41]
	s_and_b64 s[38:39], s[38:39], exec
	s_cselect_b32 s38, s24, s30
	s_cselect_b32 s39, s25, s31
	s_add_u32 s38, s38, s69
	s_addc_u32 s39, s39, s68
	s_mov_b64 s[40:41], s[38:39]
	s_mov_b32 m0, s1
	s_barrier
	ds_read_b128 v[194:197], v190 offset:16384
	ds_read_b128 v[210:213], v190 offset:18432
	ds_read_b128 v[198:201], v191 offset:16384
	ds_read_b128 v[214:217], v191 offset:18432
	ds_read_b128 v[218:221], v190 offset:20480
	ds_read_b128 v[226:229], v190 offset:22528
	ds_read_b128 v[222:225], v191 offset:20480
	ds_read_b128 v[230:233], v191 offset:22528
	s_nop 0
	global_load_lds_dwordx4 v166, s[40:41]
	s_mov_b32 m0, s50
	s_nop 0
	global_load_lds_dwordx4 v162, s[40:41]
	s_barrier
	s_waitcnt lgkmcnt(0)
	s_setprio 1
	s_waitcnt lgkmcnt(0)
	v_mfma_scale_f32_16x16x128_f8f6f4 v[92:95], v[0:7], v[194:201], v[92:95], v173, v173 op_sel_hi:[0,0,0]
	v_mfma_scale_f32_16x16x128_f8f6f4 v[88:91], v[8:15], v[194:201], v[88:91], v173, v173 op_sel_hi:[0,0,0]
	v_mfma_scale_f32_16x16x128_f8f6f4 v[76:79], v[0:7], v[210:217], v[76:79], v173, v173 op_sel_hi:[0,0,0]
	v_mfma_scale_f32_16x16x128_f8f6f4 v[72:75], v[8:15], v[210:217], v[72:75], v173, v173 op_sel_hi:[0,0,0]
	v_mfma_scale_f32_16x16x128_f8f6f4 v[60:63], v[0:7], v[218:225], v[60:63], v173, v173 op_sel_hi:[0,0,0]
	v_mfma_scale_f32_16x16x128_f8f6f4 v[56:59], v[8:15], v[218:225], v[56:59], v173, v173 op_sel_hi:[0,0,0]
	v_mfma_scale_f32_16x16x128_f8f6f4 v[44:47], v[0:7], v[226:233], v[44:47], v173, v173 op_sel_hi:[0,0,0]
	v_mfma_scale_f32_16x16x128_f8f6f4 v[40:43], v[8:15], v[226:233], v[40:43], v173, v173 op_sel_hi:[0,0,0]
	s_setprio 0
	s_barrier
	s_add_u32 s40, s36, 0x20000
	s_addc_u32 s41, s37, 0
	s_mov_b32 m0, s51
	s_nop 0
	global_load_lds_dwordx4 v164, s[40:41]
	s_mov_b32 m0, s52
	s_nop 0
	global_load_lds_dwordx4 v160, s[40:41]
	s_waitcnt vmcnt(6)
	s_barrier
	s_setprio 1
	v_mfma_scale_f32_16x16x128_f8f6f4 v[84:87], v[16:23], v[194:201], v[84:87], v173, v173 op_sel_hi:[0,0,0]
	v_mfma_scale_f32_16x16x128_f8f6f4 v[80:83], v[24:31], v[194:201], v[80:83], v173, v173 op_sel_hi:[0,0,0]
	v_mfma_scale_f32_16x16x128_f8f6f4 v[68:71], v[16:23], v[210:217], v[68:71], v173, v173 op_sel_hi:[0,0,0]
	v_mfma_scale_f32_16x16x128_f8f6f4 v[64:67], v[24:31], v[210:217], v[64:67], v173, v173 op_sel_hi:[0,0,0]
	v_mfma_scale_f32_16x16x128_f8f6f4 v[52:55], v[16:23], v[218:225], v[52:55], v173, v173 op_sel_hi:[0,0,0]
	v_mfma_scale_f32_16x16x128_f8f6f4 v[48:51], v[24:31], v[218:225], v[48:51], v173, v173 op_sel_hi:[0,0,0]
	v_mfma_scale_f32_16x16x128_f8f6f4 v[36:39], v[16:23], v[226:233], v[36:39], v173, v173 op_sel_hi:[0,0,0]
	v_mfma_scale_f32_16x16x128_f8f6f4 v[32:35], v[24:31], v[226:233], v[32:35], v173, v173 op_sel_hi:[0,0,0]
	s_setprio 0
	s_barrier
	ds_read_b128 v[0:3], v178
	ds_read_b128 v[4:7], v179
	ds_read_b128 v[8:11], v186
	ds_read_b128 v[12:15], v187
	s_add_u32 s40, s38, 0x20000
	s_addc_u32 s41, s39, 0
	s_mov_b32 m0, s53
	ds_read_b128 v[16:19], v190 offset:32768
	ds_read_b128 v[24:27], v190 offset:34816
	ds_read_b128 v[20:23], v191 offset:32768
	ds_read_b128 v[28:31], v191 offset:34816
	ds_read_b128 v[194:197], v190 offset:36864
	ds_read_b128 v[210:213], v190 offset:38912
	ds_read_b128 v[198:201], v191 offset:36864
	ds_read_b128 v[214:217], v191 offset:38912
	s_nop 0
	global_load_lds_dwordx4 v166, s[40:41]
	s_mov_b32 m0, s54
	s_nop 0
	global_load_lds_dwordx4 v162, s[40:41]
	s_waitcnt lgkmcnt(8)
	s_barrier
	s_waitcnt lgkmcnt(0)
	s_setprio 1
	s_waitcnt lgkmcnt(0)
	v_mfma_scale_f32_16x16x128_f8f6f4 v[156:159], v[0:7], v[16:23], v[156:159], v173, v173 op_sel_hi:[0,0,0]
	v_mfma_scale_f32_16x16x128_f8f6f4 v[152:155], v[8:15], v[16:23], v[152:155], v173, v173 op_sel_hi:[0,0,0]
	v_mfma_scale_f32_16x16x128_f8f6f4 v[140:143], v[0:7], v[24:31], v[140:143], v173, v173 op_sel_hi:[0,0,0]
	v_mfma_scale_f32_16x16x128_f8f6f4 v[136:139], v[8:15], v[24:31], v[136:139], v173, v173 op_sel_hi:[0,0,0]
	v_mfma_scale_f32_16x16x128_f8f6f4 v[124:127], v[0:7], v[194:201], v[124:127], v173, v173 op_sel_hi:[0,0,0]
	v_mfma_scale_f32_16x16x128_f8f6f4 v[120:123], v[8:15], v[194:201], v[120:123], v173, v173 op_sel_hi:[0,0,0]
	v_mfma_scale_f32_16x16x128_f8f6f4 v[108:111], v[0:7], v[210:217], v[108:111], v173, v173 op_sel_hi:[0,0,0]
	v_mfma_scale_f32_16x16x128_f8f6f4 v[104:107], v[8:15], v[210:217], v[104:107], v173, v173 op_sel_hi:[0,0,0]
	s_setprio 0
	s_barrier
	s_add_u32 s40, s36, 0x80
	s_addc_u32 s41, s37, 0
	s_mov_b32 m0, s56
	ds_read_b128 v[218:221], v180
	ds_read_b128 v[222:225], v181
	ds_read_b128 v[226:229], v188
	ds_read_b128 v[230:233], v189
	s_nop 0
	global_load_lds_dwordx4 v164, s[40:41]
	s_mov_b32 m0, s57
	s_nop 0
	global_load_lds_dwordx4 v160, s[40:41]
	s_barrier
	s_waitcnt lgkmcnt(0)
	s_setprio 1
	s_waitcnt lgkmcnt(0)
	v_mfma_scale_f32_16x16x128_f8f6f4 v[148:151], v[218:225], v[16:23], v[148:151], v173, v173 op_sel_hi:[0,0,0]
	v_mfma_scale_f32_16x16x128_f8f6f4 v[144:147], v[226:233], v[16:23], v[144:147], v173, v173 op_sel_hi:[0,0,0]
	v_mfma_scale_f32_16x16x128_f8f6f4 v[132:135], v[218:225], v[24:31], v[132:135], v173, v173 op_sel_hi:[0,0,0]
	v_mfma_scale_f32_16x16x128_f8f6f4 v[128:131], v[226:233], v[24:31], v[128:131], v173, v173 op_sel_hi:[0,0,0]
	v_mfma_scale_f32_16x16x128_f8f6f4 v[116:119], v[218:225], v[194:201], v[116:119], v173, v173 op_sel_hi:[0,0,0]
	v_mfma_scale_f32_16x16x128_f8f6f4 v[112:115], v[226:233], v[194:201], v[112:115], v173, v173 op_sel_hi:[0,0,0]
	v_mfma_scale_f32_16x16x128_f8f6f4 v[100:103], v[218:225], v[210:217], v[100:103], v173, v173 op_sel_hi:[0,0,0]
	v_mfma_scale_f32_16x16x128_f8f6f4 v[96:99], v[226:233], v[210:217], v[96:99], v173, v173 op_sel_hi:[0,0,0]
	s_setprio 0
	s_add_u32 s38, s38, 0x80
	s_addc_u32 s39, s39, 0
	s_mov_b32 m0, s58
	s_barrier
	ds_read_b128 v[16:19], v190 offset:49152
	ds_read_b128 v[24:27], v190 offset:51200
	ds_read_b128 v[20:23], v191 offset:49152
	ds_read_b128 v[28:31], v191 offset:51200
	ds_read_b128 v[194:197], v190 offset:53248
	ds_read_b128 v[210:213], v190 offset:55296
	ds_read_b128 v[198:201], v191 offset:53248
	ds_read_b128 v[214:217], v191 offset:55296
	s_nop 0
	global_load_lds_dwordx4 v166, s[38:39]
	s_mov_b32 m0, s59
	s_nop 0
	global_load_lds_dwordx4 v162, s[38:39]
	s_barrier
	s_waitcnt lgkmcnt(0)
	s_setprio 1
	s_waitcnt lgkmcnt(0)
	v_mfma_scale_f32_16x16x128_f8f6f4 v[92:95], v[0:7], v[16:23], v[92:95], v173, v173 op_sel_hi:[0,0,0]
	v_mfma_scale_f32_16x16x128_f8f6f4 v[88:91], v[8:15], v[16:23], v[88:91], v173, v173 op_sel_hi:[0,0,0]
	v_mfma_scale_f32_16x16x128_f8f6f4 v[76:79], v[0:7], v[24:31], v[76:79], v173, v173 op_sel_hi:[0,0,0]
	v_mfma_scale_f32_16x16x128_f8f6f4 v[72:75], v[8:15], v[24:31], v[72:75], v173, v173 op_sel_hi:[0,0,0]
	v_mfma_scale_f32_16x16x128_f8f6f4 v[60:63], v[0:7], v[194:201], v[60:63], v173, v173 op_sel_hi:[0,0,0]
	v_mfma_scale_f32_16x16x128_f8f6f4 v[56:59], v[8:15], v[194:201], v[56:59], v173, v173 op_sel_hi:[0,0,0]
	v_mfma_scale_f32_16x16x128_f8f6f4 v[44:47], v[0:7], v[210:217], v[44:47], v173, v173 op_sel_hi:[0,0,0]
	v_mfma_scale_f32_16x16x128_f8f6f4 v[40:43], v[8:15], v[210:217], v[40:43], v173, v173 op_sel_hi:[0,0,0]
	s_setprio 0
	s_barrier
	s_add_u32 s36, s36, 0x20080
	s_addc_u32 s37, s37, 0
	s_mov_b32 m0, s60
	s_nop 0
	global_load_lds_dwordx4 v164, s[36:37]
	s_mov_b32 m0, s61
	s_nop 0
	global_load_lds_dwordx4 v160, s[36:37]
	s_waitcnt vmcnt(6)
	s_barrier
	s_setprio 1
	v_mfma_scale_f32_16x16x128_f8f6f4 v[84:87], v[218:225], v[16:23], v[84:87], v173, v173 op_sel_hi:[0,0,0]
	v_mfma_scale_f32_16x16x128_f8f6f4 v[80:83], v[226:233], v[16:23], v[80:83], v173, v173 op_sel_hi:[0,0,0]
	v_mfma_scale_f32_16x16x128_f8f6f4 v[68:71], v[218:225], v[24:31], v[68:71], v173, v173 op_sel_hi:[0,0,0]
	v_mfma_scale_f32_16x16x128_f8f6f4 v[64:67], v[226:233], v[24:31], v[64:67], v173, v173 op_sel_hi:[0,0,0]
	v_mfma_scale_f32_16x16x128_f8f6f4 v[52:55], v[218:225], v[194:201], v[52:55], v173, v173 op_sel_hi:[0,0,0]
	v_mfma_scale_f32_16x16x128_f8f6f4 v[48:51], v[226:233], v[194:201], v[48:51], v173, v173 op_sel_hi:[0,0,0]
	v_mfma_scale_f32_16x16x128_f8f6f4 v[36:39], v[218:225], v[210:217], v[36:39], v173, v173 op_sel_hi:[0,0,0]
	v_mfma_scale_f32_16x16x128_f8f6f4 v[32:35], v[226:233], v[210:217], v[32:35], v173, v173 op_sel_hi:[0,0,0]
	s_setprio 0
	s_add_i32 s33, s33, 2
	s_cmp_gt_u32 s33, 5
	s_mov_b64 s[38:39], s[34:35]
	s_barrier
	s_cbranch_scc0 .LBB0_3979
	v_mov_b32_e32 v2, v172
	s_nop 15
	s_nop 15
	v_mov_b32_e32 v8, 0
	v_ashrrev_i32_e32 v0, 2, v2
	v_and_b32_e32 v0, 0xffffffc0, v0
	v_lshl_add_u32 v0, s2, 8, v0
	v_and_or_b32 v6, v2, 15, v0
	v_ashrrev_i32_e32 v7, 31, v6
	v_lshl_add_u64 v[0:1], v[6:7], 2, s[10:11]
	global_load_dword v14, v[0:1], off
	global_load_dword v194, v[0:1], off offset:64
	global_load_dword v195, v[0:1], off offset:128
	global_load_dword v196, v[0:1], off offset:192
	global_load_dword v197, v[0:1], off offset:512
	global_load_dword v198, v[0:1], off offset:576
	global_load_dword v199, v[0:1], off offset:640
	global_load_dword v200, v[0:1], off offset:704
	s_ashr_i32 s2, s0, 31
	s_lshr_b32 s2, s2, 30
	s_add_i32 s2, s0, s2
	v_lshrrev_b32_e32 v2, 1, v2
	s_and_b32 s2, s2, 0xfffffc
	v_and_b32_e32 v2, 0x78, v2
	s_sub_i32 s0, s0, s2
	v_lshl_or_b32 v4, s0, 8, v2
	v_lshlrev_b64 v[2:3], 10, v[6:7]
	v_mov_b32_e32 v9, 0
	v_mov_b32_e32 v10, 0
	v_mov_b32_e32 v11, 0
	v_ashrrev_i32_e32 v5, 31, v4
	v_or_b32_e32 v12, 16, v6
	v_lshl_add_u64 v[2:3], s[12:13], 0, v[2:3]
	v_ashrrev_i32_e32 v13, 31, v12
	v_lshl_add_u64 v[2:3], v[2:3], 0, v[4:5]
	s_mov_b64 s[28:29], s[26:27]
	s_mov_b64 s[30:31], s[24:25]
	s_mov_b32 s0, s22
	s_mov_b32 s2, s20
	s_waitcnt vmcnt(0)
	v_mul_f32_e32 v7, 0x3d000000, v14
	v_mul_f32_e32 v14, 0x42000000, v7
	v_pk_mul_f32 v[18:19], v[156:157], v[14:15] op_sel_hi:[1,0]
	v_pk_mul_f32 v[22:23], v[152:153], v[14:15] op_sel_hi:[1,0]
	v_pk_mul_f32 v[16:17], v[158:159], v[14:15] op_sel_hi:[1,0]
	v_pk_mul_f32 v[20:21], v[154:155], v[14:15] op_sel_hi:[1,0]
	v_pk_mul_f32 v[24:25], v[150:151], v[14:15] op_sel_hi:[1,0]
	v_pk_mul_f32 v[26:27], v[148:149], v[14:15] op_sel_hi:[1,0]
	v_pk_mul_f32 v[28:29], v[146:147], v[14:15] op_sel_hi:[1,0]
	v_pk_mul_f32 v[14:15], v[144:145], v[14:15] op_sel_hi:[1,0]
	v_med3_f32 v7, v18, s63, v192
	v_med3_f32 v18, v22, s63, v192
	v_med3_f32 v19, v19, s63, v192
	v_med3_f32 v22, v23, s63, v192
	v_med3_f32 v23, v26, s63, v192
	v_med3_f32 v14, v14, s63, v192
	v_med3_f32 v26, v27, s63, v192
	v_med3_f32 v15, v15, s63, v192
	v_cvt_pk_fp8_f32 v8, v7, v19
	v_cvt_pk_fp8_f32 v9, v18, v22
	v_cvt_pk_fp8_f32 v10, v23, v26
	v_cvt_pk_fp8_f32 v11, v14, v15
	v_med3_f32 v16, v16, s63, v192
	v_med3_f32 v20, v20, s63, v192
	v_med3_f32 v17, v17, s63, v192
	v_med3_f32 v21, v21, s63, v192
	v_med3_f32 v24, v24, s63, v192
	v_med3_f32 v27, v28, s63, v192
	v_med3_f32 v25, v25, s63, v192
	v_med3_f32 v28, v29, s63, v192
	v_cvt_pk_fp8_f32 v8, v16, v17 op_sel:[0,0,1]
	v_cvt_pk_fp8_f32 v9, v20, v21 op_sel:[0,0,1]
	v_cvt_pk_fp8_f32 v10, v24, v25 op_sel:[0,0,1]
	v_cvt_pk_fp8_f32 v11, v27, v28 op_sel:[0,0,1]
	v_lshl_add_u64 v[14:15], v[12:13], 2, s[10:11]
	global_store_dwordx2 v[2:3], v[8:9], off
	global_store_dwordx2 v[2:3], v[10:11], off offset:128
	v_mov_b32_e32 v8, 0
	v_mov_b32_e32 v9, 0
	v_mov_b32_e32 v10, 0
	v_mov_b32_e32 v11, 0
	v_lshlrev_b64 v[12:13], 10, v[12:13]
	v_or_b32_e32 v14, 32, v6
	v_lshl_add_u64 v[12:13], s[12:13], 0, v[12:13]
	v_ashrrev_i32_e32 v15, 31, v14
	v_lshl_add_u64 v[12:13], v[12:13], 0, v[4:5]
	v_lshl_add_u64 v[16:17], v[14:15], 2, s[10:11]
	v_or_b32_e32 v6, 48, v6
	v_mul_f32_e32 v7, 0x3d000000, v194
	v_mul_f32_e32 v18, 0x42000000, v7
	v_pk_mul_f32 v[22:23], v[140:141], v[18:19] op_sel_hi:[1,0]
	v_pk_mul_f32 v[26:27], v[136:137], v[18:19] op_sel_hi:[1,0]
	v_pk_mul_f32 v[20:21], v[142:143], v[18:19] op_sel_hi:[1,0]
	v_pk_mul_f32 v[24:25], v[138:139], v[18:19] op_sel_hi:[1,0]
	v_pk_mul_f32 v[28:29], v[134:135], v[18:19] op_sel_hi:[1,0]
	v_pk_mul_f32 v[30:31], v[132:133], v[18:19] op_sel_hi:[1,0]
	v_pk_mul_f32 v[130:131], v[130:131], v[18:19] op_sel_hi:[1,0]
	v_pk_mul_f32 v[18:19], v[128:129], v[18:19] op_sel_hi:[1,0]
	v_med3_f32 v7, v22, s63, v192
	v_med3_f32 v22, v26, s63, v192
	v_med3_f32 v23, v23, s63, v192
	v_med3_f32 v26, v27, s63, v192
	v_med3_f32 v27, v30, s63, v192
	v_med3_f32 v18, v18, s63, v192
	v_med3_f32 v30, v31, s63, v192
	v_med3_f32 v19, v19, s63, v192
	v_cvt_pk_fp8_f32 v8, v7, v23
	v_cvt_pk_fp8_f32 v9, v22, v26
	v_cvt_pk_fp8_f32 v10, v27, v30
	v_cvt_pk_fp8_f32 v11, v18, v19
	v_med3_f32 v20, v20, s63, v192
	v_med3_f32 v24, v24, s63, v192
	v_med3_f32 v21, v21, s63, v192
	v_med3_f32 v25, v25, s63, v192
	v_med3_f32 v28, v28, s63, v192
	v_med3_f32 v31, v130, s63, v192
	v_med3_f32 v29, v29, s63, v192
	v_med3_f32 v128, v131, s63, v192
	v_cvt_pk_fp8_f32 v8, v20, v21 op_sel:[0,0,1]
	v_cvt_pk_fp8_f32 v9, v24, v25 op_sel:[0,0,1]
	v_cvt_pk_fp8_f32 v10, v28, v29 op_sel:[0,0,1]
	v_cvt_pk_fp8_f32 v11, v31, v128 op_sel:[0,0,1]
	global_store_dwordx2 v[12:13], v[8:9], off
	global_store_dwordx2 v[12:13], v[10:11], off offset:128
	v_mov_b32_e32 v8, 0
	v_mov_b32_e32 v9, 0
	v_mov_b32_e32 v10, 0
	v_mov_b32_e32 v11, 0
	v_lshlrev_b64 v[12:13], 10, v[14:15]
	v_lshl_add_u64 v[12:13], s[12:13], 0, v[12:13]
	v_ashrrev_i32_e32 v7, 31, v6
	v_lshl_add_u64 v[12:13], v[12:13], 0, v[4:5]
	v_lshl_add_u64 v[14:15], v[6:7], 2, s[10:11]
	v_lshlrev_b64 v[6:7], 10, v[6:7]
	v_lshl_add_u64 v[6:7], s[12:13], 0, v[6:7]
	v_lshl_add_u64 v[4:5], v[6:7], 0, v[4:5]
	v_mov_b32_e32 v6, 0
	v_mov_b32_e32 v7, 0
	v_mul_f32_e32 v16, 0x3d000000, v195
	v_mul_f32_e32 v16, 0x42000000, v16
	v_pk_mul_f32 v[20:21], v[124:125], v[16:17] op_sel_hi:[1,0]
	v_pk_mul_f32 v[24:25], v[120:121], v[16:17] op_sel_hi:[1,0]
	v_pk_mul_f32 v[18:19], v[126:127], v[16:17] op_sel_hi:[1,0]
	v_pk_mul_f32 v[22:23], v[122:123], v[16:17] op_sel_hi:[1,0]
	v_pk_mul_f32 v[26:27], v[118:119], v[16:17] op_sel_hi:[1,0]
	v_pk_mul_f32 v[28:29], v[116:117], v[16:17] op_sel_hi:[1,0]
	v_pk_mul_f32 v[30:31], v[114:115], v[16:17] op_sel_hi:[1,0]
	v_pk_mul_f32 v[16:17], v[112:113], v[16:17] op_sel_hi:[1,0]
	v_med3_f32 v20, v20, s63, v192
	v_med3_f32 v24, v24, s63, v192
	v_med3_f32 v21, v21, s63, v192
	v_med3_f32 v25, v25, s63, v192
	v_med3_f32 v28, v28, s63, v192
	v_med3_f32 v16, v16, s63, v192
	v_med3_f32 v29, v29, s63, v192
	v_med3_f32 v17, v17, s63, v192
	v_cvt_pk_fp8_f32 v8, v20, v21
	v_cvt_pk_fp8_f32 v9, v24, v25
	v_cvt_pk_fp8_f32 v10, v28, v29
	v_cvt_pk_fp8_f32 v11, v16, v17
	v_med3_f32 v18, v18, s63, v192
	v_med3_f32 v22, v22, s63, v192
	v_med3_f32 v19, v19, s63, v192
	v_med3_f32 v23, v23, s63, v192
	v_med3_f32 v26, v26, s63, v192
	v_med3_f32 v30, v30, s63, v192
	v_med3_f32 v27, v27, s63, v192
	v_med3_f32 v31, v31, s63, v192
	v_cvt_pk_fp8_f32 v8, v18, v19 op_sel:[0,0,1]
	v_cvt_pk_fp8_f32 v9, v22, v23 op_sel:[0,0,1]
	v_cvt_pk_fp8_f32 v10, v26, v27 op_sel:[0,0,1]
	v_cvt_pk_fp8_f32 v11, v30, v31 op_sel:[0,0,1]
	global_store_dwordx2 v[12:13], v[8:9], off
	global_store_dwordx2 v[12:13], v[10:11], off offset:128
	v_mov_b32_e32 v8, 0
	v_mov_b32_e32 v9, 0
	v_mov_b32_e32 v10, 0
	v_mov_b32_e32 v11, 0
	v_mul_f32_e32 v12, 0x3d000000, v196
	v_mul_f32_e32 v12, 0x42000000, v12
	v_pk_mul_f32 v[16:17], v[108:109], v[12:13] op_sel_hi:[1,0]
	v_pk_mul_f32 v[20:21], v[104:105], v[12:13] op_sel_hi:[1,0]
	v_pk_mul_f32 v[14:15], v[110:111], v[12:13] op_sel_hi:[1,0]
	v_pk_mul_f32 v[18:19], v[106:107], v[12:13] op_sel_hi:[1,0]
	v_pk_mul_f32 v[22:23], v[102:103], v[12:13] op_sel_hi:[1,0]
	v_pk_mul_f32 v[24:25], v[100:101], v[12:13] op_sel_hi:[1,0]
	v_pk_mul_f32 v[26:27], v[98:99], v[12:13] op_sel_hi:[1,0]
	v_pk_mul_f32 v[12:13], v[96:97], v[12:13] op_sel_hi:[1,0]
	v_med3_f32 v16, v16, s63, v192
	v_med3_f32 v20, v20, s63, v192
	v_med3_f32 v17, v17, s63, v192
	v_med3_f32 v21, v21, s63, v192
	v_med3_f32 v24, v24, s63, v192
	v_med3_f32 v12, v12, s63, v192
	v_med3_f32 v25, v25, s63, v192
	v_med3_f32 v13, v13, s63, v192
	v_cvt_pk_fp8_f32 v8, v16, v17
	v_cvt_pk_fp8_f32 v9, v20, v21
	v_cvt_pk_fp8_f32 v10, v24, v25
	v_cvt_pk_fp8_f32 v11, v12, v13
	v_med3_f32 v14, v14, s63, v192
	v_med3_f32 v18, v18, s63, v192
	v_med3_f32 v15, v15, s63, v192
	v_med3_f32 v19, v19, s63, v192
	v_med3_f32 v22, v22, s63, v192
	v_med3_f32 v26, v26, s63, v192
	v_med3_f32 v23, v23, s63, v192
	v_med3_f32 v27, v27, s63, v192
	v_cvt_pk_fp8_f32 v8, v14, v15 op_sel:[0,0,1]
	v_cvt_pk_fp8_f32 v9, v18, v19 op_sel:[0,0,1]
	v_cvt_pk_fp8_f32 v10, v22, v23 op_sel:[0,0,1]
	v_cvt_pk_fp8_f32 v11, v26, v27 op_sel:[0,0,1]
	global_store_dwordx2 v[4:5], v[8:9], off
	global_store_dwordx2 v[4:5], v[10:11], off offset:128
	v_mov_b32_e32 v4, 0
	v_mov_b32_e32 v5, 0
	v_lshl_add_u64 v[8:9], v[2:3], 0, s[8:9]
	v_mul_f32_e32 v10, 0x3d000000, v197
	v_mul_f32_e32 v10, 0x42000000, v10
	v_pk_mul_f32 v[14:15], v[92:93], v[10:11] op_sel_hi:[1,0]
	v_pk_mul_f32 v[18:19], v[88:89], v[10:11] op_sel_hi:[1,0]
	v_pk_mul_f32 v[12:13], v[94:95], v[10:11] op_sel_hi:[1,0]
	v_pk_mul_f32 v[16:17], v[90:91], v[10:11] op_sel_hi:[1,0]
	v_pk_mul_f32 v[20:21], v[86:87], v[10:11] op_sel_hi:[1,0]
	v_pk_mul_f32 v[22:23], v[84:85], v[10:11] op_sel_hi:[1,0]
	v_pk_mul_f32 v[24:25], v[82:83], v[10:11] op_sel_hi:[1,0]
	v_pk_mul_f32 v[10:11], v[80:81], v[10:11] op_sel_hi:[1,0]
	v_med3_f32 v14, v14, s63, v192
	v_med3_f32 v18, v18, s63, v192
	v_med3_f32 v15, v15, s63, v192
	v_med3_f32 v19, v19, s63, v192
	v_med3_f32 v22, v22, s63, v192
	v_med3_f32 v10, v10, s63, v192
	v_med3_f32 v23, v23, s63, v192
	v_med3_f32 v11, v11, s63, v192
	v_cvt_pk_fp8_f32 v4, v14, v15
	v_cvt_pk_fp8_f32 v5, v18, v19
	v_cvt_pk_fp8_f32 v6, v22, v23
	v_cvt_pk_fp8_f32 v7, v10, v11
	v_med3_f32 v12, v12, s63, v192
	v_med3_f32 v16, v16, s63, v192
	v_med3_f32 v13, v13, s63, v192
	v_med3_f32 v17, v17, s63, v192
	v_med3_f32 v20, v20, s63, v192
	v_med3_f32 v24, v24, s63, v192
	v_med3_f32 v21, v21, s63, v192
	v_med3_f32 v25, v25, s63, v192
	v_cvt_pk_fp8_f32 v4, v12, v13 op_sel:[0,0,1]
	v_cvt_pk_fp8_f32 v5, v16, v17 op_sel:[0,0,1]
	v_cvt_pk_fp8_f32 v6, v20, v21 op_sel:[0,0,1]
	v_cvt_pk_fp8_f32 v7, v24, v25 op_sel:[0,0,1]
	v_add_co_u32_e32 v10, vcc, s64, v2
	s_nop 1
	v_addc_co_u32_e32 v11, vcc, 0, v3, vcc
	global_store_dwordx2 v[10:11], v[4:5], off
	global_store_dwordx2 v[8:9], v[6:7], off offset:128
	v_mov_b32_e32 v4, 0
	v_mov_b32_e32 v5, 0
	v_mov_b32_e32 v6, 0
	v_mov_b32_e32 v7, 0
	v_lshl_add_u64 v[8:9], v[2:3], 0, s[14:15]
	v_mul_f32_e32 v10, 0x3d000000, v198
	v_mul_f32_e32 v10, 0x42000000, v10
	v_pk_mul_f32 v[14:15], v[76:77], v[10:11] op_sel_hi:[1,0]
	v_pk_mul_f32 v[18:19], v[72:73], v[10:11] op_sel_hi:[1,0]
	v_pk_mul_f32 v[12:13], v[78:79], v[10:11] op_sel_hi:[1,0]
	v_pk_mul_f32 v[16:17], v[74:75], v[10:11] op_sel_hi:[1,0]
	v_pk_mul_f32 v[20:21], v[70:71], v[10:11] op_sel_hi:[1,0]
	v_pk_mul_f32 v[22:23], v[68:69], v[10:11] op_sel_hi:[1,0]
	v_pk_mul_f32 v[24:25], v[66:67], v[10:11] op_sel_hi:[1,0]
	v_pk_mul_f32 v[10:11], v[64:65], v[10:11] op_sel_hi:[1,0]
	v_med3_f32 v14, v14, s63, v192
	v_med3_f32 v18, v18, s63, v192
	v_med3_f32 v15, v15, s63, v192
	v_med3_f32 v19, v19, s63, v192
	v_med3_f32 v22, v22, s63, v192
	v_med3_f32 v10, v10, s63, v192
	v_med3_f32 v23, v23, s63, v192
	v_med3_f32 v11, v11, s63, v192
	v_cvt_pk_fp8_f32 v4, v14, v15
	v_cvt_pk_fp8_f32 v5, v18, v19
	v_cvt_pk_fp8_f32 v6, v22, v23
	v_cvt_pk_fp8_f32 v7, v10, v11
	v_med3_f32 v12, v12, s63, v192
	v_med3_f32 v16, v16, s63, v192
	v_med3_f32 v13, v13, s63, v192
	v_med3_f32 v17, v17, s63, v192
	v_med3_f32 v20, v20, s63, v192
	v_med3_f32 v24, v24, s63, v192
	v_med3_f32 v21, v21, s63, v192
	v_med3_f32 v25, v25, s63, v192
	v_cvt_pk_fp8_f32 v4, v12, v13 op_sel:[0,0,1]
	v_cvt_pk_fp8_f32 v5, v16, v17 op_sel:[0,0,1]
	v_cvt_pk_fp8_f32 v6, v20, v21 op_sel:[0,0,1]
	v_cvt_pk_fp8_f32 v7, v24, v25 op_sel:[0,0,1]
	v_add_co_u32_e32 v10, vcc, s65, v2
	s_nop 1
	v_addc_co_u32_e32 v11, vcc, 0, v3, vcc
	global_store_dwordx2 v[10:11], v[4:5], off
	global_store_dwordx2 v[8:9], v[6:7], off offset:128
	v_mov_b32_e32 v4, 0
	v_mov_b32_e32 v5, 0
	v_mov_b32_e32 v6, 0
	v_mov_b32_e32 v7, 0
	v_lshl_add_u64 v[8:9], v[2:3], 0, s[16:17]
	v_mul_f32_e32 v10, 0x3d000000, v199
	v_mul_f32_e32 v10, 0x42000000, v10
	v_pk_mul_f32 v[14:15], v[60:61], v[10:11] op_sel_hi:[1,0]
	v_pk_mul_f32 v[18:19], v[56:57], v[10:11] op_sel_hi:[1,0]
	v_pk_mul_f32 v[12:13], v[62:63], v[10:11] op_sel_hi:[1,0]
	v_pk_mul_f32 v[16:17], v[58:59], v[10:11] op_sel_hi:[1,0]
	v_pk_mul_f32 v[20:21], v[54:55], v[10:11] op_sel_hi:[1,0]
	v_pk_mul_f32 v[22:23], v[52:53], v[10:11] op_sel_hi:[1,0]
	v_pk_mul_f32 v[24:25], v[50:51], v[10:11] op_sel_hi:[1,0]
	v_pk_mul_f32 v[10:11], v[48:49], v[10:11] op_sel_hi:[1,0]
	v_med3_f32 v14, v14, s63, v192
	v_med3_f32 v18, v18, s63, v192
	v_med3_f32 v15, v15, s63, v192
	v_med3_f32 v19, v19, s63, v192
	v_med3_f32 v22, v22, s63, v192
	v_med3_f32 v10, v10, s63, v192
	v_med3_f32 v23, v23, s63, v192
	v_med3_f32 v11, v11, s63, v192
	v_cvt_pk_fp8_f32 v4, v14, v15
	v_cvt_pk_fp8_f32 v5, v18, v19
	v_cvt_pk_fp8_f32 v6, v22, v23
	v_cvt_pk_fp8_f32 v7, v10, v11
	v_med3_f32 v12, v12, s63, v192
	v_med3_f32 v16, v16, s63, v192
	v_med3_f32 v13, v13, s63, v192
	v_med3_f32 v17, v17, s63, v192
	v_med3_f32 v20, v20, s63, v192
	v_med3_f32 v24, v24, s63, v192
	v_med3_f32 v21, v21, s63, v192
	v_med3_f32 v25, v25, s63, v192
	v_cvt_pk_fp8_f32 v4, v12, v13 op_sel:[0,0,1]
	v_cvt_pk_fp8_f32 v5, v16, v17 op_sel:[0,0,1]
	v_cvt_pk_fp8_f32 v6, v20, v21 op_sel:[0,0,1]
	v_cvt_pk_fp8_f32 v7, v24, v25 op_sel:[0,0,1]
	v_add_co_u32_e32 v10, vcc, s66, v2
	s_nop 1
	v_addc_co_u32_e32 v11, vcc, 0, v3, vcc
	global_store_dwordx2 v[10:11], v[4:5], off
	global_store_dwordx2 v[8:9], v[6:7], off offset:128
	v_mov_b32_e32 v0, 0
	v_mov_b32_e32 v1, 0
	v_mov_b32_e32 v4, 0
	v_mov_b32_e32 v5, 0
	s_and_b64 vcc, exec, s[4:5]
	v_lshl_add_u64 v[6:7], v[2:3], 0, s[18:19]
	v_add_co_u32_e64 v2, s[4:5], s67, v2
	v_mul_f32_e32 v8, 0x3d000000, v200
	v_mul_f32_e32 v8, 0x42000000, v8
	v_pk_mul_f32 v[12:13], v[44:45], v[8:9] op_sel_hi:[1,0]
	v_pk_mul_f32 v[16:17], v[40:41], v[8:9] op_sel_hi:[1,0]
	v_pk_mul_f32 v[10:11], v[46:47], v[8:9] op_sel_hi:[1,0]
	v_pk_mul_f32 v[14:15], v[42:43], v[8:9] op_sel_hi:[1,0]
	v_pk_mul_f32 v[18:19], v[38:39], v[8:9] op_sel_hi:[1,0]
	v_pk_mul_f32 v[20:21], v[36:37], v[8:9] op_sel_hi:[1,0]
	v_pk_mul_f32 v[22:23], v[34:35], v[8:9] op_sel_hi:[1,0]
	v_pk_mul_f32 v[8:9], v[32:33], v[8:9] op_sel_hi:[1,0]
	v_med3_f32 v12, v12, s63, v192
	v_med3_f32 v16, v16, s63, v192
	v_med3_f32 v13, v13, s63, v192
	v_med3_f32 v17, v17, s63, v192
	v_med3_f32 v20, v20, s63, v192
	v_med3_f32 v8, v8, s63, v192
	v_med3_f32 v21, v21, s63, v192
	v_med3_f32 v9, v9, s63, v192
	v_cvt_pk_fp8_f32 v0, v12, v13
	v_cvt_pk_fp8_f32 v1, v16, v17
	v_cvt_pk_fp8_f32 v4, v20, v21
	v_cvt_pk_fp8_f32 v5, v8, v9
	v_med3_f32 v10, v10, s63, v192
	v_med3_f32 v14, v14, s63, v192
	v_med3_f32 v11, v11, s63, v192
	v_med3_f32 v15, v15, s63, v192
	v_med3_f32 v18, v18, s63, v192
	v_med3_f32 v22, v22, s63, v192
	v_med3_f32 v19, v19, s63, v192
	v_med3_f32 v23, v23, s63, v192
	v_cvt_pk_fp8_f32 v0, v10, v11 op_sel:[0,0,1]
	v_cvt_pk_fp8_f32 v1, v14, v15 op_sel:[0,0,1]
	v_cvt_pk_fp8_f32 v4, v18, v19 op_sel:[0,0,1]
	v_cvt_pk_fp8_f32 v5, v22, v23 op_sel:[0,0,1]
	v_addc_co_u32_e64 v3, s[4:5], 0, v3, s[4:5]
	global_store_dwordx2 v[2:3], v[0:1], off
	global_store_dwordx2 v[6:7], v[4:5], off offset:128
	s_cbranch_vccz .LBB0_3976
	s_waitcnt vmcnt(0)
	s_cmpk_gt_u32 s42, 0xff
	s_cbranch_scc1 .LBB0_3983
	s_barrier
